# expert row scales stored as (u scale, v scale) pairs; GEMM3 routing tail fetches both with one 8-byte gather per expert (16 gathers per row instead of 32, no separate v-scale wait rounds)
# speedup vs baseline: 1.0138x; 1.0138x over previous
; #define GAS __attribute__((address_space(1)))
; __device__ __forceinline__ void row_to_fp8_2(int lane, const float* xrow0, const float* xrow1, unsigned (&ow0)[4], unsigned (&ow1)[4], float& isc0, float& isc1) {
;     const GAS f32x4* xr0 = (const GAS f32x4*)xrow0 + lane; const GAS f32x4* xr1 = (const GAS f32x4*)xrow1 + lane;
;     f32x4 v0[4], v1[4];
; #pragma unroll
;     for (int j = 0; j < 4; ++j) { v0[j] = __builtin_nontemporal_load(xr0 + 64 * j); v1[j] = __builtin_nontemporal_load(xr1 + 64 * j); }
;     float m0 = 0.f, m1 = 0.f;
; #pragma unroll
;     for (int j = 0; j < 4; ++j) { m0 = fmaxf(m0, fmaxf(fmaxf(fabsf(v0[j].x), fabsf(v0[j].y)), fmaxf(fabsf(v0[j].z), fabsf(v0[j].w)))); m1 = fmaxf(m1, fmaxf(fmaxf(fabsf(v1[j].x), fabsf(v1[j].y)), fmaxf(fabsf(v1[j].z), fabsf(v1[j].w)))); }
; #pragma unroll
;     for (int o = 1; o < 64; o <<= 1) { m0 = fmaxf(m0, __shfl_xor(m0, o)); m1 = fmaxf(m1, __shfl_xor(m1, o)); }
;     int b0 = (int)((__float_as_uint(m0) >> 23) & 255u); b0 = b0 < 16 ? 16 : (b0 > 240 ? 240 : b0);
;     int b1 = (int)((__float_as_uint(m1) >> 23) & 255u); b1 = b1 < 16 ? 16 : (b1 > 240 ? 240 : b1);
;     const float s0 = __uint_as_float((unsigned)(261 - b0) << 23), s1 = __uint_as_float((unsigned)(261 - b1) << 23);
;     isc0 = __uint_as_float((unsigned)(b0 - 7) << 23); isc1 = __uint_as_float((unsigned)(b1 - 7) << 23);
; #pragma unroll
;     for (int j = 0; j < 4; ++j) { int p = __builtin_amdgcn_cvt_pk_fp8_f32(v0[j].x * s0, v0[j].y * s0, 0, false); p = __builtin_amdgcn_cvt_pk_fp8_f32(v0[j].z * s0, v0[j].w * s0, p, true); ow0[j] = (unsigned)p;
; __device__ __forceinline__ void tables_part(LAS unsigned char* lds, int wave, int lane, const float* pu, const float* pv, unsigned char* ws, int gw, int ngw, int wg, int nwg, int r0, int r1, int i0, int i1) {
;     for (int m = r0 + gw; m < r1; m += 2 * ngw) {
;         const int m1 = (m + ngw < r1) ? m + ngw : m;
;         float isc0, isc1; unsigned ow0[4], ow1[4];
;         row_to_fp8_2(lane, pu + (size_t)m * D, pu + (size_t)m1 * D, ow0, ow1, isc0, isc1);
; #pragma unroll
;         for (int j = 0; j < 4; ++j) { *((GAS unsigned*)(ws + WS_UT + (size_t)m * D + j * 256) + lane) = ow0[j]; *((GAS unsigned*)(ws + WS_UT + (size_t)m1 * D + j * 256) + lane) = ow1[j]; }
;         if (lane == 0) { ((float*)(ws + WS_ESC))[m] = isc0; ((float*)(ws + WS_ESC))[m1] = isc1; } }
.LBB0_176:
	s_cmpk_lt_i32 s3, 0x80
	s_cselect_b32 s99, 0x100, 0
	s_add_i32 s3, s3, s99
	v_xor_b32_e32 v0, 16, v172
	v_cmp_lt_i32_e32 vcc, v0, v177
	s_add_i32 s8, s3, 0xffffff80
	s_waitcnt lgkmcnt(0)
	v_xor_b32_e32 v1, 32, v172
	v_cndmask_b32_e32 v0, v172, v0, vcc
	v_lshlrev_b32_e32 v10, 2, v0
	v_mov_b32_e32 v0, v172
	s_load_dwordx2 s[14:15], s[12:13], 0x60
	s_lshl_b32 s4, s8, 3
	v_cmp_lt_i32_e32 vcc, v1, v177
	s_add_i32 s6, s4, s61
	s_cmpk_gt_i32 s6, 0x3fff
	v_cndmask_b32_e32 v1, v172, v1, vcc
	v_lshlrev_b32_e32 v11, 2, v1
	s_cbranch_scc1 .LBB0_181
	s_cmp_lg_u32 s99, 0
	s_cbranch_scc1 .LBB0_181
	v_ashrrev_i32_e32 v1, 31, v0
	s_add_u32 s9, s10, 0x19000000
	v_lshlrev_b64 v[6:7], 2, v[0:1]
	s_load_dwordx2 s[12:13], s[12:13], 0x58
	s_addc_u32 s22, s11, 0
	v_lshl_add_u64 v[4:5], s[10:11], 0, v[6:7]
	s_mov_b64 s[16:17], 0x15000000
	s_ashr_i32 s7, s6, 31
	v_lshl_add_u64 v[4:5], v[4:5], 0, s[16:17]
	s_lshl_b64 s[16:17], s[6:7], 3
	s_add_u32 s23, s16, 0x19000000
	s_addc_u32 s24, s17, 0
	s_lshl_b64 s[16:17], s[6:7], 10
	v_lshlrev_b64 v[8:9], 4, v[0:1]
	v_lshl_add_u64 v[6:7], s[16:17], 0, v[6:7]
	s_lshl_b64 s[16:17], s[6:7], 12
	s_waitcnt lgkmcnt(0)
	v_lshl_add_u64 v[2:3], s[12:13], 0, v[8:9]
	s_add_u32 s12, s12, s16
	s_addc_u32 s13, s13, s17
	v_lshl_add_u64 v[8:9], s[12:13], 0, v[8:9]
	s_mov_b64 s[12:13], 0x800
	v_cmp_eq_u32_e64 s[4:5], 0, v0
	v_lshl_add_u64 v[8:9], v[8:9], 0, s[12:13]
	v_mov_b32_e32 v1, 0xf0
	v_mov_b32_e32 v12, 0
	s_mov_b64 s[12:13], 0x200000
	s_mov_b64 s[16:17], 0x800000
	s_branch .LBB0_179
.LBB0_178:
	s_or_b64 exec, exec, s[20:21]
	s_add_u32 s23, s23, 0x4000
	s_addc_u32 s24, s24, 0
	s_add_i32 s7, s6, 0x800
	v_lshl_add_u64 v[6:7], v[6:7], 0, s[12:13]
	v_lshl_add_u64 v[8:9], v[8:9], 0, s[16:17]
	s_cmpk_gt_i32 s6, 0x37ff
	s_mov_b32 s6, s7
	s_cbranch_scc1 .LBB0_181
.LBB0_179:
	global_load_dwordx4 v[14:17], v[8:9], off offset:-2048 nt
	global_load_dwordx4 v[18:21], v[8:9], off offset:-1024 nt
	global_load_dwordx4 v[22:25], v[8:9], off nt
	global_load_dwordx4 v[26:29], v[8:9], off offset:1024 nt
	s_add_i32 s7, s6, 0x400
	s_cmpk_lt_i32 s6, 0x3c00
	s_cselect_b32 s18, s7, s6
	s_ashr_i32 s19, s18, 31
	s_lshl_b64 s[20:21], s[18:19], 12
	v_lshl_add_u64 v[46:47], v[2:3], 0, s[20:21]
	global_load_dwordx4 v[30:33], v[46:47], off nt
	global_load_dwordx4 v[34:37], v[46:47], off offset:1024 nt
	global_load_dwordx4 v[38:41], v[46:47], off offset:2048 nt
	global_load_dwordx4 v[42:45], v[46:47], off offset:3072 nt
	v_mov_b32_e32 v55, 0
	s_lshl_b64 s[20:21], s[18:19], 10
	s_waitcnt vmcnt(0)
	v_max_f32_e64 v13, |v17|, |v17|
	v_max_f32_e64 v46, |v16|, |v16|
	v_max_f32_e64 v47, |v21|, |v21|
	v_max_f32_e64 v48, |v20|, |v20|
	v_max_f32_e64 v49, |v25|, |v25|
	v_max_f32_e64 v50, |v24|, |v24|
	v_max_f32_e64 v51, |v29|, |v29|
	v_max_f32_e64 v52, |v28|, |v28|
	v_max_f32_e32 v13, v46, v13
	v_max_f32_e32 v46, v48, v47
	v_max_f32_e32 v47, v50, v49
	v_max_f32_e32 v48, v52, v51
	v_max3_f32 v13, |v14|, |v15|, v13
	v_max3_f32 v46, |v18|, |v19|, v46
	v_max3_f32 v47, |v22|, |v23|, v47
	v_max3_f32 v48, |v26|, |v27|, v48
	v_max3_f32 v13, v13, 0, v46
	v_max3_f32 v13, v13, v47, v48
	ds_bpermute_b32 v46, v173, v13
	v_max_f32_e64 v47, |v33|, |v33|
	v_max_f32_e64 v48, |v32|, |v32|
	v_max_f32_e64 v49, |v37|, |v37|
	v_max_f32_e64 v50, |v36|, |v36|
	v_max_f32_e64 v51, |v41|, |v41|
	v_max_f32_e64 v52, |v40|, |v40|
	v_max_f32_e64 v53, |v45|, |v45|
	v_max_f32_e64 v54, |v44|, |v44|
	v_max_f32_e32 v47, v48, v47
	v_max_f32_e32 v48, v50, v49
	v_max_f32_e32 v49, v52, v51
	v_max_f32_e32 v50, v54, v53
	v_max3_f32 v47, |v30|, |v31|, v47
	v_max3_f32 v48, |v34|, |v35|, v48
	v_max3_f32 v49, |v38|, |v39|, v49
	v_max3_f32 v50, |v42|, |v43|, v50
	v_max3_f32 v47, v47, 0, v48
	v_max3_f32 v47, v47, v49, v50
	s_waitcnt lgkmcnt(0)
	v_max_f32_e32 v46, v46, v46
	ds_bpermute_b32 v48, v173, v47
	v_max_f32_e32 v13, v13, v46
	ds_bpermute_b32 v46, v174, v13
	v_mov_b32_e32 v49, 0
	v_mov_b32_e32 v53, 0
	s_waitcnt lgkmcnt(1)
	v_max_f32_e32 v48, v48, v48
	v_max_f32_e32 v47, v47, v48
	s_waitcnt lgkmcnt(0)
	v_max_f32_e32 v46, v46, v46
	ds_bpermute_b32 v48, v174, v47
	v_max_f32_e32 v13, v13, v46
	ds_bpermute_b32 v46, v175, v13
	v_mov_b32_e32 v51, 0
	v_mov_b32_e32 v54, 0
	s_waitcnt lgkmcnt(1)
	v_max_f32_e32 v48, v48, v48
	v_max_f32_e32 v47, v47, v48
	s_waitcnt lgkmcnt(0)
	v_max_f32_e32 v46, v46, v46
	ds_bpermute_b32 v48, v175, v47
	v_max_f32_e32 v13, v13, v46
	ds_bpermute_b32 v46, v176, v13
	v_mov_b32_e32 v50, 0
	v_mov_b32_e32 v52, 0
	s_waitcnt lgkmcnt(1)
; #define GAS __attribute__((address_space(1)))
; __device__ __forceinline__ void row_to_fp8_2(int lane, const float* xrow0, const float* xrow1, unsigned (&ow0)[4], unsigned (&ow1)[4], float& isc0, float& isc1) {
;     ...
;     for (int j = 0; j < 4; ++j) { m0 = fmaxf(m0, fmaxf(fmaxf(fabsf(v0[j].x), fabsf(v0[j].y)), fmaxf(fabsf(v0[j].z), fabsf(v0[j].w)))); m1 = fmaxf(m1, fmaxf(fmaxf(fabsf(v1[j].x), fabsf(v1[j].y)), fmaxf(fabsf(v1[j].z), fabsf(v1[j].w)))); }
; #pragma unroll
;     for (int o = 1; o < 64; o <<= 1) { m0 = fmaxf(m0, __shfl_xor(m0, o)); m1 = fmaxf(m1, __shfl_xor(m1, o)); }
;     int b0 = (int)((__float_as_uint(m0) >> 23) & 255u); b0 = b0 < 16 ? 16 : (b0 > 240 ? 240 : b0);
;     int b1 = (int)((__float_as_uint(m1) >> 23) & 255u); b1 = b1 < 16 ? 16 : (b1 > 240 ? 240 : b1);
;     const float s0 = __uint_as_float((unsigned)(261 - b0) << 23), s1 = __uint_as_float((unsigned)(261 - b1) << 23);
;     isc0 = __uint_as_float((unsigned)(b0 - 7) << 23); isc1 = __uint_as_float((unsigned)(b1 - 7) << 23);
; #pragma unroll
;     for (int j = 0; j < 4; ++j) { int p = __builtin_amdgcn_cvt_pk_fp8_f32(v0[j].x * s0, v0[j].y * s0, 0, false); p = __builtin_amdgcn_cvt_pk_fp8_f32(v0[j].z * s0, v0[j].w * s0, p, true); ow0[j] = (unsigned)p;
;         int q = __builtin_amdgcn_cvt_pk_fp8_f32(v1[j].x * s1, v1[j].y * s1, 0, false); q = __builtin_amdgcn_cvt_pk_fp8_f32(v1[j].z * s1, v1[j].w * s1, q, true); ow1[j] = (unsigned)q; }
; }
; __device__ __forceinline__ void tables_part(LAS unsigned char* lds, int wave, int lane, const float* pu, const float* pv, unsigned char* ws, int gw, int ngw, int wg, int nwg, int r0, int r1, int i0, int i1) {
;     for (int m = r0 + gw; m < r1; m += 2 * ngw) {
;         const int m1 = (m + ngw < r1) ? m + ngw : m;
;         float isc0, isc1; unsigned ow0[4], ow1[4];
;         row_to_fp8_2(lane, pu + (size_t)m * D, pu + (size_t)m1 * D, ow0, ow1, isc0, isc1);
; #pragma unroll
;         for (int j = 0; j < 4; ++j) { *((GAS unsigned*)(ws + WS_UT + (size_t)m * D + j * 256) + lane) = ow0[j]; *((GAS unsigned*)(ws + WS_UT + (size_t)m1 * D + j * 256) + lane) = ow1[j]; }
;         if (lane == 0) { ((float*)(ws + WS_ESC))[m] = isc0; ((float*)(ws + WS_ESC))[m1] = isc1; } }
;     for (int it = i0 + wg; it < i1; it += nwg) { const int l = it >> 8;
	v_max_f32_e32 v48, v48, v48
	v_max_f32_e32 v47, v47, v48
	s_waitcnt lgkmcnt(0)
	v_max_f32_e32 v46, v46, v46
	ds_bpermute_b32 v48, v176, v47
	v_max_f32_e32 v13, v13, v46
	ds_bpermute_b32 v46, v10, v13
	s_waitcnt lgkmcnt(1)
	v_max_f32_e32 v48, v48, v48
	v_max_f32_e32 v47, v47, v48
	s_waitcnt lgkmcnt(0)
	v_max_f32_e32 v46, v46, v46
	ds_bpermute_b32 v48, v10, v47
	v_max_f32_e32 v13, v13, v46
	ds_bpermute_b32 v46, v11, v13
	s_waitcnt lgkmcnt(1)
	v_max_f32_e32 v48, v48, v48
	v_max_f32_e32 v47, v47, v48
	s_waitcnt lgkmcnt(0)
	v_max_f32_e32 v46, v46, v46
	v_max_f32_e32 v13, v13, v46
	ds_bpermute_b32 v46, v11, v47
	v_bfe_u32 v13, v13, 23, 8
	v_med3_u32 v13, v13, 16, v1
	v_lshlrev_b32_e32 v13, 23, v13
	v_sub_u32_e32 v48, 0x82800000, v13
	s_waitcnt lgkmcnt(0)
	v_max_f32_e32 v46, v46, v46
	v_mul_f32_e32 v14, v14, v48
	v_mul_f32_e32 v15, v15, v48
	v_mul_f32_e32 v22, v22, v48
	v_mul_f32_e32 v23, v23, v48
	v_max_f32_e32 v46, v47, v46
	v_cvt_pk_fp8_f32 v49, v14, v15
	v_cvt_pk_fp8_f32 v53, v22, v23
	v_bfe_u32 v14, v46, 23, 8
	v_med3_u32 v14, v14, 16, v1
	v_lshlrev_b32_e32 v14, 23, v14
	v_mul_f32_e32 v18, v18, v48
	v_mul_f32_e32 v19, v19, v48
	v_mul_f32_e32 v24, v24, v48
	v_mul_f32_e32 v25, v25, v48
	v_sub_u32_e32 v15, 0x82800000, v14
	v_cvt_pk_fp8_f32 v51, v18, v19
	v_cvt_pk_fp8_f32 v53, v24, v25 op_sel:[0,0,1]
	v_mul_f32_e32 v24, v38, v15
	v_mul_f32_e32 v25, v39, v15
	v_cvt_pk_fp8_f32 v54, v24, v25
	v_mul_f32_e32 v16, v16, v48
	v_mul_f32_e32 v17, v17, v48
	v_mul_f32_e32 v20, v20, v48
	v_mul_f32_e32 v21, v21, v48
	v_mul_f32_e32 v26, v26, v48
	v_mul_f32_e32 v27, v27, v48
	v_cvt_pk_fp8_f32 v49, v16, v17 op_sel:[0,0,1]
	v_mul_f32_e32 v16, v30, v15
	v_mul_f32_e32 v17, v31, v15
	v_cvt_pk_fp8_f32 v55, v26, v27
	v_cvt_pk_fp8_f32 v51, v20, v21 op_sel:[0,0,1]
	v_mul_f32_e32 v20, v34, v15
	v_mul_f32_e32 v21, v35, v15
	v_mul_f32_e32 v26, v40, v15
	v_cvt_pk_fp8_f32 v50, v16, v17
	v_mul_f32_e32 v16, v41, v15
	v_cvt_pk_fp8_f32 v52, v20, v21
	v_cvt_pk_fp8_f32 v54, v26, v16 op_sel:[0,0,1]
	v_mul_f32_e32 v16, v42, v15
	v_mul_f32_e32 v17, v43, v15
	v_mov_b32_e32 v20, 0
	v_cvt_pk_fp8_f32 v20, v16, v17
	v_mul_f32_e32 v18, v32, v15
	v_mul_f32_e32 v19, v33, v15
	v_mul_f32_e32 v22, v36, v15
	v_mul_f32_e32 v23, v37, v15
	v_cvt_pk_fp8_f32 v50, v18, v19 op_sel:[0,0,1]
	v_mul_f32_e32 v16, v44, v15
	v_mul_f32_e32 v15, v45, v15
	v_cvt_pk_fp8_f32 v20, v16, v15 op_sel:[0,0,1]
	v_lshl_add_u64 v[16:17], s[10:11], 0, v[6:7]
	v_cvt_pk_fp8_f32 v52, v22, v23 op_sel:[0,0,1]
	v_add_co_u32_e32 v16, vcc, 0x15000000, v16
	v_mul_f32_e32 v28, v28, v48
	v_mul_f32_e32 v29, v29, v48
	v_addc_co_u32_e32 v17, vcc, 0, v17, vcc
	v_lshl_add_u64 v[18:19], v[4:5], 0, s[20:21]
	v_cvt_pk_fp8_f32 v55, v28, v29 op_sel:[0,0,1]
	global_store_dword v[16:17], v49, off
	global_store_dword v[18:19], v50, off
	global_store_dword v[16:17], v51, off offset:256
	global_store_dword v[18:19], v52, off offset:256
	global_store_dword v[16:17], v53, off offset:512
	global_store_dword v[18:19], v54, off offset:512
	global_store_dword v[16:17], v55, off offset:768
	global_store_dword v[18:19], v20, off offset:768
	s_and_saveexec_b64 s[20:21], s[4:5]
	s_cbranch_execz .LBB0_178
	s_lshl_b64 s[18:19], s[18:19], 3
	s_add_u32 s18, s9, s18
	s_addc_u32 s19, s22, s19
	s_add_u32 s26, s10, s23
	v_add_u32_e32 v13, 0xfc800000, v13
	s_addc_u32 s27, s11, s24
	v_add_u32_e32 v14, 0xfc800000, v14
	global_store_dword v12, v13, s[26:27]
	global_store_dword v12, v14, s[18:19]
	s_branch .LBB0_178
.LBB0_181:
	s_cmpk_gt_u32 s8, 0xff
	s_cbranch_scc1 .LBB0_191
	s_add_u32 s22, s10, 0x17000000
	s_addc_u32 s23, s11, 0
	s_lshl_b32 s16, s61, 3
	s_mul_i32 s9, s61, 0x2040
	s_ashr_i32 s17, s16, 31
	s_add_i32 s9, s9, 0
	s_lshl_b64 s[18:19], s[16:17], 12
	v_or_b32_e32 v6, s56, v0
	v_and_b32_e32 v0, 63, v0
	s_waitcnt lgkmcnt(0)
	s_add_u32 s14, s14, s18
	v_cmp_eq_u32_e64 s[4:5], 0, v0
	v_lshl_add_u32 v7, v0, 2, s9
	v_lshlrev_b32_e32 v0, 4, v0
	v_mov_b32_e32 v1, 0
	s_addc_u32 s15, s15, s19
	s_lshl_b32 s12, s3, 6
	v_lshl_add_u64 v[2:3], s[14:15], 0, v[0:1]
	s_mov_b64 s[14:15], 0x1c00
	s_addk_i32 s12, 0xe000
	v_lshl_add_u64 v[2:3], v[2:3], 0, s[14:15]
	s_lshr_b32 s24, s12, 6
	s_lshl_b64 s[14:15], s[16:17], 3
	s_add_u32 s10, s10, s14
	s_mov_b32 s13, 0
	s_addc_u32 s11, s11, s15
	s_movk_i32 s6, 0x1000
	s_mov_b32 s9, s13
	s_add_u32 s25, s10, 0x19000008
	v_cmp_gt_i32_e64 s[6:7], s6, v6
	s_addc_u32 s26, s11, 0
	v_lshlrev_b32_e32 v0, 1, v6
	v_mov_b32_e32 v8, 0xf0
	s_mov_b64 s[10:11], 0x2000
	s_movk_i32 s27, 0xdff
	s_mov_b64 s[14:15], s[8:9]
	s_branch .LBB0_184

; #define GAS __attribute__((address_space(1)))
; #define LAS __attribute__((address_space(3)))
; __device__ __forceinline__ void row_to_fp8_2(int lane, const float* xrow0, const float* xrow1, unsigned (&ow0)[4], unsigned (&ow1)[4], float& isc0, float& isc1) {
;     const GAS f32x4* xr0 = (const GAS f32x4*)xrow0 + lane; const GAS f32x4* xr1 = (const GAS f32x4*)xrow1 + lane;
;     f32x4 v0[4], v1[4];
; #pragma unroll
;     for (int j = 0; j < 4; ++j) { v0[j] = __builtin_nontemporal_load(xr0 + 64 * j); v1[j] = __builtin_nontemporal_load(xr1 + 64 * j); }
;     float m0 = 0.f, m1 = 0.f;
; #pragma unroll
;     for (int j = 0; j < 4; ++j) { m0 = fmaxf(m0, fmaxf(fmaxf(fabsf(v0[j].x), fabsf(v0[j].y)), fmaxf(fabsf(v0[j].z), fabsf(v0[j].w)))); m1 = fmaxf(m1, fmaxf(fmaxf(fabsf(v1[j].x), fabsf(v1[j].y)), fmaxf(fabsf(v1[j].z), fabsf(v1[j].w)))); }
; #pragma unroll
;     for (int o = 1; o < 64; o <<= 1) { m0 = fmaxf(m0, __shfl_xor(m0, o)); m1 = fmaxf(m1, __shfl_xor(m1, o)); }
;     int b0 = (int)((__float_as_uint(m0) >> 23) & 255u); b0 = b0 < 16 ? 16 : (b0 > 240 ? 240 : b0);
;     int b1 = (int)((__float_as_uint(m1) >> 23) & 255u); b1 = b1 < 16 ? 16 : (b1 > 240 ? 240 : b1);
;     const float s0 = __uint_as_float((unsigned)(261 - b0) << 23), s1 = __uint_as_float((unsigned)(261 - b1) << 23);
;     isc0 = __uint_as_float((unsigned)(b0 - 7) << 23); isc1 = __uint_as_float((unsigned)(b1 - 7) << 23);
; #pragma unroll
;     for (int j = 0; j < 4; ++j) { int p = __builtin_amdgcn_cvt_pk_fp8_f32(v0[j].x * s0, v0[j].y * s0, 0, false); p = __builtin_amdgcn_cvt_pk_fp8_f32(v0[j].z * s0, v0[j].w * s0, p, true); ow0[j] = (unsigned)p;
; __device__ __forceinline__ void p0_vslice_item(LAS unsigned char* lds, int wave, int tid, const float* vt_l, unsigned char* VS_l, float* vsc_l, int item) {
;     const int lane = tid & 63, e0 = item * 64;
;     __syncthreads();
; #pragma unroll 1
;     for (int i = 0; i < 8; i += 2) { const int er = wave * 8 + i; float isc0, isc1; unsigned ow0[4], ow1[4];
;         row_to_fp8_2(lane, vt_l + (size_t)(e0 + er) * 1024, vt_l + (size_t)(e0 + er + 1) * 1024, ow0, ow1, isc0, isc1);
; #pragma unroll
;         for (int j = 0; j < 4; ++j) { *(LAS unsigned*)(lds + er * 1032 + j * 256 + lane * 4) = ow0[j]; *(LAS unsigned*)(lds + (er + 1) * 1032 + j * 256 + lane * 4) = ow1[j]; }
;         if (lane == 0) { vsc_l[e0 + er] = isc0; vsc_l[e0 + er + 1] = isc1; } }
.LBB0_184:
	s_lshl_b64 s[16:17], s[14:15], 18
	s_and_b32 s12, s24, 0xff
	s_and_b32 s9, s16, 0xfc000000
	s_lshl_b32 s16, s12, 18
	s_or_b32 s16, s9, s16
	v_lshl_add_u64 v[4:5], v[2:3], 0, s[16:17]
	s_lshr_b32 s16, s8, 8
	s_lshl_b32 s9, s12, 9
	s_lshl_b32 s12, s16, 14
	s_lshl_b64 s[18:19], s[12:13], 3
	s_or_b32 s9, s18, s9
	s_add_u32 s18, s25, s9
	s_addc_u32 s19, s26, s19
	s_mov_b32 s9, -2
	v_mov_b32_e32 v9, v7
	s_waitcnt vmcnt(0)
	s_barrier
	s_branch .LBB0_186
.LBB0_185:
	s_or_b64 exec, exec, s[20:21]
	s_add_i32 s9, s9, 2
	s_add_u32 s18, s18, 16
	s_addc_u32 s19, s19, 0
	v_add_u32_e32 v9, 0x810, v9
	s_cmp_gt_u32 s9, 5
	v_lshl_add_u64 v[4:5], v[4:5], 0, s[10:11]
	s_cbranch_scc1 .LBB0_188
.LBB0_186:
	global_load_dwordx4 v[14:17], v[4:5], off offset:-3072 nt
	global_load_dwordx4 v[18:21], v[4:5], off offset:-2048 nt
	global_load_dwordx4 v[22:25], v[4:5], off offset:-1024 nt
	global_load_dwordx4 v[26:29], v[4:5], off nt
	v_add_co_u32_e32 v12, vcc, 0xfffff000, v4
	s_waitcnt vmcnt(2)
	v_max_f32_e64 v46, |v21|, |v21|
	v_addc_co_u32_e32 v13, vcc, -1, v5, vcc
	global_load_dwordx4 v[30:33], v[12:13], off offset:-3072 nt
	global_load_dwordx4 v[34:37], v[12:13], off offset:-2048 nt
	global_load_dwordx4 v[38:41], v[12:13], off offset:-1024 nt
	global_load_dwordx4 v[42:45], v[4:5], off offset:-4096 nt
	v_max_f32_e64 v12, |v17|, |v17|
	v_max_f32_e64 v13, |v16|, |v16|
	v_max_f32_e64 v47, |v20|, |v20|
	s_waitcnt vmcnt(5)
	v_max_f32_e64 v48, |v25|, |v25|
	v_max_f32_e64 v49, |v24|, |v24|
	s_waitcnt vmcnt(4)
	v_max_f32_e64 v50, |v29|, |v29|
	v_max_f32_e64 v51, |v28|, |v28|
	v_max_f32_e32 v12, v13, v12
	v_max_f32_e32 v13, v47, v46
	v_max_f32_e32 v46, v49, v48
	v_max_f32_e32 v47, v51, v50
	v_max3_f32 v12, |v14|, |v15|, v12
	v_max3_f32 v13, |v18|, |v19|, v13
	v_max3_f32 v46, |v22|, |v23|, v46
	v_max3_f32 v47, |v26|, |v27|, v47
	v_max3_f32 v12, v12, 0, v13
	v_max3_f32 v12, v12, v46, v47
	ds_bpermute_b32 v47, v173, v12
	s_waitcnt lgkmcnt(0)
	v_max_f32_e32 v47, v47, v47
	v_max_f32_e32 v12, v12, v47
	ds_bpermute_b32 v47, v174, v12
	s_waitcnt lgkmcnt(0)
	v_max_f32_e32 v47, v47, v47
	v_max_f32_e32 v12, v12, v47
	ds_bpermute_b32 v47, v175, v12
	s_waitcnt lgkmcnt(0)
	v_max_f32_e32 v47, v47, v47
	v_max_f32_e32 v12, v12, v47
	ds_bpermute_b32 v47, v176, v12
	s_waitcnt lgkmcnt(0)
	v_max_f32_e32 v47, v47, v47
	v_max_f32_e32 v12, v12, v47
	ds_bpermute_b32 v47, v10, v12
	s_waitcnt lgkmcnt(0)
	v_max_f32_e32 v47, v47, v47
	v_max_f32_e32 v12, v12, v47
	ds_bpermute_b32 v47, v11, v12
	s_waitcnt lgkmcnt(0)
	v_max_f32_e32 v47, v47, v47
	v_max_f32_e32 v12, v12, v47
	v_bfe_u32 v12, v12, 23, 8
	v_med3_u32 v12, v12, 16, v8
	v_lshlrev_b32_e32 v12, 23, v12
	s_waitcnt vmcnt(3)
	v_max_f32_e64 v48, |v33|, |v33|
	v_max_f32_e64 v49, |v32|, |v32|
	s_waitcnt vmcnt(2)
	v_max_f32_e64 v50, |v37|, |v37|
	v_max_f32_e64 v51, |v36|, |v36|
	s_waitcnt vmcnt(1)
	v_max_f32_e64 v52, |v41|, |v41|
	v_max_f32_e64 v53, |v40|, |v40|
	s_waitcnt vmcnt(0)
	v_max_f32_e64 v54, |v45|, |v45|
	v_max_f32_e64 v55, |v44|, |v44|
	v_max_f32_e32 v48, v49, v48
	v_max_f32_e32 v49, v51, v50
	v_max_f32_e32 v13, v53, v52
	v_max_f32_e32 v50, v55, v54
	v_max3_f32 v48, |v30|, |v31|, v48
	v_max3_f32 v49, |v34|, |v35|, v49
	v_max3_f32 v13, |v38|, |v39|, v13
	v_max3_f32 v50, |v42|, |v43|, v50
	v_max3_f32 v46, v48, 0, v49
	v_max3_f32 v13, v46, v13, v50
	ds_bpermute_b32 v46, v173, v13
	v_mov_b32_e32 v49, 0
	v_mov_b32_e32 v48, 0
	v_mov_b32_e32 v53, 0
	v_mov_b32_e32 v50, 0
	s_waitcnt lgkmcnt(0)
	v_max_f32_e32 v46, v46, v46
	v_max_f32_e32 v13, v13, v46
	ds_bpermute_b32 v46, v174, v13
	v_mov_b32_e32 v51, 0
	v_mov_b32_e32 v52, 0
	v_mov_b32_e32 v54, 0
	s_waitcnt lgkmcnt(0)
	v_max_f32_e32 v46, v46, v46
	v_max_f32_e32 v13, v13, v46
	ds_bpermute_b32 v46, v175, v13
	s_waitcnt lgkmcnt(0)
	v_max_f32_e32 v46, v46, v46
	v_max_f32_e32 v13, v13, v46
	ds_bpermute_b32 v46, v176, v13
	s_waitcnt lgkmcnt(0)
	v_max_f32_e32 v46, v46, v46
	v_max_f32_e32 v13, v13, v46
	ds_bpermute_b32 v46, v10, v13
	s_waitcnt lgkmcnt(0)
	v_max_f32_e32 v46, v46, v46
	v_max_f32_e32 v13, v13, v46
	ds_bpermute_b32 v46, v11, v13
	s_waitcnt lgkmcnt(0)
	v_max_f32_e32 v46, v46, v46
	v_max_f32_e32 v13, v13, v46
	v_bfe_u32 v13, v13, 23, 8
	v_med3_u32 v13, v13, 16, v8
	v_sub_u32_e32 v46, 0x82800000, v12
	v_lshlrev_b32_e32 v13, 23, v13
	v_mul_f32_e32 v14, v14, v46
	v_mul_f32_e32 v15, v15, v46
	v_sub_u32_e32 v47, 0x82800000, v13
	v_cvt_pk_fp8_f32 v49, v14, v15
	v_mul_f32_e32 v14, v30, v47
	v_mul_f32_e32 v15, v31, v47
	v_cvt_pk_fp8_f32 v48, v14, v15
	v_mul_f32_e32 v22, v22, v46
	v_mul_f32_e32 v23, v23, v46
	v_mul_f32_e32 v18, v18, v46
	v_mul_f32_e32 v19, v19, v46
	v_cvt_pk_fp8_f32 v53, v22, v23
	v_mul_f32_e32 v22, v34, v47
	v_mul_f32_e32 v23, v35, v47
	v_mul_f32_e32 v16, v16, v46
	v_mul_f32_e32 v17, v17, v46
	v_cvt_pk_fp8_f32 v51, v18, v19
	v_mul_f32_e32 v18, v32, v47
	v_mul_f32_e32 v19, v33, v47
	v_mul_f32_e32 v30, v36, v47
	v_mul_f32_e32 v31, v37, v47
	v_mul_f32_e32 v32, v38, v47
	v_mul_f32_e32 v33, v39, v47
	v_mul_f32_e32 v36, v42, v47
	v_mul_f32_e32 v37, v43, v47
	v_cvt_pk_fp8_f32 v50, v22, v23
	v_cvt_pk_fp8_f32 v52, v32, v33
	v_cvt_pk_fp8_f32 v54, v36, v37
	v_cvt_pk_fp8_f32 v49, v16, v17 op_sel:[0,0,1]
	v_cvt_pk_fp8_f32 v48, v18, v19 op_sel:[0,0,1]
	v_mul_f32_e32 v16, v26, v46
	v_mul_f32_e32 v17, v27, v46
	v_mov_b32_e32 v18, 0
	v_cvt_pk_fp8_f32 v18, v16, v17
	v_mul_f32_e32 v20, v20, v46
	v_mul_f32_e32 v21, v21, v46
	v_mul_f32_e32 v34, v40, v47
	v_mul_f32_e32 v35, v41, v47
	v_cvt_pk_fp8_f32 v51, v20, v21 op_sel:[0,0,1]
	v_cvt_pk_fp8_f32 v50, v30, v31 op_sel:[0,0,1]
	v_mul_f32_e32 v14, v44, v47
	v_mul_f32_e32 v15, v45, v47
	v_mul_f32_e32 v24, v24, v46
	v_mul_f32_e32 v25, v25, v46
	v_cvt_pk_fp8_f32 v52, v34, v35 op_sel:[0,0,1]
	v_cvt_pk_fp8_f32 v54, v14, v15 op_sel:[0,0,1]
	v_mul_f32_e32 v14, v28, v46
	v_mul_f32_e32 v15, v29, v46
	v_cvt_pk_fp8_f32 v53, v24, v25 op_sel:[0,0,1]
	v_cvt_pk_fp8_f32 v18, v14, v15 op_sel:[0,0,1]
	v_add_u32_e32 v14, 8, v9
	ds_write2st64_b32 v9, v48, v50 offset1:1
	ds_write2st64_b32 v14, v49, v51 offset0:4 offset1:5
	ds_write2st64_b32 v9, v52, v54 offset0:2 offset1:3
	ds_write2st64_b32 v14, v53, v18 offset0:6 offset1:7
	s_and_saveexec_b64 s[20:21], s[4:5]
	s_cbranch_execz .LBB0_185
	v_add_u32_e32 v14, 0xfc800000, v13
	v_add_u32_e32 v15, 0xfc800000, v12
	global_store_dword v1, v14, s[18:19] offset:-4
	global_store_dword v1, v15, s[18:19] offset:4
	s_branch .LBB0_185

; template <class Epi, class Sched, bool ALIGN_EPI = false, bool SP2 = false>
; __device__ __forceinline__ void gemm_phase(int wave_id  , PG8_LAS unsigned char* lds, const Gemm g, const Sched& S, const Epi& E) {
;     ...
;     const int tid = tid_, wid = __builtin_amdgcn_readfirstlane(tid >> 6), lane = tid & 63, wr = wid >> 2, wc = wid & 3, fr = lane & 15, fq = lane >> 4;
;     const int K = g.K, nt = K / BK;
;     unsigned voffA[2], voffB[2];
; #pragma unroll
;     for (int i = 0; i < 2; ++i) { int R, C; stage_rc(tid * 16 + i * 8192, R, C); const int Rb = Epi::PERM ? ((R & ~31) + perm32(R & 31)) : R;
;         voffA[i] = (unsigned)(R * K + C) * 2u; voffB[i] = (unsigned)(Rb * K + C) * 2u; }
;     const size_t kstep = (size_t)(BK * 2);
;     const size_t hstep = (size_t)HALF * K * 2;
;     const size_t tstep = 2 * hstep;
;     const unsigned ldsw = (unsigned)wid * 1024u;
;     const int aoff = lds_byte(wr * 64 + fr, fq * 8), boff = lds_byte(wc * 32 + fr, fq * 8);
;     ...
;     Unit cur, nxt; int ui = 0;
;     if (!S.next(0, cur)) return;
;     f32x4 acc[2][2][4][2];
; #pragma unroll
;     for (int a = 0; a < 2; ++a)
; #pragma unroll
;         for (int b = 0; b < 2; ++b)
; #pragma unroll
;             for (int m = 0; m < 4; ++m)
; #pragma unroll
;                 for (int n = 0; n < 2; ++n) acc[a][b][m][n] = (f32x4){0.f, 0.f, 0.f, 0.f};
;     bf16x8 At[4][2], B0[2][2], B1[2][2];
;     const char* cA = (const char*)g.A + (size_t)cur.pm * tstep; const char* cB = (const char*)g.Bt + (size_t)cur.pn * tstep;
;     S.a_ready(cur);
;     if constexpr (SP2) {
;         PG8_STAGE(PG8_SB(0, 0), cB, voffB); PG8_STAGE(PG8_SB(0, 1), cB + hstep, voffB); PG8_STAGE(PG8_SA(0, 0), cA, voffA); PG8_STAGE(PG8_SA(0, 1), cA + hstep, voffA);
;         if (wr == 1) PG8_BAR;
; template <int K> __device__ __forceinline__ void run_phase(Frame& F, const XcdBarrier& bar, int lo, int hi, unsigned char* lds) {
;     ...
;             pg8::Gemm g{X1B, (bf16*)(ws + WS_WQ) + (size_t)l * NPQ * D, M, NPQ, D}; pg8::StaticOrder S; S.init(M, NPQ, G, bx, MK_WGM3);
;     ...
;             pg8::EpiRoute E{(int*)(ws + WS_EIDX), (float*)(ws + WS_EGATE), (float*)(ws + WS_EUS), (const float*)(ws + WS_ESC) + l * 16384, (const float*)(ws + WS_ESC) + 32768 + l * 16384};
;             pg8::OneUnit S0{S, 0}, S1{S, 1};
;             pg8::gemm_phase<pg8::EpiRoute, pg8::OneUnit, false, true>(F.wave, F.lds + RING_OFF, g, S0, E);
.LBB0_572:
	s_cmp_gt_i32 s40, 4
	s_cselect_b64 s[4:5], -1, 0
	s_cmp_lt_i32 s41, 5
	s_cselect_b64 s[6:7], -1, 0
	s_or_b64 s[4:5], s[4:5], s[6:7]
	s_and_b64 vcc, exec, s[4:5]
	s_cbranch_vccnz .LBB0_665
	s_mov_b64 s[4:5], s[0:1]
	s_waitcnt lgkmcnt(0)
	s_load_dwordx2 s[14:15], s[4:5], 0x80
	s_waitcnt vmcnt(0)
	v_mbcnt_lo_u32_b32 v0, -1, 0
	v_mbcnt_hi_u32_b32 v136, -1, v0
	v_lshl_or_b32 v137, s61, 6, v136
	s_mov_b32 s49, s60
	s_waitcnt lgkmcnt(0)
	s_add_u32 s3, s14, 0x6000000
	s_addc_u32 s46, s15, 0
	s_add_u32 s47, s14, 0x1000000
	s_addc_u32 s48, s15, 0
	s_add_u32 s12, s14, 0x14000000
	s_addc_u32 s13, s15, 0
	s_add_u32 s10, s14, 0x14800000
	s_addc_u32 s11, s15, 0
	s_add_u32 s8, s14, 0x19000000
	s_addc_u32 s9, s15, 0
	s_add_u32 s6, s14, 0x19000004
	s_mov_b32 s50, s2
	s_addc_u32 s7, s15, 0
	v_mov_b32_e32 v139, v137
	s_cmpk_gt_i32 s50, 0x1ff
	s_nop 0
	v_readfirstlane_b32 s53, v139
	s_cbranch_scc1 .LBB0_591
	v_lshlrev_b32_e32 v0, 4, v139
	v_add_u32_e32 v1, 0x2000, v0
	v_ashrrev_i32_e32 v2, 31, v1
	v_lshrrev_b32_e32 v2, 22, v2
	v_add_u32_e32 v2, v1, v2
	v_ashrrev_i32_e32 v8, 10, v2
	v_mul_i32_i24_e32 v3, 0x400, v8
	v_sub_u32_e32 v1, v1, v3
	v_lshrrev_b32_e32 v3, 4, v1
	v_bitop3_b32 v1, v3, v1, 32 bitop3:0x6c
	v_ashrrev_i32_e32 v3, 31, v1
	v_lshrrev_b32_e32 v3, 26, v3
	v_add_u32_e32 v3, v1, v3
	v_ashrrev_i32_e32 v10, 6, v3
	v_and_b32_e32 v3, 0xc0, v3
	v_sub_u32_e32 v1, v1, v3
	v_mov_b32_e32 v3, 1
	v_lshlrev_b32_e32 v2, 5, v8
	v_ashrrev_i16_sdwa v1, v3, sext(v1) dst_sel:DWORD dst_unused:UNUSED_PAD src0_sel:DWORD src1_sel:BYTE_0
	v_and_b32_e32 v2, 32, v2
	v_bfe_i32 v11, v1, 0, 16
	s_ashr_i32 s4, s50, 31
	v_add_u32_e32 v1, v2, v11
	v_lshlrev_b32_e32 v2, 3, v8
	s_lshr_b32 s4, s4, 29
	v_and_b32_e32 v2, 0x1ffff0, v2
	s_add_i32 s4, s50, s4
	v_add_lshl_u32 v2, v10, v2, 11
	s_ashr_i32 s5, s4, 3
	s_and_b32 s4, s4, -8
	s_ashr_i32 s51, s53, 6
	v_lshl_add_u32 v128, v1, 1, v2
	v_bfe_i32 v2, v139, 27, 1
	s_sub_i32 s4, s50, s4
	s_ashr_i32 s52, s53, 8
	s_lshl_b32 s42, s51, 10
	v_lshrrev_b32_e32 v2, 22, v2
	s_lshl_b32 s17, s4, 6
	v_add_u32_e32 v2, v0, v2
	s_mul_i32 s16, s4, 0x41
	s_cmp_lt_i32 s4, 0
	v_and_b32_e32 v2, 0xfffffc00, v2
	s_cselect_b32 s28, s16, s17
	v_sub_u32_e32 v0, v0, v2
	s_add_i32 s28, s28, s5
	v_lshrrev_b32_e32 v2, 4, v0
	s_ashr_i32 s4, s28, 31
	v_bitop3_b32 v0, v2, v0, 32 bitop3:0x6c
	s_lshr_b32 s4, s4, 27
	v_ashrrev_i32_e32 v2, 31, v0
	s_add_i32 s4, s28, s4
	v_ashrrev_i32_e32 v1, 31, v139
	v_lshrrev_b32_e32 v2, 26, v2
	s_ashr_i32 s43, s4, 5
	v_lshrrev_b32_e32 v1, 26, v1
	v_add_u32_e32 v2, v0, v2
	s_lshl_b32 s29, s43, 2
	v_add_u32_e32 v1, v139, v1
	v_ashrrev_i32_e32 v12, 6, v2
	v_and_b32_e32 v2, 0xc0, v2
	s_sub_i32 s5, 64, s29
	v_ashrrev_i32_e32 v9, 6, v1
	v_sub_u32_e32 v0, v0, v2
	s_min_u32 s16, s5, 4
	s_andn2_b32 s4, s4, 31
	v_lshlrev_b32_e32 v1, 5, v9
	v_ashrrev_i16_sdwa v0, v3, sext(v0) dst_sel:DWORD dst_unused:UNUSED_PAD src0_sel:DWORD src1_sel:BYTE_0
	s_sub_i32 s17, s28, s4
	v_cvt_f32_ubyte0_e32 v3, s16
	v_and_b32_e32 v1, 32, v1
	v_bfe_i32 v13, v0, 0, 16
	v_cvt_f32_i32_e32 v2, s17
	v_rcp_iflag_f32_e32 v4, v3
	v_add_u32_e32 v0, v1, v13
	v_lshlrev_b32_e32 v1, 3, v9
	v_and_b32_e32 v1, 0x1ffff0, v1
	v_add_lshl_u32 v1, v12, v1, 11
	v_lshl_add_u32 v130, v0, 1, v1
	v_mul_f32_e32 v0, v2, v4
	v_trunc_f32_e32 v0, v0
	v_fma_f32 v1, -v0, v3, v2
	v_cvt_i32_f32_e32 v0, v0
	s_ashr_i32 s4, s17, 30
	s_or_b32 s18, s4, 1
	v_cmp_ge_f32_e64 s[4:5], |v1|, v3
	s_and_b64 s[4:5], s[4:5], exec
	s_cselect_b32 s4, s18, 0
	v_readfirstlane_b32 s5, v0
	s_add_i32 s4, s5, s4
	s_mul_i32 s44, s4, s16
	s_sub_i32 s5, s17, s44
	s_sext_i32_i8 s5, s5
	s_add_i32 s18, s29, s5
	s_bfe_i64 s[16:17], s[4:5], 0x80000
	s_ashr_i32 s19, s18, 31
	s_lshl_b64 s[20:21], s[18:19], 19
	s_lshl_b64 s[26:27], s[16:17], 19
	s_add_u32 s4, s47, s26
	s_addc_u32 s5, s48, s27
	s_add_i32 s19, s42, 0
	s_add_i32 m0, s19, 0x10000
	v_mov_b32_e32 v131, 0
	global_load_lds_dwordx4 v130, s[4:5]
	s_add_i32 m0, s19, 0x12000
	s_add_u32 s22, s4, 0x40000
	global_load_lds_dwordx4 v128, s[4:5]
	s_addc_u32 s23, s5, 0
	s_add_i32 m0, s19, 0x14000
	v_mov_b32_e32 v129, v131
	global_load_lds_dwordx4 v130, s[22:23]
	s_add_i32 m0, s19, 0x16000
	v_lshl_add_u64 v[6:7], s[4:5], 0, v[130:131]
	global_load_lds_dwordx4 v128, s[22:23]
	s_add_u32 s22, s3, s20
	s_addc_u32 s23, s46, s21
	s_add_i32 s54, s19, 0x2000
	s_mov_b32 m0, s19
	s_add_u32 s20, s22, 0x40000
	global_load_lds_dwordx4 v130, s[22:23]
	s_mov_b32 m0, s54
	s_addc_u32 s21, s23, 0
	s_add_i32 s55, s19, 0x4000
	global_load_lds_dwordx4 v128, s[22:23]
	s_mov_b32 m0, s55
	s_add_i32 s56, s19, 0x6000
	global_load_lds_dwordx4 v130, s[20:21]
	s_mov_b32 m0, s56
	s_cmp_eq_u32 s52, 1
	global_load_lds_dwordx4 v128, s[20:21]
	v_lshl_add_u64 v[4:5], s[4:5], 0, v[128:129]
	v_lshl_add_u64 v[0:1], s[22:23], 0, v[130:131]
	s_cselect_b64 s[20:21], -1, 0
	s_cmp_lg_u32 s52, 1
	v_lshl_add_u64 v[2:3], s[22:23], 0, v[128:129]
	s_cbranch_scc1 .LBB0_576
	s_barrier

; #define PG8_LAS __attribute__((address_space(3)))
;     __device__ __forceinline__ void fused(f32x4 (&acc)[2][2][4][2], const Unit& u, int wr, int wc, int fr, int fq, PG8_LAS unsigned char* lds, int wid, int lane) const {
;     ...
;         if (half == 0) {
;             PG8_LAS int* idxl = (PG8_LAS int*)(lds + 65536) + row * 32;
;             float v0[16], v1[16];
; #pragma unroll
;             for (int q = 0; q < 16; ++q) { const unsigned b0 = __float_as_uint(top0[q]), b1 = __float_as_uint(top1[q]);
;                 v0[q] = __uint_as_float(b0 & ~127u); v1[q] = __uint_as_float(b1 & ~127u); idxl[q] = (int)(b0 & 127u); idxl[16 + q] = (int)(b1 & 127u); }
;             float best[16];
;             { float cv[16]; cv[0] = __uint_as_float((__float_as_uint(v0[0] + v1[0]) & ~255u) | 0u); cv[1] = __uint_as_float((__float_as_uint(v0[0] + v1[1]) & ~255u) | 1u); cv[2] = __uint_as_float((__float_as_uint(v0[0] + v1[2]) & ~255u) | 2u); cv[3] = __uint_as_float((__float_as_uint(v0[0] + v1[3]) & ~255u) | 3u); cv[4] = __uint_as_float((__float_as_uint(v0[0] + v1[4]) & ~255u) | 4u); cv[5] = __uint_as_float((__float_as_uint(v0[0] + v1[5]) & ~255u) | 5u); cv[6] = __uint_as_float((__float_as_uint(v0[0] + v1[6]) & ~255u) | 6u); cv[7] = __uint_as_float((__float_as_uint(v0[0] + v1[7]) & ~255u) | 7u); cv[8] = __uint_as_float((__float_as_uint(v0[0] + v1[8]) & ~255u) | 8u); cv[9] = __uint_as_float((__float_as_uint(v0[0] + v1[9]) & ~255u) | 9u); cv[10] = __uint_as_float((__float_as_uint(v0[0] + v1[10]) & ~255u) | 10u); cv[11] = __uint_as_float((__float_as_uint(v0[0] + v1[11]) & ~255u) | 11u); cv[12] = __uint_as_float((__float_as_uint(v0[0] + v1[12]) & ~255u) | 12u); cv[13] = __uint_as_float((__float_as_uint(v0[0] + v1[13]) & ~255u) | 13u); cv[14] = __uint_as_float((__float_as_uint(v0[0] + v1[14]) & ~255u) | 14u); cv[15] = __uint_as_float((__float_as_uint(v0[0] + v1[15]) & ~255u) | 15u); sort16_desc(cv);
; #pragma unroll
;               for (int q = 0; q < 16; ++q) best[q] = cv[q]; }
.LBB0_588:
	s_waitcnt lgkmcnt(0)
	s_barrier
	s_and_b64 vcc, exec, s[4:5]
	s_cbranch_vccnz .LBB0_590
	v_lshl_add_u32 v16, v128, 7, 0
	v_add_u32_e32 v16, 0x10000, v16
	v_and_b32_e32 v17, 0xffffff80, v12
	v_and_b32_e32 v18, 0xffffff80, v13
	v_and_b32_e32 v21, 0x7f, v77
	v_and_b32_e32 v20, 0x7f, v76
	v_and_b32_e32 v13, 0x7f, v13
	v_and_b32_e32 v12, 0x7f, v12
	v_and_b32_e32 v26, 0xffffff80, v14
	v_and_b32_e32 v28, 0xffffff80, v15
	v_and_b32_e32 v23, 0x7f, v79
	v_and_b32_e32 v22, 0x7f, v78
	v_and_b32_e32 v15, 0x7f, v15
	v_and_b32_e32 v14, 0x7f, v14
	ds_write_b128 v16, v[20:23]
	ds_write_b128 v16, v[12:15] offset:64
	v_and_b32_e32 v21, 0xffffff80, v8
	v_and_b32_e32 v23, 0xffffff80, v9
	v_and_b32_e32 v13, 0x7f, v73
	v_and_b32_e32 v12, 0x7f, v72
	v_and_b32_e32 v9, 0x7f, v9
	v_and_b32_e32 v8, 0x7f, v8
	v_and_b32_e32 v30, 0xffffff80, v10
	v_and_b32_e32 v32, 0xffffff80, v11
	v_and_b32_e32 v15, 0x7f, v75
	v_and_b32_e32 v14, 0x7f, v74
	v_and_b32_e32 v11, 0x7f, v11
	v_and_b32_e32 v10, 0x7f, v10
	v_and_b32_e32 v19, 0xffffff80, v76
	ds_write_b128 v16, v[12:15] offset:16
	ds_write_b128 v16, v[8:11] offset:80
	v_and_b32_e32 v13, 0xffffff80, v4
	v_and_b32_e32 v15, 0xffffff80, v5
	v_and_b32_e32 v9, 0x7f, v69
	v_and_b32_e32 v8, 0x7f, v68
	v_and_b32_e32 v5, 0x7f, v5
	v_and_b32_e32 v4, 0x7f, v4
	v_and_b32_e32 v34, 0xffffff80, v6
	v_and_b32_e32 v36, 0xffffff80, v7
	v_and_b32_e32 v11, 0x7f, v71
	v_and_b32_e32 v10, 0x7f, v70
	v_and_b32_e32 v7, 0x7f, v7
	v_and_b32_e32 v6, 0x7f, v6
	ds_write_b128 v16, v[8:11] offset:32
	ds_write_b128 v16, v[4:7] offset:96
	v_and_b32_e32 v5, 0x7f, v65
	v_and_b32_e32 v4, 0x7f, v64
	v_and_b32_e32 v41, 0xffffff80, v2
	v_and_b32_e32 v42, 0xffffff80, v3
	v_and_b32_e32 v7, 0x7f, v67
	v_and_b32_e32 v6, 0x7f, v66
	v_and_b32_e32 v11, 0x7f, v3
	v_and_b32_e32 v10, 0x7f, v2
	v_add_f32_e32 v2, v19, v17
	s_movk_i32 s4, 0xff00
	v_add_f32_e32 v3, v19, v18
	v_and_b32_e32 v24, 0xffffff80, v77
	ds_write_b128 v16, v[4:7] offset:48
	v_and_b32_e32 v2, 0xffffff00, v2
	v_and_or_b32 v3, v3, s4, 1
	v_add_f32_e32 v4, v19, v26
	v_add_f32_e32 v5, v19, v28
	v_and_b32_e32 v40, 0xffffff80, v1
	v_and_b32_e32 v9, 0x7f, v1
	v_and_b32_e32 v8, 0x7f, v0
	v_and_or_b32 v4, v4, s4, 2
	v_and_or_b32 v5, v5, s4, 3
	v_add_f32_e32 v48, v24, v17
	v_add_f32_e32 v49, v24, v18
	ds_write_b128 v16, v[8:11] offset:112
	v_add_f32_e32 v6, v19, v21
	v_add_f32_e32 v7, v19, v23
	v_add_f32_e32 v11, v19, v15
	v_add_f32_e32 v15, v19, v36
	v_add_f32_e32 v36, v19, v40
	v_max_f32_e32 v40, v2, v3
	v_min_f32_e32 v2, v2, v3
	v_max_f32_e32 v3, v5, v5
	v_and_or_b32 v48, v48, s4, 16
	v_and_or_b32 v49, v49, s4, 17
	v_add_f32_e32 v50, v24, v26
	v_add_f32_e32 v51, v24, v28
	v_and_or_b32 v6, v6, s4, 4
	v_and_or_b32 v7, v7, s4, 5
	v_add_f32_e32 v8, v19, v30
	v_add_f32_e32 v9, v19, v32
	v_max_f32_e32 v5, v4, v3
	v_min_f32_e32 v3, v4, v3
	v_and_or_b32 v50, v50, s4, 18
	v_and_or_b32 v51, v51, s4, 19
	v_and_or_b32 v8, v8, s4, 6
	v_and_or_b32 v9, v9, s4, 7
	v_max_f32_e32 v4, v40, v5
	v_min_f32_e32 v5, v40, v5
	v_max_f32_e32 v40, v2, v3
	v_add_f32_e32 v52, v24, v21
	v_add_f32_e32 v23, v24, v23
	v_add_f32_e32 v30, v24, v30
	v_add_f32_e32 v24, v24, v32
	v_max_f32_e32 v58, v48, v49
	v_min_f32_e32 v48, v48, v49
	v_max_f32_e32 v49, v51, v51
	v_min_f32_e32 v2, v2, v3
	v_max_f32_e32 v3, v40, v5
	v_min_f32_e32 v5, v40, v5
	v_max_f32_e32 v40, v6, v7
	v_min_f32_e32 v6, v6, v7
	v_max_f32_e32 v7, v9, v9
	v_and_or_b32 v52, v52, s4, 20
	v_and_or_b32 v23, v23, s4, 21
	v_and_or_b32 v30, v30, s4, 22
	v_and_or_b32 v24, v24, s4, 23
	v_max_f32_e32 v51, v50, v49
	v_min_f32_e32 v49, v50, v49
	v_max_f32_e32 v9, v8, v7
	v_min_f32_e32 v7, v8, v7
	v_max_f32_e32 v50, v58, v51
	v_min_f32_e32 v51, v58, v51
	v_max_f32_e32 v58, v48, v49
	v_max_f32_e32 v8, v40, v9
	v_min_f32_e32 v9, v40, v9
	v_max_f32_e32 v40, v6, v7
	v_min_f32_e32 v48, v48, v49
	v_max_f32_e32 v49, v58, v51
	v_min_f32_e32 v51, v58, v51
	v_max_f32_e32 v58, v52, v23
	v_min_f32_e32 v23, v52, v23
	v_max_f32_e32 v52, v30, v24
	v_min_f32_e32 v24, v30, v24
	v_min_f32_e32 v6, v6, v7
	v_max_f32_e32 v7, v40, v9
	v_min_f32_e32 v9, v40, v9
	v_max_f32_e32 v30, v58, v52
	v_min_f32_e32 v52, v58, v52
	v_max_f32_e32 v58, v23, v24
	v_max_f32_e32 v40, v4, v8
	v_min_f32_e32 v4, v4, v8
	v_max_f32_e32 v8, v5, v9
	v_min_f32_e32 v23, v23, v24
	v_max_f32_e32 v24, v58, v52
	v_min_f32_e32 v52, v58, v52
	v_and_b32_e32 v25, 0xffffff80, v78
	v_add_f32_e32 v10, v19, v13
	v_min_f32_e32 v5, v5, v9
	v_max_f32_e32 v9, v8, v4
	v_min_f32_e32 v4, v8, v4
	v_max_f32_e32 v8, v3, v7
	v_min_f32_e32 v3, v3, v7
	v_max_f32_e32 v7, v2, v6
	v_max_f32_e32 v58, v50, v30
	v_min_f32_e32 v30, v50, v30
	v_max_f32_e32 v50, v51, v52
	v_and_or_b32 v10, v10, s4, 8
	v_and_or_b32 v11, v11, s4, 9
	v_add_f32_e32 v13, v19, v34
	v_min_f32_e32 v2, v2, v6
	v_max_f32_e32 v6, v7, v3
	v_min_f32_e32 v3, v7, v3
	v_add_f32_e32 v32, v25, v17
	v_add_f32_e32 v53, v25, v18
	v_min_f32_e32 v51, v51, v52
	v_max_f32_e32 v52, v50, v30
	v_min_f32_e32 v30, v50, v30
	v_max_f32_e32 v50, v49, v24
	v_min_f32_e32 v24, v49, v24
	v_max_f32_e32 v49, v48, v23
	v_and_or_b32 v13, v13, s4, 10
	v_and_or_b32 v15, v15, s4, 11
	v_max_f32_e32 v7, v8, v9
	v_min_f32_e32 v8, v8, v9
	v_max_f32_e32 v9, v6, v4
	v_min_f32_e32 v4, v6, v4
	v_max_f32_e32 v6, v3, v5
	v_min_f32_e32 v3, v3, v5
	v_max_f32_e32 v5, v11, v11
	v_and_or_b32 v32, v32, s4, 32
	v_and_or_b32 v53, v53, s4, 33
	v_add_f32_e32 v54, v25, v26
	v_add_f32_e32 v55, v25, v28
	v_min_f32_e32 v23, v48, v23
	v_max_f32_e32 v48, v49, v24
	v_min_f32_e32 v24, v49, v24
	v_and_b32_e32 v27, 0xffffff80, v79
	v_and_b32_e32 v38, 0xffffff80, v0
	v_max_f32_e32 v11, v10, v5
	v_min_f32_e32 v5, v10, v5
	v_max_f32_e32 v10, v15, v15
;     __device__ __forceinline__ void fused(f32x4 (&acc)[2][2][4][2], const Unit& u, int wr, int wc, int fr, int fq, PG8_LAS unsigned char* lds, int wid, int lane) const {
;     ...
;             { float cv[16]; cv[0] = __uint_as_float((__float_as_uint(v0[0] + v1[0]) & ~255u) | 0u); cv[1] = __uint_as_float((__float_as_uint(v0[0] + v1[1]) & ~255u) | 1u); cv[2] = __uint_as_float((__float_as_uint(v0[0] + v1[2]) & ~255u) | 2u); cv[3] = __uint_as_float((__float_as_uint(v0[0] + v1[3]) & ~255u) | 3u); cv[4] = __uint_as_float((__float_as_uint(v0[0] + v1[4]) & ~255u) | 4u); cv[5] = __uint_as_float((__float_as_uint(v0[0] + v1[5]) & ~255u) | 5u); cv[6] = __uint_as_float((__float_as_uint(v0[0] + v1[6]) & ~255u) | 6u); cv[7] = __uint_as_float((__float_as_uint(v0[0] + v1[7]) & ~255u) | 7u); cv[8] = __uint_as_float((__float_as_uint(v0[0] + v1[8]) & ~255u) | 8u); cv[9] = __uint_as_float((__float_as_uint(v0[0] + v1[9]) & ~255u) | 9u); cv[10] = __uint_as_float((__float_as_uint(v0[0] + v1[10]) & ~255u) | 10u); cv[11] = __uint_as_float((__float_as_uint(v0[0] + v1[11]) & ~255u) | 11u); cv[12] = __uint_as_float((__float_as_uint(v0[0] + v1[12]) & ~255u) | 12u); cv[13] = __uint_as_float((__float_as_uint(v0[0] + v1[13]) & ~255u) | 13u); cv[14] = __uint_as_float((__float_as_uint(v0[0] + v1[14]) & ~255u) | 14u); cv[15] = __uint_as_float((__float_as_uint(v0[0] + v1[15]) & ~255u) | 15u); sort16_desc(cv);
; #pragma unroll
;               for (int q = 0; q < 16; ++q) best[q] = cv[q]; }
	v_and_or_b32 v54, v54, s4, 34
	v_and_or_b32 v55, v55, s4, 35
	v_max_f32_e32 v49, v50, v52
	v_min_f32_e32 v50, v50, v52
	v_max_f32_e32 v52, v48, v30
	v_min_f32_e32 v30, v48, v30
	v_max_f32_e32 v48, v24, v51
	v_min_f32_e32 v24, v24, v51
	v_max_f32_e32 v51, v53, v53
	v_add_f32_e32 v34, v19, v38
	v_max_f32_e32 v15, v13, v10
	v_min_f32_e32 v10, v13, v10
	v_add_f32_e32 v21, v25, v21
	v_add_f32_e32 v25, v27, v17
	v_max_f32_e32 v53, v32, v51
	v_min_f32_e32 v32, v32, v51
	v_max_f32_e32 v51, v55, v55
	v_and_or_b32 v34, v34, s4, 12
	v_and_or_b32 v36, v36, s4, 13
	v_add_f32_e32 v38, v19, v41
	v_add_f32_e32 v19, v19, v42
	v_max_f32_e32 v13, v11, v15
	v_min_f32_e32 v11, v11, v15
	v_max_f32_e32 v15, v5, v10
	v_and_or_b32 v21, v21, s4, 36
	v_and_or_b32 v25, v25, s4, 48
	v_add_f32_e32 v56, v27, v18
	v_add_f32_e32 v57, v27, v26
	v_max_f32_e32 v55, v54, v51
	v_min_f32_e32 v51, v54, v51
	v_and_or_b32 v38, v38, s4, 14
	v_and_or_b32 v19, v19, s4, 15
	v_min_f32_e32 v5, v5, v10
	v_max_f32_e32 v10, v15, v11
	v_min_f32_e32 v11, v15, v11
	v_max_f32_e32 v15, v36, v36
	v_and_or_b32 v56, v56, s4, 49
	v_and_or_b32 v57, v57, s4, 50
	v_max_f32_e32 v54, v53, v55
	v_min_f32_e32 v53, v53, v55
	v_max_f32_e32 v55, v32, v51
	v_max_f32_e32 v36, v34, v15
	v_min_f32_e32 v15, v34, v15
	v_max_f32_e32 v34, v38, v38
	v_min_f32_e32 v32, v32, v51
	v_max_f32_e32 v51, v55, v53
	v_min_f32_e32 v53, v55, v53
	v_max_f32_e32 v55, v21, v25
	v_min_f32_e32 v21, v21, v25
	v_max_f32_e32 v25, v57, v57
	v_max_f32_e32 v38, v34, v19
	v_min_f32_e32 v19, v34, v19
	v_max_f32_e32 v57, v56, v25
	v_min_f32_e32 v25, v56, v25
	v_max_f32_e32 v34, v36, v38
	v_min_f32_e32 v36, v36, v38
	v_max_f32_e32 v38, v15, v19
	v_max_f32_e32 v56, v55, v57
	v_min_f32_e32 v55, v55, v57
	v_max_f32_e32 v57, v21, v25
	v_min_f32_e32 v15, v15, v19
	v_max_f32_e32 v19, v38, v36
	v_min_f32_e32 v36, v38, v36
	v_min_f32_e32 v21, v21, v25
	v_max_f32_e32 v25, v57, v55
	v_min_f32_e32 v55, v57, v55
	v_max_f32_e32 v38, v13, v34
	v_min_f32_e32 v13, v13, v34
	v_max_f32_e32 v34, v11, v36
	v_max_f32_e32 v57, v54, v56
	v_min_f32_e32 v54, v54, v56
	v_max_f32_e32 v56, v53, v55
	v_min_f32_e32 v11, v11, v36
	v_max_f32_e32 v36, v34, v13
	v_min_f32_e32 v13, v34, v13
	v_max_f32_e32 v34, v10, v19
	v_min_f32_e32 v10, v10, v19
	v_max_f32_e32 v19, v5, v15
	v_min_f32_e32 v53, v53, v55
	v_max_f32_e32 v55, v56, v54
	v_min_f32_e32 v54, v56, v54
	v_max_f32_e32 v56, v51, v25
	v_min_f32_e32 v25, v51, v25
	v_max_f32_e32 v51, v32, v21
	v_min_f32_e32 v5, v5, v15
	v_max_f32_e32 v15, v19, v10
	v_min_f32_e32 v21, v32, v21
	v_max_f32_e32 v32, v51, v25
	v_min_f32_e32 v10, v19, v10
	v_max_f32_e32 v19, v34, v36
	v_min_f32_e32 v34, v34, v36
	v_max_f32_e32 v36, v15, v13
	v_min_f32_e32 v13, v15, v13
	v_min_f32_e32 v25, v51, v25
	v_max_f32_e32 v51, v56, v55
	v_min_f32_e32 v55, v56, v55
	v_max_f32_e32 v56, v32, v54
	v_min_f32_e32 v32, v32, v54
	v_max_f32_e32 v15, v10, v11
	v_min_f32_e32 v10, v10, v11
	v_min_f32_e32 v11, v40, v38
	v_max_f32_e32 v41, v4, v13
	v_max_f32_e32 v54, v25, v53
	v_min_f32_e32 v25, v25, v53
	v_min_f32_e32 v53, v58, v57
	v_max_f32_e32 v59, v30, v32
	v_min_f32_e32 v4, v4, v13
	v_max_f32_e32 v13, v41, v11
	v_min_f32_e32 v11, v41, v11
	v_max_f32_e32 v41, v8, v34
	v_min_f32_e32 v8, v8, v34
	v_max_f32_e32 v34, v3, v10
	v_min_f32_e32 v30, v30, v32
	v_max_f32_e32 v32, v59, v53
	v_min_f32_e32 v53, v59, v53
	v_max_f32_e32 v59, v50, v55
	v_min_f32_e32 v50, v50, v55
	v_max_f32_e32 v55, v24, v25
	v_min_f32_e32 v3, v3, v10
	v_max_f32_e32 v10, v34, v8
	v_min_f32_e32 v8, v34, v8
	v_min_f32_e32 v24, v24, v25
	v_max_f32_e32 v25, v55, v50
	v_min_f32_e32 v50, v55, v50
	v_max_f32_e32 v34, v41, v13
	v_min_f32_e32 v13, v41, v13
	v_max_f32_e32 v41, v10, v11
	v_min_f32_e32 v10, v10, v11
	v_max_f32_e32 v11, v8, v4
	v_min_f32_e32 v4, v8, v4
	v_max_f32_e32 v8, v7, v19
	v_min_f32_e32 v7, v7, v19
	v_max_f32_e32 v19, v6, v15
	v_max_f32_e32 v55, v59, v32
	v_min_f32_e32 v32, v59, v32
	v_max_f32_e32 v59, v25, v53
	v_min_f32_e32 v25, v25, v53
	v_max_f32_e32 v53, v50, v30
	v_min_f32_e32 v30, v50, v30
	v_max_f32_e32 v50, v49, v51
	v_min_f32_e32 v49, v49, v51
	v_max_f32_e32 v51, v48, v54
	v_min_f32_e32 v6, v6, v15
	v_max_f32_e32 v15, v19, v7
	v_min_f32_e32 v7, v19, v7
	v_max_f32_e32 v19, v9, v36
	v_min_f32_e32 v9, v9, v36
	v_max_f32_e32 v36, v2, v5
	v_min_f32_e32 v48, v48, v54
	v_max_f32_e32 v54, v51, v49
	v_min_f32_e32 v49, v51, v49
	v_max_f32_e32 v51, v52, v56
	v_min_f32_e32 v52, v52, v56
	v_max_f32_e32 v56, v23, v21
	v_min_f32_e32 v2, v2, v5
	v_max_f32_e32 v5, v36, v9
	v_min_f32_e32 v9, v36, v9
	v_max_f32_e32 v36, v19, v15
	v_min_f32_e32 v21, v23, v21
	v_max_f32_e32 v23, v56, v52
	v_min_f32_e32 v52, v56, v52
	v_and_b32_e32 v20, 0xffffff80, v72
	v_min_f32_e32 v15, v19, v15
	v_max_f32_e32 v19, v5, v7
	v_min_f32_e32 v5, v5, v7
	v_max_f32_e32 v7, v9, v6
	v_min_f32_e32 v6, v9, v6
	v_min_f32_e32 v9, v8, v34
	v_min_f32_e32 v42, v36, v13
	v_max_f32_e32 v56, v51, v54
	v_min_f32_e32 v51, v51, v54
	v_max_f32_e32 v54, v23, v49
	v_min_f32_e32 v23, v23, v49
	v_max_f32_e32 v49, v52, v48
	v_min_f32_e32 v48, v52, v48
	v_and_b32_e32 v39, 0xffffff80, v65
	v_min_f32_e32 v65, v48, v24
	v_max3_f32 v9, v9, v48, v24
	v_max3_f32 v24, v42, v49, v30
	v_add_f32_e32 v27, v27, v28
	v_add_f32_e32 v28, v20, v17
	v_add_f32_e32 v42, v20, v18
	v_add_f32_e32 v20, v20, v26
	v_and_b32_e32 v22, 0xffffff80, v73
	v_and_or_b32 v27, v27, s4, 51
	v_and_or_b32 v28, v28, s4, 64
	v_and_b32_e32 v42, 0xffffff00, v42
	v_and_b32_e32 v20, 0xffffff00, v20
	v_and_b32_e32 v29, 0xffffff80, v74
	v_and_b32_e32 v31, 0xffffff80, v75
	v_and_b32_e32 v33, 0xffffff80, v70
	v_and_b32_e32 v35, 0xffffff80, v71
	v_and_b32_e32 v37, 0xffffff80, v64
;     __device__ __forceinline__ void fused(f32x4 (&acc)[2][2][4][2], const Unit& u, int wr, int wc, int fr, int fq, PG8_LAS unsigned char* lds, int wid, int lane) const {
;     ...
;             { float cv[16]; cv[0] = __uint_as_float((__float_as_uint(v0[1] + v1[0]) & ~255u) | 16u); cv[1] = __uint_as_float((__float_as_uint(v0[1] + v1[1]) & ~255u) | 17u); cv[2] = __uint_as_float((__float_as_uint(v0[1] + v1[2]) & ~255u) | 18u); cv[3] = __uint_as_float((__float_as_uint(v0[1] + v1[3]) & ~255u) | 19u); cv[4] = __uint_as_float((__float_as_uint(v0[1] + v1[4]) & ~255u) | 20u); cv[5] = __uint_as_float((__float_as_uint(v0[1] + v1[5]) & ~255u) | 21u); cv[6] = __uint_as_float((__float_as_uint(v0[1] + v1[6]) & ~255u) | 22u); cv[7] = __uint_as_float((__float_as_uint(v0[1] + v1[7]) & ~255u) | 23u); cv[8] = __uint_as_float((__float_as_uint(v0[2] + v1[0]) & ~255u) | 32u); cv[9] = __uint_as_float((__float_as_uint(v0[2] + v1[1]) & ~255u) | 33u); cv[10] = __uint_as_float((__float_as_uint(v0[2] + v1[2]) & ~255u) | 34u); cv[11] = __uint_as_float((__float_as_uint(v0[2] + v1[3]) & ~255u) | 35u); cv[12] = __uint_as_float((__float_as_uint(v0[2] + v1[4]) & ~255u) | 36u); cv[13] = __uint_as_float((__float_as_uint(v0[3] + v1[0]) & ~255u) | 48u); cv[14] = __uint_as_float((__float_as_uint(v0[3] + v1[1]) & ~255u) | 49u); cv[15] = __uint_as_float((__float_as_uint(v0[3] + v1[2]) & ~255u) | 50u); sort16_desc(cv); merge_top16(best, cv); }
	v_min_f32_e32 v43, v15, v41
	v_min_f32_e32 v44, v19, v10
	v_min_f32_e32 v62, v54, v25
	v_or_b32_e32 v42, 0x41, v42
	v_or_b32_e32 v20, 0x42, v20
	v_add_f32_e32 v26, v22, v17
	v_add_f32_e32 v22, v22, v18
	v_min_f32_e32 v63, v23, v53
	v_max3_f32 v23, v43, v23, v53
	v_max3_f32 v10, v19, v10, v62
	v_max3_f32 v19, v44, v54, v25
	v_and_b32_e32 v26, 0xffffff00, v26
	v_and_b32_e32 v22, 0xffffff00, v22
	v_add_f32_e32 v43, v29, v17
	v_add_f32_e32 v29, v29, v18
	v_add_f32_e32 v44, v31, v17
	v_add_f32_e32 v18, v31, v18
	v_add_f32_e32 v31, v33, v17
	v_add_f32_e32 v33, v35, v17
	v_add_f32_e32 v35, v37, v17
	v_add_f32_e32 v37, v39, v17
	v_max_f32_e32 v39, v27, v28
	v_min_f32_e32 v27, v27, v28
	v_max_f32_e32 v28, v42, v42
	v_or_b32_e32 v26, 0x50, v26
	v_or_b32_e32 v22, 0x51, v22
	v_and_b32_e32 v43, 0xffffff00, v43
	v_and_b32_e32 v29, 0xffffff00, v29
	v_max_f32_e32 v42, v28, v20
	v_min_f32_e32 v20, v28, v20
	v_or_b32_e32 v43, 0x60, v43
	v_or_b32_e32 v29, 0x61, v29
	v_max_f32_e32 v28, v39, v42
	v_min_f32_e32 v39, v39, v42
	v_max_f32_e32 v42, v27, v20
	v_min_f32_e32 v20, v27, v20
	v_max_f32_e32 v27, v42, v39
	v_min_f32_e32 v39, v42, v39
	v_max_f32_e32 v42, v26, v22
	v_min_f32_e32 v22, v26, v22
	v_max_f32_e32 v26, v29, v29
	v_max_f32_e32 v29, v43, v43
	v_max_f32_e32 v43, v29, v26
	v_min_f32_e32 v26, v29, v26
	v_max_f32_e32 v29, v42, v43
	v_min_f32_e32 v42, v42, v43
	v_max_f32_e32 v43, v22, v26
	v_and_b32_e32 v12, 0xffffff80, v68
	v_and_b32_e32 v14, 0xffffff80, v69
	v_min_f32_e32 v22, v22, v26
	v_max_f32_e32 v26, v43, v42
	v_min_f32_e32 v42, v43, v42
	v_add_f32_e32 v12, v12, v17
	v_add_f32_e32 v14, v14, v17
	v_max_f32_e32 v43, v28, v29
	v_min_f32_e32 v28, v28, v29
	v_max_f32_e32 v29, v39, v42
	v_and_b32_e32 v44, 0xffffff00, v44
	v_and_b32_e32 v18, 0xffffff00, v18
	v_and_b32_e32 v12, 0xffffff00, v12
	v_and_b32_e32 v14, 0xffffff00, v14
	v_min_f32_e32 v39, v39, v42
	v_max_f32_e32 v42, v29, v28
	v_min_f32_e32 v28, v29, v28
	v_max_f32_e32 v29, v27, v26
	v_min_f32_e32 v26, v27, v26
	v_max_f32_e32 v27, v20, v22
	v_or_b32_e32 v44, 0x70, v44
	v_or_b32_e32 v18, 0x71, v18
	v_or_b32_e32 v12, 0x80, v12
	v_or_b32_e32 v14, 0x90, v14
	v_min_f32_e32 v20, v20, v22
	v_max_f32_e32 v22, v27, v26
	v_min_f32_e32 v26, v27, v26
	v_and_b32_e32 v31, 0xffffff00, v31
	v_and_b32_e32 v33, 0xffffff00, v33
	v_max_f32_e32 v27, v29, v42
	v_min_f32_e32 v29, v29, v42
	v_max_f32_e32 v42, v22, v28
	v_min_f32_e32 v22, v22, v28
	v_max_f32_e32 v28, v26, v39
	v_min_f32_e32 v26, v26, v39
	v_max_f32_e32 v39, v44, v44
	v_or_b32_e32 v31, 0xa0, v31
	v_or_b32_e32 v33, 0xb0, v33
	v_and_b32_e32 v35, 0xffffff00, v35
	v_and_b32_e32 v37, 0xffffff00, v37
	v_max_f32_e32 v44, v39, v18
	v_min_f32_e32 v18, v39, v18
	v_max_f32_e32 v39, v12, v14
	v_min_f32_e32 v12, v12, v14
	v_or_b32_e32 v35, 0xc0, v35
	v_or_b32_e32 v37, 0xd0, v37
	v_max_f32_e32 v14, v44, v39
	v_min_f32_e32 v39, v44, v39
	v_max_f32_e32 v44, v18, v12
	v_min_f32_e32 v12, v18, v12
	v_max_f32_e32 v18, v44, v39
	v_min_f32_e32 v39, v44, v39
	v_max_f32_e32 v44, v31, v33
	v_min_f32_e32 v31, v31, v33
	v_max_f32_e32 v33, v37, v37
	v_max_f32_e32 v37, v35, v33
	v_min_f32_e32 v33, v35, v33
	v_max_f32_e32 v35, v44, v37
	v_min_f32_e32 v37, v44, v37
	v_max_f32_e32 v44, v31, v33
	v_min_f32_e32 v31, v31, v33
	v_max_f32_e32 v33, v44, v37
	v_min_f32_e32 v37, v44, v37
	v_max_f32_e32 v44, v14, v35
	v_min_f32_e32 v14, v14, v35
	v_max_f32_e32 v35, v39, v37
	v_min_f32_e32 v37, v39, v37
	v_max_f32_e32 v39, v35, v14
	v_min_f32_e32 v14, v35, v14
	v_max_f32_e32 v35, v18, v33
	v_min_f32_e32 v18, v18, v33
	v_max_f32_e32 v33, v12, v31
	v_min_f32_e32 v12, v12, v31
	v_max_f32_e32 v31, v33, v18
	v_min_f32_e32 v45, v5, v11
	v_min_f32_e32 v61, v51, v59
	v_min_f32_e32 v18, v33, v18
	v_max_f32_e32 v33, v35, v39
	v_min_f32_e32 v35, v35, v39
	v_max_f32_e32 v39, v31, v14
	v_min_f32_e32 v14, v31, v14
	v_max3_f32 v5, v5, v11, v61
	v_max3_f32 v11, v45, v51, v59
	v_max_f32_e32 v31, v18, v37
	v_min_f32_e32 v18, v18, v37
	v_min_f32_e32 v37, v43, v44
	v_max_f32_e32 v45, v22, v14
	v_min_f32_e32 v14, v22, v14
	v_max_f32_e32 v22, v45, v37
	v_min_f32_e32 v37, v45, v37
	v_max_f32_e32 v45, v29, v35
	v_min_f32_e32 v29, v29, v35
	v_max_f32_e32 v35, v26, v18
	v_min_f32_e32 v46, v7, v4
	v_min_f32_e32 v47, v6, v3
	v_min_f32_e32 v52, v50, v55
	v_min_f32_e32 v60, v56, v32
	v_min_f32_e32 v64, v49, v30
	v_min_f32_e32 v18, v26, v18
	v_max_f32_e32 v26, v35, v29
	v_min_f32_e32 v29, v35, v29
	v_max3_f32 v21, v40, v38, v21
	v_max3_f32 v8, v8, v34, v65
	v_max3_f32 v13, v36, v13, v64
	v_max3_f32 v15, v15, v41, v63
	v_max3_f32 v4, v7, v4, v60
	v_max3_f32 v7, v46, v56, v32
	v_max3_f32 v3, v6, v3, v52
	v_max3_f32 v6, v47, v50, v55
	v_max3_f32 v2, v2, v58, v57
	v_max_f32_e32 v35, v45, v22
	v_min_f32_e32 v22, v45, v22
	v_max_f32_e32 v45, v26, v37
	v_min_f32_e32 v26, v26, v37
	v_max_f32_e32 v37, v29, v14
	v_min_f32_e32 v14, v29, v14
	v_max_f32_e32 v29, v27, v33
	v_min_f32_e32 v27, v27, v33
	v_max_f32_e32 v33, v28, v31
	v_max_f32_e32 v25, v21, v19
	v_min_f32_e32 v19, v21, v19
	v_max_f32_e32 v21, v8, v5
	v_min_f32_e32 v5, v8, v5
	v_max_f32_e32 v8, v9, v11
	v_min_f32_e32 v9, v9, v11
	v_max_f32_e32 v11, v13, v4
	v_min_f32_e32 v4, v13, v4
	v_max_f32_e32 v13, v24, v7
	v_min_f32_e32 v7, v24, v7
	v_max_f32_e32 v24, v15, v3
	v_min_f32_e32 v3, v15, v3
	v_max_f32_e32 v15, v23, v6
	v_min_f32_e32 v6, v23, v6
	v_max_f32_e32 v23, v10, v2
	v_min_f32_e32 v2, v10, v2
	v_min_f32_e32 v28, v28, v31
	v_max_f32_e32 v31, v33, v27
	v_min_f32_e32 v27, v33, v27
	v_max_f32_e32 v33, v42, v39
	v_min_f32_e32 v39, v42, v39
	v_max_f32_e32 v42, v20, v12
	v_max_f32_e32 v10, v25, v13
	v_min_f32_e32 v13, v25, v13
	v_max_f32_e32 v25, v21, v24
	v_min_f32_e32 v21, v21, v24
;     __device__ __forceinline__ void fused(f32x4 (&acc)[2][2][4][2], const Unit& u, int wr, int wc, int fr, int fq, PG8_LAS unsigned char* lds, int wid, int lane) const {
;     ...
;             { float cv[16]; cv[0] = __uint_as_float((__float_as_uint(v0[14] + v1[0]) & ~255u) | 224u); cv[1] = __uint_as_float((__float_as_uint(v0[15] + v1[0]) & ~255u) | 240u); cv[2] = -INFINITY; cv[3] = -INFINITY; cv[4] = -INFINITY; cv[5] = -INFINITY; cv[6] = -INFINITY; cv[7] = -INFINITY; cv[8] = -INFINITY; cv[9] = -INFINITY; cv[10] = -INFINITY; cv[11] = -INFINITY; cv[12] = -INFINITY; cv[13] = -INFINITY; cv[14] = -INFINITY; cv[15] = -INFINITY; sort16_desc(cv); merge_top16(best, cv); }
;             float sc[16], sum = 0.f;
; #pragma unroll
;             for (int q = 0; q < 16; ++q) { sc[q] = __uint_as_float(__float_as_uint(best[q]) & ~255u); }
;             const float smax = sc[0];
; #pragma unroll
;             for (int q = 0; q < 16; ++q) { sc[q] = __builtin_amdgcn_exp2f((sc[q] - smax) * 1.4426950408889634f); }
; #pragma unroll
;             for (int q = 0; q < 16; ++q) sum += sc[q];
;             const float rs = 1.0f / sum;
;             asm volatile("s_waitcnt lgkmcnt(0)" ::: "memory");
;             int ex[16];
; #pragma unroll
;             for (int q = 0; q < 16; ++q) { const unsigned cid = __float_as_uint(best[q]) & 255u; ex[q] = idxl[cid >> 4] * 128 + idxl[16 + (cid & 15u)]; }
	v_max_f32_e32 v24, v8, v15
	v_min_f32_e32 v8, v8, v15
	v_max_f32_e32 v15, v11, v23
	v_min_f32_e32 v11, v11, v23
	v_max_f32_e32 v23, v19, v7
	v_min_f32_e32 v7, v19, v7
	v_max_f32_e32 v19, v5, v3
	v_min_f32_e32 v3, v5, v3
	v_max_f32_e32 v5, v9, v6
	v_min_f32_e32 v6, v9, v6
	v_max_f32_e32 v9, v4, v2
	v_min_f32_e32 v2, v4, v2
	v_min_f32_e32 v12, v20, v12
	v_max_f32_e32 v20, v42, v39
	v_min_f32_e32 v39, v42, v39
	v_and_b32_e32 v1, 0xffffff80, v66
	v_and_b32_e32 v0, 0xffffff80, v67
	v_max_f32_e32 v4, v10, v24
	v_min_f32_e32 v10, v10, v24
	v_max_f32_e32 v24, v25, v15
	v_min_f32_e32 v15, v25, v15
	v_max_f32_e32 v25, v13, v8
	v_min_f32_e32 v8, v13, v8
	v_max_f32_e32 v13, v21, v11
	v_min_f32_e32 v11, v21, v11
	v_max_f32_e32 v21, v23, v5
	v_min_f32_e32 v5, v23, v5
	v_max_f32_e32 v23, v19, v9
	v_min_f32_e32 v9, v19, v9
	v_max_f32_e32 v19, v7, v6
	v_min_f32_e32 v6, v7, v6
	v_max_f32_e32 v7, v3, v2
	v_min_f32_e32 v2, v3, v2
	v_max_f32_e32 v42, v33, v31
	v_min_f32_e32 v31, v33, v31
	v_max_f32_e32 v33, v20, v27
	v_min_f32_e32 v20, v20, v27
	v_max_f32_e32 v27, v39, v28
	v_min_f32_e32 v28, v39, v28
	v_min_f32_e32 v3, v4, v24
	v_min_f32_e32 v30, v10, v15
	v_min_f32_e32 v32, v25, v13
	v_min_f32_e32 v34, v8, v11
	v_min_f32_e32 v36, v21, v23
	v_min_f32_e32 v38, v5, v9
	v_min_f32_e32 v40, v19, v7
	v_min_f32_e32 v41, v6, v2
	v_max_f32_e32 v39, v29, v35
	v_min_f32_e32 v29, v29, v35
	v_max_f32_e32 v35, v42, v22
	v_min_f32_e32 v22, v42, v22
	v_max_f32_e32 v42, v31, v45
	v_min_f32_e32 v31, v31, v45
	v_max_f32_e32 v45, v33, v26
	v_min_f32_e32 v26, v33, v26
	v_max_f32_e32 v33, v20, v37
	v_min_f32_e32 v20, v20, v37
	v_max_f32_e32 v37, v27, v14
	v_min_f32_e32 v14, v27, v14
	v_max_f32_e32 v27, v28, v18
	v_min_f32_e32 v18, v28, v18
	v_add_f32_e32 v1, v1, v17
	v_add_f32_e32 v0, v0, v17
	v_max3_f32 v4, v4, v24, v12
	v_max_f32_e32 v3, v3, v18
	v_max3_f32 v10, v10, v15, v27
	v_max_f32_e32 v12, v30, v14
	v_max3_f32 v13, v25, v13, v37
	v_max_f32_e32 v14, v32, v20
	v_max3_f32 v8, v8, v11, v33
	v_max_f32_e32 v11, v34, v26
	v_max3_f32 v15, v21, v23, v45
	v_max_f32_e32 v18, v36, v31
	v_max3_f32 v5, v5, v9, v42
	v_max_f32_e32 v9, v38, v22
	v_max3_f32 v7, v19, v7, v35
	v_max_f32_e32 v19, v40, v29
	v_max3_f32 v2, v6, v2, v39
	v_max3_f32 v6, v41, v43, v44
	v_and_b32_e32 v1, 0xffffff00, v1
	v_and_b32_e32 v0, 0xffffff00, v0
	v_max_f32_e32 v20, v4, v15
	v_min_f32_e32 v4, v4, v15
	v_max_f32_e32 v15, v3, v18
	v_min_f32_e32 v3, v3, v18
	v_max_f32_e32 v18, v10, v5
	v_min_f32_e32 v5, v10, v5
	v_max_f32_e32 v10, v12, v9
	v_min_f32_e32 v9, v12, v9
	v_max_f32_e32 v12, v13, v7
	v_min_f32_e32 v7, v13, v7
	v_max_f32_e32 v13, v14, v19
	v_min_f32_e32 v14, v14, v19
	v_max_f32_e32 v19, v8, v2
	v_min_f32_e32 v2, v8, v2
	v_max_f32_e32 v8, v11, v6
	v_min_f32_e32 v6, v11, v6
	v_or_b32_e32 v1, 0xe0, v1
	v_or_b32_e32 v0, 0xf0, v0
	v_max_f32_e32 v11, v20, v12
	v_min_f32_e32 v12, v20, v12
	v_max_f32_e32 v20, v15, v13
	v_min_f32_e32 v13, v15, v13
	v_max_f32_e32 v15, v18, v19
	v_min_f32_e32 v18, v18, v19
	v_max_f32_e32 v19, v10, v8
	v_min_f32_e32 v8, v10, v8
	v_max_f32_e32 v10, v4, v7
	v_min_f32_e32 v4, v4, v7
	v_max_f32_e32 v7, v3, v14
	v_min_f32_e32 v3, v3, v14
	v_max_f32_e32 v14, v5, v2
	v_min_f32_e32 v2, v5, v2
	v_max_f32_e32 v5, v9, v6
	v_min_f32_e32 v6, v9, v6
	v_max_f32_e32 v9, v11, v15
	v_min_f32_e32 v11, v11, v15
	v_max_f32_e32 v15, v20, v19
	v_min_f32_e32 v19, v20, v19
	v_max_f32_e32 v20, v12, v18
	v_min_f32_e32 v12, v12, v18
	v_max_f32_e32 v18, v13, v8
	v_min_f32_e32 v8, v13, v8
	v_max_f32_e32 v13, v10, v14
	v_min_f32_e32 v10, v10, v14
	v_max_f32_e32 v14, v7, v5
	v_min_f32_e32 v5, v7, v5
	v_max_f32_e32 v7, v4, v2
	v_min_f32_e32 v2, v4, v2
	v_max_f32_e32 v4, v3, v6
	v_min_f32_e32 v3, v3, v6
	v_max_f32_e32 v17, v1, v0
	v_min_f32_e32 v0, v1, v0
	v_min_f32_e32 v6, v9, v15
	v_min_f32_e32 v21, v11, v19
	v_min_f32_e32 v22, v20, v18
	v_min_f32_e32 v23, v12, v8
	v_min_f32_e32 v24, v13, v14
	v_min_f32_e32 v25, v10, v5
	v_min_f32_e32 v26, v7, v4
	v_min_f32_e32 v27, v2, v3
	s_mov_b32 s4, 0xff800000
	v_max_f32_e32 v0, 0xff800000, v0
	v_max3_f32 v1, v9, v15, s4
	v_max_f32_e32 v6, 0xff800000, v6
	v_max3_f32 v9, v11, v19, s4
	v_max_f32_e32 v11, 0xff800000, v21
	v_max3_f32 v15, v20, v18, s4
	v_max_f32_e32 v18, 0xff800000, v22
	v_max3_f32 v8, v12, v8, s4
	v_max_f32_e32 v12, 0xff800000, v23
	v_max3_f32 v13, v13, v14, s4
	v_max_f32_e32 v14, 0xff800000, v24
	v_max3_f32 v5, v10, v5, s4
	v_max_f32_e32 v10, 0xff800000, v25
	v_max3_f32 v4, v7, v4, s4
	v_max_f32_e32 v7, 0xff800000, v26
	v_max3_f32 v0, v2, v3, v0
	v_max3_f32 v2, v27, v17, s4
	v_max_f32_e32 v3, v1, v13
	v_min_f32_e32 v1, v1, v13
	v_max_f32_e32 v13, v6, v14
	v_min_f32_e32 v6, v6, v14
	v_max_f32_e32 v14, v9, v5
	v_min_f32_e32 v5, v9, v5
	v_max_f32_e32 v9, v11, v10
	v_min_f32_e32 v10, v11, v10
	v_max_f32_e32 v11, v15, v4
	v_min_f32_e32 v4, v15, v4
	v_max_f32_e32 v15, v18, v7
	v_max_f32_e32 v17, v8, v0
	v_min_f32_e32 v0, v8, v0
	v_max_f32_e32 v8, v12, v2
	v_min_f32_e32 v2, v12, v2
	v_max_f32_e32 v12, v3, v11
	v_min_f32_e32 v3, v3, v11
	v_max_f32_e32 v11, v13, v15
	v_min_f32_e32 v13, v13, v15
	v_max_f32_e32 v15, v14, v17
	v_min_f32_e32 v14, v14, v17
	v_max_f32_e32 v17, v9, v8
	v_min_f32_e32 v8, v9, v8
	v_max_f32_e32 v9, v1, v4
	v_min_f32_e32 v24, v1, v4
	v_max_f32_e32 v27, v5, v0
	v_min_f32_e32 v28, v5, v0
	v_max_f32_e32 v29, v10, v2
	v_min_f32_e32 v30, v10, v2
	v_max_f32_e32 v0, v12, v15
	v_min_f32_e32 v1, v12, v15
	v_max_f32_e32 v2, v11, v17
	v_min_f32_e32 v4, v11, v17
	v_min_f32_e32 v7, v18, v7
	v_max_f32_e32 v33, v0, v2
	v_min_f32_e32 v34, v0, v2
	v_min_f32_e32 v36, v1, v4
	v_max_f32_e32 v25, v6, v7
	v_min_f32_e32 v26, v6, v7
	v_max_f32_e32 v35, v1, v4
	v_lshrrev_b32_e32 v0, 2, v33
	v_lshrrev_b32_e32 v2, 2, v34
	v_lshrrev_b32_e32 v6, 2, v36
	v_max_f32_e32 v17, v3, v14
	v_min_f32_e32 v31, v3, v14
	v_and_b32_e32 v0, 60, v0
	v_and_b32_e32 v1, 15, v33
	v_and_b32_e32 v2, 60, v2
	v_and_b32_e32 v3, 15, v34
	v_lshrrev_b32_e32 v4, 2, v35
	v_and_b32_e32 v5, 15, v35
	v_and_b32_e32 v6, 60, v6
	v_and_b32_e32 v7, 15, v36
	s_waitcnt lgkmcnt(0)
; #define RT_PK(q_) (ex[q_] | (int)((__float_as_uint(usc[ex[q_]]) >> 23) << 14))
;     __device__ __forceinline__ void fused(f32x4 (&acc)[2][2][4][2], const Unit& u, int wr, int wc, int fr, int fq, PG8_LAS unsigned char* lds, int wid, int lane) const {
;     ...
;             for (int q = 0; q < 16; ++q) { sc[q] = __uint_as_float(__float_as_uint(best[q]) & ~255u); }
;             const float smax = sc[0];
; #pragma unroll
;             for (int q = 0; q < 16; ++q) { sc[q] = __builtin_amdgcn_exp2f((sc[q] - smax) * 1.4426950408889634f); }
; #pragma unroll
;             for (int q = 0; q < 16; ++q) sum += sc[q];
;             const float rs = 1.0f / sum;
;             asm volatile("s_waitcnt lgkmcnt(0)" ::: "memory");
;             int ex[16];
; #pragma unroll
;             for (int q = 0; q < 16; ++q) { const unsigned cid = __float_as_uint(best[q]) & 255u; ex[q] = idxl[cid >> 4] * 128 + idxl[16 + (cid & 15u)]; }
;             const size_t o = ((size_t)u.pn * 16384 + (size_t)(u.pm * BM + row)) * 16;
;             typedef int i32x4 __attribute__((ext_vector_type(4)));
; #pragma unroll
;             for (int i = 0; i < 4; ++i) {
;     ...
;                 *(i32x4*)(eidx + o + 4 * i) = (i32x4){RT_PK(4 * i), RT_PK(4 * i + 1), RT_PK(4 * i + 2), RT_PK(4 * i + 3)};
;                 *(f32x4*)(egate + o + 4 * i) = (f32x4){sc[4 * i] * rs * vsc[ex[4 * i]], sc[4 * i + 1] * rs * vsc[ex[4 * i + 1]], sc[4 * i + 2] * rs * vsc[ex[4 * i + 2]], sc[4 * i + 3] * rs * vsc[ex[4 * i + 3]]};
	v_add_u32_e32 v0, v16, v0
	v_lshl_add_u32 v1, v1, 2, v16
	v_add_u32_e32 v2, v16, v2
	v_lshl_add_u32 v3, v3, 2, v16
	v_and_b32_e32 v4, 60, v4
	v_lshl_add_u32 v5, v5, 2, v16
	v_add_u32_e32 v6, v16, v6
	v_lshl_add_u32 v7, v7, 2, v16
	v_add_u32_e32 v4, v16, v4
	ds_read_b32 v0, v0
	ds_read_b32 v1, v1 offset:64
	ds_read_b32 v2, v2
	ds_read_b32 v3, v3 offset:64
	ds_read_b32 v10, v4
	ds_read_b32 v5, v5 offset:64
	ds_read_b32 v6, v6
	ds_read_b32 v7, v7 offset:64
	s_waitcnt lgkmcnt(0)
	v_lshl_add_u32 v0, v0, 7, v1
	v_ashrrev_i32_e32 v1, 31, v0
	v_lshl_add_u32 v4, v2, 7, v3
	v_lshlrev_b64 v[14:15], 3, v[0:1]
	v_lshl_add_u32 v10, v10, 7, v5
	v_lshl_add_u32 v12, v6, 7, v7
	v_lshl_add_u64 v[2:3], s[8:9], 0, v[14:15]
	v_ashrrev_i32_e32 v5, 31, v4
	v_max_f32_e32 v32, v13, v8
	v_min_f32_e32 v8, v13, v8
	global_load_dwordx2 v[170:171], v[2:3], off
	v_lshlrev_b64 v[18:19], 3, v[4:5]
	v_ashrrev_i32_e32 v11, 31, v10
	v_ashrrev_i32_e32 v13, 31, v12
	v_lshl_add_u64 v[2:3], s[8:9], 0, v[18:19]
	v_lshlrev_b64 v[20:21], 3, v[10:11]
	v_lshlrev_b64 v[22:23], 3, v[12:13]
	v_lshl_add_u64 v[6:7], s[8:9], 0, v[20:21]
	global_load_dwordx2 v[172:173], v[2:3], off
	global_load_dwordx2 v[174:175], v[6:7], off
	v_lshl_add_u64 v[2:3], s[8:9], 0, v[22:23]
	global_load_dwordx2 v[176:177], v[2:3], off
	v_min_f32_e32 v2, v9, v27
	v_min_f32_e32 v6, v25, v29
	v_max_f32_e32 v43, v2, v6
	v_min_f32_e32 v44, v2, v6
	v_and_b32_e32 v2, 0xffffff00, v34
	v_and_b32_e32 v51, 0xffffff00, v33
	v_max_f32_e32 v37, v9, v27
	v_max_f32_e32 v3, v25, v29
	v_sub_f32_e32 v2, v2, v51
	v_min_f32_e32 v9, v24, v28
	v_min_f32_e32 v25, v26, v30
	v_max_f32_e32 v41, v37, v3
	v_min_f32_e32 v42, v37, v3
	v_and_b32_e32 v3, 0xffffff00, v35
	v_mul_f32_e32 v2, 0x3fb8aa3b, v2
	v_max_f32_e32 v47, v9, v25
	v_min_f32_e32 v48, v9, v25
	v_exp_f32_e32 v25, v2
	v_sub_f32_e32 v2, v3, v51
	v_and_b32_e32 v6, 0xffffff00, v36
	v_mul_f32_e32 v2, 0x3fb8aa3b, v2
	v_max_f32_e32 v7, v24, v28
	v_max_f32_e32 v24, v26, v30
	v_max_f32_e32 v38, v17, v32
	v_exp_f32_e32 v26, v2
	v_sub_f32_e32 v2, v6, v51
	v_max_f32_e32 v45, v7, v24
	v_min_f32_e32 v46, v7, v24
	v_and_b32_e32 v7, 0xffffff00, v38
	v_mul_f32_e32 v2, 0x3fb8aa3b, v2
	v_min_f32_e32 v17, v17, v32
	v_exp_f32_e32 v27, v2
	v_sub_f32_e32 v2, v7, v51
	v_max_f32_e32 v39, v31, v8
	v_min_f32_e32 v40, v31, v8
	v_and_b32_e32 v8, 0xffffff00, v17
	v_mul_f32_e32 v2, 0x3fb8aa3b, v2
	v_exp_f32_e32 v28, v2
	v_sub_f32_e32 v2, v8, v51
	v_and_b32_e32 v9, 0xffffff00, v39
	v_mul_f32_e32 v2, 0x3fb8aa3b, v2
	v_exp_f32_e32 v29, v2
	v_sub_f32_e32 v2, v9, v51
	v_and_b32_e32 v31, 0xffffff00, v40
	v_mul_f32_e32 v2, 0x3fb8aa3b, v2
	v_exp_f32_e32 v30, v2
	v_sub_f32_e32 v2, v31, v51
	v_and_b32_e32 v32, 0xffffff00, v41
	v_mul_f32_e32 v2, 0x3fb8aa3b, v2
	v_exp_f32_e32 v31, v2
	v_sub_f32_e32 v2, v32, v51
	v_and_b32_e32 v34, 0xffffff00, v42
	v_mul_f32_e32 v2, 0x3fb8aa3b, v2
	v_exp_f32_e32 v6, v2
	v_sub_f32_e32 v2, v34, v51
	v_and_b32_e32 v35, 0xffffff00, v43
	v_mul_f32_e32 v2, 0x3fb8aa3b, v2
	v_exp_f32_e32 v7, v2
	v_sub_f32_e32 v2, v35, v51
	v_mul_f32_e32 v2, 0x3fb8aa3b, v2
	v_exp_f32_e32 v8, v2
	v_lshl_or_b32 v2, s18, 8, v128
	v_ashrrev_i32_e32 v3, 31, v2
	s_lshl_b64 s[4:5], s[16:17], 18
	v_lshl_add_u64 v[32:33], v[2:3], 4, s[4:5]
	s_mov_b32 s4, 0x7fc000
	v_sub_f32_e32 v24, v51, v51
	v_mul_f32_e32 v24, 0x3fb8aa3b, v24
	v_exp_f32_e32 v24, v24
	s_waitcnt vmcnt(0)
	v_lshrrev_b32_e32 v1, 9, v170
	v_and_or_b32 v2, v1, s4, v0
	v_and_b32_e32 v36, 0xffffff00, v44
	v_and_b32_e32 v37, 0xffffff00, v45
	v_and_b32_e32 v49, 0xffffff00, v46
	v_and_b32_e32 v50, 0xffffff00, v47
	v_and_b32_e32 v52, 0xffffff00, v48
	v_lshrrev_b32_e32 v0, 9, v172
	v_and_or_b32 v3, v0, s4, v4
	v_lshrrev_b32_e32 v0, 9, v174
	v_and_or_b32 v4, v0, s4, v10
	v_lshrrev_b32_e32 v0, 9, v176
	v_and_or_b32 v5, v0, s4, v12
	v_lshlrev_b64 v[12:13], 2, v[32:33]
	v_lshl_add_u64 v[0:1], s[12:13], 0, v[12:13]
	global_store_dwordx4 v[0:1], v[2:5], off
	v_lshrrev_b32_e32 v32, 2, v40
	v_add_f32_e32 v10, 0, v24
	v_add_f32_e32 v10, v25, v10
	v_add_f32_e32 v10, v26, v10
	v_add_f32_e32 v10, v27, v10
	v_sub_f32_e32 v2, v36, v51
	v_add_f32_e32 v10, v28, v10
	v_mul_f32_e32 v2, 0x3fb8aa3b, v2
	v_add_f32_e32 v10, v29, v10
	v_exp_f32_e32 v9, v2
	v_sub_f32_e32 v2, v37, v51
	v_add_f32_e32 v10, v30, v10
	v_mul_f32_e32 v2, 0x3fb8aa3b, v2
	v_sub_f32_e32 v3, v49, v51
	v_add_f32_e32 v10, v31, v10
	v_exp_f32_e32 v2, v2
	v_mul_f32_e32 v3, 0x3fb8aa3b, v3
	v_sub_f32_e32 v4, v50, v51
	v_add_f32_e32 v10, v6, v10
	v_exp_f32_e32 v3, v3
	v_mul_f32_e32 v4, 0x3fb8aa3b, v4
	v_sub_f32_e32 v5, v52, v51
	v_add_f32_e32 v10, v7, v10
	v_exp_f32_e32 v4, v4
	v_mul_f32_e32 v5, 0x3fb8aa3b, v5
	v_add_f32_e32 v10, v8, v10
	v_exp_f32_e32 v5, v5
	v_add_f32_e32 v10, v9, v10
	v_add_f32_e32 v10, v2, v10
	v_lshrrev_b32_e32 v11, 2, v38
	v_lshrrev_b32_e32 v15, 2, v17
	v_add_f32_e32 v10, v3, v10
	v_and_b32_e32 v11, 60, v11
	v_and_b32_e32 v14, 15, v38
	v_and_b32_e32 v15, 60, v15
	v_and_b32_e32 v17, 15, v17
	v_lshrrev_b32_e32 v22, 2, v39
	v_and_b32_e32 v23, 15, v39
	v_and_b32_e32 v33, 15, v40
	v_add_f32_e32 v10, v4, v10
	v_add_u32_e32 v11, v16, v11
	v_lshl_add_u32 v14, v14, 2, v16
	v_add_u32_e32 v15, v16, v15
	v_lshl_add_u32 v17, v17, 2, v16
	v_and_b32_e32 v22, 60, v22
	v_lshl_add_u32 v23, v23, 2, v16
	v_and_b32_e32 v32, 60, v32
	v_lshl_add_u32 v33, v33, 2, v16
	v_add_f32_e32 v10, v5, v10
	v_add_u32_e32 v22, v16, v22
	v_add_u32_e32 v32, v16, v32
	ds_read_b32 v11, v11
	ds_read_b32 v14, v14 offset:64
	ds_read_b32 v15, v15
	ds_read_b32 v17, v17 offset:64
	ds_read_b32 v34, v22
	ds_read_b32 v23, v23 offset:64
	ds_read_b32 v35, v32
	ds_read_b32 v33, v33 offset:64
	s_waitcnt lgkmcnt(6)
; #define RT_PK(q_) (ex[q_] | (int)((__float_as_uint(usc[ex[q_]]) >> 23) << 14))
;     __device__ __forceinline__ void fused(f32x4 (&acc)[2][2][4][2], const Unit& u, int wr, int wc, int fr, int fq, PG8_LAS unsigned char* lds, int wid, int lane) const {
;     ...
;             for (int q = 0; q < 16; ++q) { const unsigned cid = __float_as_uint(best[q]) & 255u; ex[q] = idxl[cid >> 4] * 128 + idxl[16 + (cid & 15u)]; }
;             const size_t o = ((size_t)u.pn * 16384 + (size_t)(u.pm * BM + row)) * 16;
;             typedef int i32x4 __attribute__((ext_vector_type(4)));
; #pragma unroll
;             for (int i = 0; i < 4; ++i) {
;     ...
;                 *(i32x4*)(eidx + o + 4 * i) = (i32x4){RT_PK(4 * i), RT_PK(4 * i + 1), RT_PK(4 * i + 2), RT_PK(4 * i + 3)};
;                 *(f32x4*)(egate + o + 4 * i) = (f32x4){sc[4 * i] * rs * vsc[ex[4 * i]], sc[4 * i + 1] * rs * vsc[ex[4 * i + 1]], sc[4 * i + 2] * rs * vsc[ex[4 * i + 2]], sc[4 * i + 3] * rs * vsc[ex[4 * i + 3]]};
	v_lshl_add_u32 v14, v11, 7, v14
	v_div_scale_f32 v11, s[16:17], v10, v10, 1.0
	v_rcp_f32_e32 v36, v11
	s_waitcnt lgkmcnt(4)
	v_lshl_add_u32 v22, v15, 7, v17
	s_waitcnt lgkmcnt(2)
	v_lshl_add_u32 v32, v34, 7, v23
	s_waitcnt lgkmcnt(0)
	v_lshl_add_u32 v34, v35, 7, v33
	v_fma_f32 v15, -v11, v36, 1.0
	v_fmac_f32_e32 v36, v15, v36
	v_div_scale_f32 v15, vcc, 1.0, v10, 1.0
	v_mul_f32_e32 v17, v15, v36
	v_fma_f32 v23, -v11, v17, v15
	v_fmac_f32_e32 v17, v23, v36
	v_fma_f32 v11, -v11, v17, v15
	v_div_fmas_f32 v11, v11, v36, v17
	v_div_fixup_f32 v10, v11, v10, 1.0
	v_pk_mul_f32 v[24:25], v[24:25], v[10:11] op_sel_hi:[1,0]
	v_pk_mul_f32 v[26:27], v[26:27], v[10:11] op_sel_hi:[1,0]
	v_ashrrev_i32_e32 v15, 31, v14
	v_ashrrev_i32_e32 v33, 31, v32
	v_lshl_add_u64 v[12:13], s[10:11], 0, v[12:13]
	v_ashrrev_i32_e32 v23, 31, v22
	v_lshlrev_b64 v[36:37], 3, v[32:33]
	v_lshl_add_u64 v[38:39], s[8:9], 0, v[36:37]
	v_ashrrev_i32_e32 v35, 31, v34
	v_mul_f32_e32 v18, v24, v171
	v_mul_f32_e32 v19, v25, v173
	v_lshlrev_b64 v[24:25], 3, v[14:15]
	v_mul_f32_e32 v20, v26, v175
	v_mul_f32_e32 v21, v27, v177
	global_store_dwordx4 v[12:13], v[18:21], off
	v_lshlrev_b64 v[26:27], 3, v[22:23]
	s_nop 0
	v_lshl_add_u64 v[18:19], s[8:9], 0, v[24:25]
	v_lshl_add_u64 v[20:21], s[8:9], 0, v[26:27]
	global_load_dwordx2 v[178:179], v[18:19], off
	global_load_dwordx2 v[180:181], v[20:21], off
	global_load_dwordx2 v[182:183], v[38:39], off
	v_lshlrev_b64 v[38:39], 3, v[34:35]
	v_lshl_add_u64 v[18:19], s[8:9], 0, v[38:39]
	global_load_dwordx2 v[184:185], v[18:19], off
	s_waitcnt vmcnt(3)
	v_lshrrev_b32_e32 v11, 9, v178
	v_and_or_b32 v18, v11, s4, v14
	s_waitcnt vmcnt(2)
	v_lshrrev_b32_e32 v11, 9, v180
	v_and_or_b32 v19, v11, s4, v22
	s_waitcnt vmcnt(1)
	v_lshrrev_b32_e32 v11, 9, v182
	v_and_or_b32 v20, v11, s4, v32
	s_waitcnt vmcnt(0)
	v_lshrrev_b32_e32 v11, 9, v184
	v_and_or_b32 v21, v11, s4, v34
	global_store_dwordx4 v[0:1], v[18:21], off offset:16
	v_lshrrev_b32_e32 v11, 2, v41
	v_lshrrev_b32_e32 v15, 2, v42
	v_lshrrev_b32_e32 v18, 2, v43
	v_lshrrev_b32_e32 v20, 2, v44
	v_and_b32_e32 v11, 60, v11
	v_and_b32_e32 v14, 15, v41
	v_and_b32_e32 v15, 60, v15
	v_and_b32_e32 v17, 15, v42
	v_and_b32_e32 v18, 60, v18
	v_and_b32_e32 v19, 15, v43
	v_and_b32_e32 v20, 60, v20
	v_and_b32_e32 v21, 15, v44
	v_add_u32_e32 v11, v16, v11
	v_lshl_add_u32 v14, v14, 2, v16
	v_add_u32_e32 v15, v16, v15
	v_lshl_add_u32 v17, v17, 2, v16
	v_add_u32_e32 v18, v16, v18
	v_lshl_add_u32 v19, v19, 2, v16
	v_add_u32_e32 v20, v16, v20
	v_lshl_add_u32 v21, v21, 2, v16
	ds_read_b32 v11, v11
	ds_read_b32 v14, v14 offset:64
	ds_read_b32 v15, v15
	ds_read_b32 v17, v17 offset:64
	ds_read_b32 v18, v18
	ds_read_b32 v19, v19 offset:64
	ds_read_b32 v20, v20
	ds_read_b32 v21, v21 offset:64
	s_waitcnt lgkmcnt(6)
	v_lshl_add_u32 v14, v11, 7, v14
	s_waitcnt lgkmcnt(4)
	v_lshl_add_u32 v22, v15, 7, v17
	s_waitcnt lgkmcnt(2)
	v_lshl_add_u32 v32, v18, 7, v19
	v_pk_mul_f32 v[18:19], v[28:29], v[10:11] op_sel_hi:[1,0]
	s_waitcnt lgkmcnt(0)
	v_lshl_add_u32 v34, v20, 7, v21
	v_pk_mul_f32 v[20:21], v[30:31], v[10:11] op_sel_hi:[1,0]
	v_ashrrev_i32_e32 v15, 31, v14
	v_ashrrev_i32_e32 v33, 31, v32
	v_ashrrev_i32_e32 v23, 31, v22
	v_lshlrev_b64 v[28:29], 3, v[32:33]
	v_lshl_add_u64 v[30:31], s[8:9], 0, v[28:29]
	v_ashrrev_i32_e32 v35, 31, v34
	v_mul_f32_e32 v20, v20, v183
	v_mul_f32_e32 v21, v21, v185
	v_mul_f32_e32 v18, v18, v179
	v_mul_f32_e32 v19, v19, v181
	v_lshlrev_b64 v[24:25], 3, v[14:15]
	global_store_dwordx4 v[12:13], v[18:21], off offset:16
	v_lshlrev_b64 v[26:27], 3, v[22:23]
	s_nop 0
	v_lshl_add_u64 v[18:19], s[8:9], 0, v[24:25]
	v_lshl_add_u64 v[20:21], s[8:9], 0, v[26:27]
	global_load_dwordx2 v[186:187], v[18:19], off
	global_load_dwordx2 v[188:189], v[20:21], off
	global_load_dwordx2 v[190:191], v[30:31], off
	v_lshlrev_b64 v[30:31], 3, v[34:35]
	v_lshl_add_u64 v[18:19], s[8:9], 0, v[30:31]
	global_load_dwordx2 v[192:193], v[18:19], off
	s_waitcnt vmcnt(3)
	v_lshrrev_b32_e32 v11, 9, v186
	v_and_or_b32 v18, v11, s4, v14
	s_waitcnt vmcnt(2)
	v_lshrrev_b32_e32 v11, 9, v188
	v_and_or_b32 v19, v11, s4, v22
	s_waitcnt vmcnt(1)
	v_lshrrev_b32_e32 v11, 9, v190
	v_and_or_b32 v20, v11, s4, v32
	s_waitcnt vmcnt(0)
	v_lshrrev_b32_e32 v11, 9, v192
	v_and_or_b32 v21, v11, s4, v34
	global_store_dwordx4 v[0:1], v[18:21], off offset:32
	v_lshrrev_b32_e32 v11, 2, v45
	v_lshrrev_b32_e32 v15, 2, v46
	v_lshrrev_b32_e32 v18, 2, v47
	v_lshrrev_b32_e32 v20, 2, v48
	v_and_b32_e32 v11, 60, v11
	v_and_b32_e32 v14, 15, v45
	v_and_b32_e32 v15, 60, v15
	v_and_b32_e32 v17, 15, v46
	v_and_b32_e32 v18, 60, v18
	v_and_b32_e32 v19, 15, v47
	v_and_b32_e32 v20, 60, v20
	v_add_u32_e32 v11, v16, v11
	v_lshl_add_u32 v14, v14, 2, v16
	v_add_u32_e32 v15, v16, v15
	v_lshl_add_u32 v17, v17, 2, v16
	v_add_u32_e32 v18, v16, v18
	v_lshl_add_u32 v19, v19, 2, v16
	v_add_u32_e32 v20, v16, v20
	v_and_b32_e32 v21, 15, v48
	v_lshl_add_u32 v16, v21, 2, v16
	ds_read_b32 v11, v11
	ds_read_b32 v14, v14 offset:64
	ds_read_b32 v15, v15
	ds_read_b32 v17, v17 offset:64
	ds_read_b32 v18, v18
	ds_read_b32 v19, v19 offset:64
	ds_read_b32 v20, v20
	ds_read_b32 v21, v16 offset:64
	s_waitcnt lgkmcnt(6)
	v_lshl_add_u32 v14, v11, 7, v14
	s_waitcnt lgkmcnt(4)
	v_lshl_add_u32 v16, v15, 7, v17
	s_waitcnt lgkmcnt(2)
	v_lshl_add_u32 v18, v18, 7, v19
	v_pk_mul_f32 v[6:7], v[6:7], v[10:11] op_sel_hi:[1,0]
	v_pk_mul_f32 v[8:9], v[8:9], v[10:11] op_sel_hi:[1,0]
	v_ashrrev_i32_e32 v15, 31, v14
	v_ashrrev_i32_e32 v19, 31, v18
	s_waitcnt lgkmcnt(0)
	v_lshl_add_u32 v20, v20, 7, v21
	v_lshlrev_b64 v[22:23], 3, v[14:15]
	v_ashrrev_i32_e32 v17, 31, v16
	v_ashrrev_i32_e32 v21, 31, v20
	v_mul_f32_e32 v8, v8, v191
	v_mul_f32_e32 v9, v9, v193
	v_mul_f32_e32 v6, v6, v187
	v_mul_f32_e32 v7, v7, v189
	v_lshlrev_b64 v[26:27], 3, v[18:19]
	global_store_dwordx4 v[12:13], v[6:9], off offset:32
	v_lshlrev_b64 v[24:25], 3, v[16:17]
	v_lshl_add_u64 v[28:29], s[8:9], 0, v[26:27]
	v_lshl_add_u64 v[6:7], s[8:9], 0, v[22:23]
	v_lshl_add_u64 v[8:9], s[8:9], 0, v[24:25]
	global_load_dwordx2 v[194:195], v[6:7], off
	global_load_dwordx2 v[196:197], v[8:9], off
	global_load_dwordx2 v[198:199], v[28:29], off
	v_lshlrev_b64 v[28:29], 3, v[20:21]
	v_lshl_add_u64 v[6:7], s[8:9], 0, v[28:29]
	global_load_dwordx2 v[200:201], v[6:7], off
	s_waitcnt vmcnt(3)
	v_lshrrev_b32_e32 v6, 9, v194
	s_waitcnt vmcnt(2)
	v_lshrrev_b32_e32 v7, 9, v196
	s_waitcnt vmcnt(1)
	v_lshrrev_b32_e32 v8, 9, v198
	v_and_or_b32 v6, v6, s4, v14
	v_and_or_b32 v7, v7, s4, v16
	s_waitcnt vmcnt(0)
	v_lshrrev_b32_e32 v9, 9, v200
	v_and_or_b32 v8, v8, s4, v18
	v_and_or_b32 v9, v9, s4, v20
	global_store_dwordx4 v[0:1], v[6:9], off offset:48
	v_pk_mul_f32 v[0:1], v[2:3], v[10:11] op_sel_hi:[1,0]
	v_pk_mul_f32 v[2:3], v[4:5], v[10:11] op_sel_hi:[1,0]
	v_mul_f32_e32 v0, v0, v195
	v_mul_f32_e32 v1, v1, v197
	v_mul_f32_e32 v2, v2, v199
	v_mul_f32_e32 v3, v3, v201
	global_store_dwordx4 v[12:13], v[0:3], off offset:48

; #define PG8_LAS __attribute__((address_space(3)))
;     __device__ __forceinline__ void fused(f32x4 (&acc)[2][2][4][2], const Unit& u, int wr, int wc, int fr, int fq, PG8_LAS unsigned char* lds, int wid, int lane) const {
;     ...
;         if (half == 0) {
;             PG8_LAS int* idxl = (PG8_LAS int*)(lds + 65536) + row * 32;
;             float v0[16], v1[16];
; #pragma unroll
;             for (int q = 0; q < 16; ++q) { const unsigned b0 = __float_as_uint(top0[q]), b1 = __float_as_uint(top1[q]);
;                 v0[q] = __uint_as_float(b0 & ~127u); v1[q] = __uint_as_float(b1 & ~127u); idxl[q] = (int)(b0 & 127u); idxl[16 + q] = (int)(b1 & 127u); }
;             float best[16];
;             { float cv[16]; cv[0] = __uint_as_float((__float_as_uint(v0[0] + v1[0]) & ~255u) | 0u); cv[1] = __uint_as_float((__float_as_uint(v0[0] + v1[1]) & ~255u) | 1u); cv[2] = __uint_as_float((__float_as_uint(v0[0] + v1[2]) & ~255u) | 2u); cv[3] = __uint_as_float((__float_as_uint(v0[0] + v1[3]) & ~255u) | 3u); cv[4] = __uint_as_float((__float_as_uint(v0[0] + v1[4]) & ~255u) | 4u); cv[5] = __uint_as_float((__float_as_uint(v0[0] + v1[5]) & ~255u) | 5u); cv[6] = __uint_as_float((__float_as_uint(v0[0] + v1[6]) & ~255u) | 6u); cv[7] = __uint_as_float((__float_as_uint(v0[0] + v1[7]) & ~255u) | 7u); cv[8] = __uint_as_float((__float_as_uint(v0[0] + v1[8]) & ~255u) | 8u); cv[9] = __uint_as_float((__float_as_uint(v0[0] + v1[9]) & ~255u) | 9u); cv[10] = __uint_as_float((__float_as_uint(v0[0] + v1[10]) & ~255u) | 10u); cv[11] = __uint_as_float((__float_as_uint(v0[0] + v1[11]) & ~255u) | 11u); cv[12] = __uint_as_float((__float_as_uint(v0[0] + v1[12]) & ~255u) | 12u); cv[13] = __uint_as_float((__float_as_uint(v0[0] + v1[13]) & ~255u) | 13u); cv[14] = __uint_as_float((__float_as_uint(v0[0] + v1[14]) & ~255u) | 14u); cv[15] = __uint_as_float((__float_as_uint(v0[0] + v1[15]) & ~255u) | 15u); sort16_desc(cv);
; #pragma unroll
;               for (int q = 0; q < 16; ++q) best[q] = cv[q]; }
.LBB0_606:
	s_waitcnt lgkmcnt(0)
	s_barrier
	s_and_b64 vcc, exec, s[4:5]
	s_cbranch_vccnz .LBB0_608
	v_lshl_add_u32 v16, v128, 7, 0
	v_add_u32_e32 v16, 0x10000, v16
	v_and_b32_e32 v17, 0xffffff80, v12
	v_and_b32_e32 v18, 0xffffff80, v13
	v_and_b32_e32 v21, 0x7f, v77
	v_and_b32_e32 v20, 0x7f, v76
	v_and_b32_e32 v13, 0x7f, v13
	v_and_b32_e32 v12, 0x7f, v12
	v_and_b32_e32 v26, 0xffffff80, v14
	v_and_b32_e32 v28, 0xffffff80, v15
	v_and_b32_e32 v23, 0x7f, v79
	v_and_b32_e32 v22, 0x7f, v78
	v_and_b32_e32 v15, 0x7f, v15
	v_and_b32_e32 v14, 0x7f, v14
	ds_write_b128 v16, v[20:23]
	ds_write_b128 v16, v[12:15] offset:64
	v_and_b32_e32 v21, 0xffffff80, v8
	v_and_b32_e32 v23, 0xffffff80, v9
	v_and_b32_e32 v13, 0x7f, v73
	v_and_b32_e32 v12, 0x7f, v72
	v_and_b32_e32 v9, 0x7f, v9
	v_and_b32_e32 v8, 0x7f, v8
	v_and_b32_e32 v30, 0xffffff80, v10
	v_and_b32_e32 v32, 0xffffff80, v11
	v_and_b32_e32 v15, 0x7f, v75
	v_and_b32_e32 v14, 0x7f, v74
	v_and_b32_e32 v11, 0x7f, v11
	v_and_b32_e32 v10, 0x7f, v10
	v_and_b32_e32 v19, 0xffffff80, v76
	ds_write_b128 v16, v[12:15] offset:16
	ds_write_b128 v16, v[8:11] offset:80
	v_and_b32_e32 v13, 0xffffff80, v4
	v_and_b32_e32 v15, 0xffffff80, v5
	v_and_b32_e32 v9, 0x7f, v69
	v_and_b32_e32 v8, 0x7f, v68
	v_and_b32_e32 v5, 0x7f, v5
	v_and_b32_e32 v4, 0x7f, v4
	v_and_b32_e32 v34, 0xffffff80, v6
	v_and_b32_e32 v36, 0xffffff80, v7
	v_and_b32_e32 v11, 0x7f, v71
	v_and_b32_e32 v10, 0x7f, v70
	v_and_b32_e32 v7, 0x7f, v7
	v_and_b32_e32 v6, 0x7f, v6
	ds_write_b128 v16, v[8:11] offset:32
	ds_write_b128 v16, v[4:7] offset:96
	v_and_b32_e32 v5, 0x7f, v65
	v_and_b32_e32 v4, 0x7f, v64
	v_and_b32_e32 v41, 0xffffff80, v2
	v_and_b32_e32 v42, 0xffffff80, v3
	v_and_b32_e32 v7, 0x7f, v67
	v_and_b32_e32 v6, 0x7f, v66
	v_and_b32_e32 v11, 0x7f, v3
	v_and_b32_e32 v10, 0x7f, v2
	v_add_f32_e32 v2, v19, v17
	s_movk_i32 s3, 0xff00
	v_add_f32_e32 v3, v19, v18
	v_and_b32_e32 v24, 0xffffff80, v77
	ds_write_b128 v16, v[4:7] offset:48
	v_and_b32_e32 v2, 0xffffff00, v2
	v_and_or_b32 v3, v3, s3, 1
	v_add_f32_e32 v4, v19, v26
	v_add_f32_e32 v5, v19, v28
	v_and_b32_e32 v40, 0xffffff80, v1
	v_and_b32_e32 v9, 0x7f, v1
	v_and_b32_e32 v8, 0x7f, v0
	v_and_or_b32 v4, v4, s3, 2
	v_and_or_b32 v5, v5, s3, 3
	v_add_f32_e32 v48, v24, v17
	v_add_f32_e32 v49, v24, v18
	ds_write_b128 v16, v[8:11] offset:112
	v_add_f32_e32 v6, v19, v21
	v_add_f32_e32 v7, v19, v23
	v_add_f32_e32 v11, v19, v15
	v_add_f32_e32 v15, v19, v36
	v_add_f32_e32 v36, v19, v40
	v_max_f32_e32 v40, v2, v3
	v_min_f32_e32 v2, v2, v3
	v_max_f32_e32 v3, v5, v5
	v_and_or_b32 v48, v48, s3, 16
	v_and_or_b32 v49, v49, s3, 17
	v_add_f32_e32 v50, v24, v26
	v_add_f32_e32 v51, v24, v28
	v_and_or_b32 v6, v6, s3, 4
	v_and_or_b32 v7, v7, s3, 5
	v_add_f32_e32 v8, v19, v30
	v_add_f32_e32 v9, v19, v32
	v_max_f32_e32 v5, v4, v3
	v_min_f32_e32 v3, v4, v3
	v_and_or_b32 v50, v50, s3, 18
	v_and_or_b32 v51, v51, s3, 19
	v_and_or_b32 v8, v8, s3, 6
	v_and_or_b32 v9, v9, s3, 7
	v_max_f32_e32 v4, v40, v5
	v_min_f32_e32 v5, v40, v5
	v_max_f32_e32 v40, v2, v3
	v_add_f32_e32 v52, v24, v21
	v_add_f32_e32 v23, v24, v23
	v_add_f32_e32 v30, v24, v30
	v_add_f32_e32 v24, v24, v32
	v_max_f32_e32 v58, v48, v49
	v_min_f32_e32 v48, v48, v49
	v_max_f32_e32 v49, v51, v51
	v_min_f32_e32 v2, v2, v3
	v_max_f32_e32 v3, v40, v5
	v_min_f32_e32 v5, v40, v5
	v_max_f32_e32 v40, v6, v7
	v_min_f32_e32 v6, v6, v7
	v_max_f32_e32 v7, v9, v9
	v_and_or_b32 v52, v52, s3, 20
	v_and_or_b32 v23, v23, s3, 21
	v_and_or_b32 v30, v30, s3, 22
	v_and_or_b32 v24, v24, s3, 23
	v_max_f32_e32 v51, v50, v49
	v_min_f32_e32 v49, v50, v49
	v_max_f32_e32 v9, v8, v7
	v_min_f32_e32 v7, v8, v7
	v_max_f32_e32 v50, v58, v51
	v_min_f32_e32 v51, v58, v51
	v_max_f32_e32 v58, v48, v49
	v_max_f32_e32 v8, v40, v9
	v_min_f32_e32 v9, v40, v9
	v_max_f32_e32 v40, v6, v7
	v_min_f32_e32 v48, v48, v49
	v_max_f32_e32 v49, v58, v51
	v_min_f32_e32 v51, v58, v51
	v_max_f32_e32 v58, v52, v23
	v_min_f32_e32 v23, v52, v23
	v_max_f32_e32 v52, v30, v24
	v_min_f32_e32 v24, v30, v24
	v_min_f32_e32 v6, v6, v7
	v_max_f32_e32 v7, v40, v9
	v_min_f32_e32 v9, v40, v9
	v_max_f32_e32 v30, v58, v52
	v_min_f32_e32 v52, v58, v52
	v_max_f32_e32 v58, v23, v24
	v_max_f32_e32 v40, v4, v8
	v_min_f32_e32 v4, v4, v8
	v_max_f32_e32 v8, v5, v9
	v_min_f32_e32 v23, v23, v24
	v_max_f32_e32 v24, v58, v52
	v_min_f32_e32 v52, v58, v52
	v_and_b32_e32 v25, 0xffffff80, v78
	v_add_f32_e32 v10, v19, v13
	v_min_f32_e32 v5, v5, v9
	v_max_f32_e32 v9, v8, v4
	v_min_f32_e32 v4, v8, v4
	v_max_f32_e32 v8, v3, v7
	v_min_f32_e32 v3, v3, v7
	v_max_f32_e32 v7, v2, v6
	v_max_f32_e32 v58, v50, v30
	v_min_f32_e32 v30, v50, v30
	v_max_f32_e32 v50, v51, v52
	v_and_or_b32 v10, v10, s3, 8
	v_and_or_b32 v11, v11, s3, 9
	v_add_f32_e32 v13, v19, v34
	v_min_f32_e32 v2, v2, v6
	v_max_f32_e32 v6, v7, v3
	v_min_f32_e32 v3, v7, v3
	v_add_f32_e32 v32, v25, v17
	v_add_f32_e32 v53, v25, v18
	v_min_f32_e32 v51, v51, v52
	v_max_f32_e32 v52, v50, v30
	v_min_f32_e32 v30, v50, v30
	v_max_f32_e32 v50, v49, v24
	v_min_f32_e32 v24, v49, v24
	v_max_f32_e32 v49, v48, v23
	v_and_or_b32 v13, v13, s3, 10
	v_and_or_b32 v15, v15, s3, 11
	v_max_f32_e32 v7, v8, v9
	v_min_f32_e32 v8, v8, v9
	v_max_f32_e32 v9, v6, v4
	v_min_f32_e32 v4, v6, v4
	v_max_f32_e32 v6, v3, v5
	v_min_f32_e32 v3, v3, v5
	v_max_f32_e32 v5, v11, v11
	v_and_or_b32 v32, v32, s3, 32
	v_and_or_b32 v53, v53, s3, 33
	v_add_f32_e32 v54, v25, v26
	v_add_f32_e32 v55, v25, v28
	v_min_f32_e32 v23, v48, v23
	v_max_f32_e32 v48, v49, v24
	v_min_f32_e32 v24, v49, v24
	v_and_b32_e32 v27, 0xffffff80, v79
	v_and_b32_e32 v38, 0xffffff80, v0
	v_max_f32_e32 v11, v10, v5
	v_min_f32_e32 v5, v10, v5
	v_max_f32_e32 v10, v15, v15
;     __device__ __forceinline__ void fused(f32x4 (&acc)[2][2][4][2], const Unit& u, int wr, int wc, int fr, int fq, PG8_LAS unsigned char* lds, int wid, int lane) const {
;     ...
;             { float cv[16]; cv[0] = __uint_as_float((__float_as_uint(v0[0] + v1[0]) & ~255u) | 0u); cv[1] = __uint_as_float((__float_as_uint(v0[0] + v1[1]) & ~255u) | 1u); cv[2] = __uint_as_float((__float_as_uint(v0[0] + v1[2]) & ~255u) | 2u); cv[3] = __uint_as_float((__float_as_uint(v0[0] + v1[3]) & ~255u) | 3u); cv[4] = __uint_as_float((__float_as_uint(v0[0] + v1[4]) & ~255u) | 4u); cv[5] = __uint_as_float((__float_as_uint(v0[0] + v1[5]) & ~255u) | 5u); cv[6] = __uint_as_float((__float_as_uint(v0[0] + v1[6]) & ~255u) | 6u); cv[7] = __uint_as_float((__float_as_uint(v0[0] + v1[7]) & ~255u) | 7u); cv[8] = __uint_as_float((__float_as_uint(v0[0] + v1[8]) & ~255u) | 8u); cv[9] = __uint_as_float((__float_as_uint(v0[0] + v1[9]) & ~255u) | 9u); cv[10] = __uint_as_float((__float_as_uint(v0[0] + v1[10]) & ~255u) | 10u); cv[11] = __uint_as_float((__float_as_uint(v0[0] + v1[11]) & ~255u) | 11u); cv[12] = __uint_as_float((__float_as_uint(v0[0] + v1[12]) & ~255u) | 12u); cv[13] = __uint_as_float((__float_as_uint(v0[0] + v1[13]) & ~255u) | 13u); cv[14] = __uint_as_float((__float_as_uint(v0[0] + v1[14]) & ~255u) | 14u); cv[15] = __uint_as_float((__float_as_uint(v0[0] + v1[15]) & ~255u) | 15u); sort16_desc(cv);
; #pragma unroll
;               for (int q = 0; q < 16; ++q) best[q] = cv[q]; }
	v_and_or_b32 v54, v54, s3, 34
	v_and_or_b32 v55, v55, s3, 35
	v_max_f32_e32 v49, v50, v52
	v_min_f32_e32 v50, v50, v52
	v_max_f32_e32 v52, v48, v30
	v_min_f32_e32 v30, v48, v30
	v_max_f32_e32 v48, v24, v51
	v_min_f32_e32 v24, v24, v51
	v_max_f32_e32 v51, v53, v53
	v_add_f32_e32 v34, v19, v38
	v_max_f32_e32 v15, v13, v10
	v_min_f32_e32 v10, v13, v10
	v_add_f32_e32 v21, v25, v21
	v_add_f32_e32 v25, v27, v17
	v_max_f32_e32 v53, v32, v51
	v_min_f32_e32 v32, v32, v51
	v_max_f32_e32 v51, v55, v55
	v_and_or_b32 v34, v34, s3, 12
	v_and_or_b32 v36, v36, s3, 13
	v_add_f32_e32 v38, v19, v41
	v_add_f32_e32 v19, v19, v42
	v_max_f32_e32 v13, v11, v15
	v_min_f32_e32 v11, v11, v15
	v_max_f32_e32 v15, v5, v10
	v_and_or_b32 v21, v21, s3, 36
	v_and_or_b32 v25, v25, s3, 48
	v_add_f32_e32 v56, v27, v18
	v_add_f32_e32 v57, v27, v26
	v_max_f32_e32 v55, v54, v51
	v_min_f32_e32 v51, v54, v51
	v_and_or_b32 v38, v38, s3, 14
	v_and_or_b32 v19, v19, s3, 15
	v_min_f32_e32 v5, v5, v10
	v_max_f32_e32 v10, v15, v11
	v_min_f32_e32 v11, v15, v11
	v_max_f32_e32 v15, v36, v36
	v_and_or_b32 v56, v56, s3, 49
	v_and_or_b32 v57, v57, s3, 50
	v_max_f32_e32 v54, v53, v55
	v_min_f32_e32 v53, v53, v55
	v_max_f32_e32 v55, v32, v51
	v_max_f32_e32 v36, v34, v15
	v_min_f32_e32 v15, v34, v15
	v_max_f32_e32 v34, v38, v38
	v_min_f32_e32 v32, v32, v51
	v_max_f32_e32 v51, v55, v53
	v_min_f32_e32 v53, v55, v53
	v_max_f32_e32 v55, v21, v25
	v_min_f32_e32 v21, v21, v25
	v_max_f32_e32 v25, v57, v57
	v_max_f32_e32 v38, v34, v19
	v_min_f32_e32 v19, v34, v19
	v_max_f32_e32 v57, v56, v25
	v_min_f32_e32 v25, v56, v25
	v_max_f32_e32 v34, v36, v38
	v_min_f32_e32 v36, v36, v38
	v_max_f32_e32 v38, v15, v19
	v_max_f32_e32 v56, v55, v57
	v_min_f32_e32 v55, v55, v57
	v_max_f32_e32 v57, v21, v25
	v_min_f32_e32 v15, v15, v19
	v_max_f32_e32 v19, v38, v36
	v_min_f32_e32 v36, v38, v36
	v_min_f32_e32 v21, v21, v25
	v_max_f32_e32 v25, v57, v55
	v_min_f32_e32 v55, v57, v55
	v_max_f32_e32 v38, v13, v34
	v_min_f32_e32 v13, v13, v34
	v_max_f32_e32 v34, v11, v36
	v_max_f32_e32 v57, v54, v56
	v_min_f32_e32 v54, v54, v56
	v_max_f32_e32 v56, v53, v55
	v_min_f32_e32 v11, v11, v36
	v_max_f32_e32 v36, v34, v13
	v_min_f32_e32 v13, v34, v13
	v_max_f32_e32 v34, v10, v19
	v_min_f32_e32 v10, v10, v19
	v_max_f32_e32 v19, v5, v15
	v_min_f32_e32 v53, v53, v55
	v_max_f32_e32 v55, v56, v54
	v_min_f32_e32 v54, v56, v54
	v_max_f32_e32 v56, v51, v25
	v_min_f32_e32 v25, v51, v25
	v_max_f32_e32 v51, v32, v21
	v_min_f32_e32 v5, v5, v15
	v_max_f32_e32 v15, v19, v10
	v_min_f32_e32 v21, v32, v21
	v_max_f32_e32 v32, v51, v25
	v_min_f32_e32 v10, v19, v10
	v_max_f32_e32 v19, v34, v36
	v_min_f32_e32 v34, v34, v36
	v_max_f32_e32 v36, v15, v13
	v_min_f32_e32 v13, v15, v13
	v_min_f32_e32 v25, v51, v25
	v_max_f32_e32 v51, v56, v55
	v_min_f32_e32 v55, v56, v55
	v_max_f32_e32 v56, v32, v54
	v_min_f32_e32 v32, v32, v54
	v_max_f32_e32 v15, v10, v11
	v_min_f32_e32 v10, v10, v11
	v_min_f32_e32 v11, v40, v38
	v_max_f32_e32 v41, v4, v13
	v_max_f32_e32 v54, v25, v53
	v_min_f32_e32 v25, v25, v53
	v_min_f32_e32 v53, v58, v57
	v_max_f32_e32 v59, v30, v32
	v_min_f32_e32 v4, v4, v13
	v_max_f32_e32 v13, v41, v11
	v_min_f32_e32 v11, v41, v11
	v_max_f32_e32 v41, v8, v34
	v_min_f32_e32 v8, v8, v34
	v_max_f32_e32 v34, v3, v10
	v_min_f32_e32 v30, v30, v32
	v_max_f32_e32 v32, v59, v53
	v_min_f32_e32 v53, v59, v53
	v_max_f32_e32 v59, v50, v55
	v_min_f32_e32 v50, v50, v55
	v_max_f32_e32 v55, v24, v25
	v_min_f32_e32 v3, v3, v10
	v_max_f32_e32 v10, v34, v8
	v_min_f32_e32 v8, v34, v8
	v_min_f32_e32 v24, v24, v25
	v_max_f32_e32 v25, v55, v50
	v_min_f32_e32 v50, v55, v50
	v_max_f32_e32 v34, v41, v13
	v_min_f32_e32 v13, v41, v13
	v_max_f32_e32 v41, v10, v11
	v_min_f32_e32 v10, v10, v11
	v_max_f32_e32 v11, v8, v4
	v_min_f32_e32 v4, v8, v4
	v_max_f32_e32 v8, v7, v19
	v_min_f32_e32 v7, v7, v19
	v_max_f32_e32 v19, v6, v15
	v_max_f32_e32 v55, v59, v32
	v_min_f32_e32 v32, v59, v32
	v_max_f32_e32 v59, v25, v53
	v_min_f32_e32 v25, v25, v53
	v_max_f32_e32 v53, v50, v30
	v_min_f32_e32 v30, v50, v30
	v_max_f32_e32 v50, v49, v51
	v_min_f32_e32 v49, v49, v51
	v_max_f32_e32 v51, v48, v54
	v_min_f32_e32 v6, v6, v15
	v_max_f32_e32 v15, v19, v7
	v_min_f32_e32 v7, v19, v7
	v_max_f32_e32 v19, v9, v36
	v_min_f32_e32 v9, v9, v36
	v_max_f32_e32 v36, v2, v5
	v_min_f32_e32 v48, v48, v54
	v_max_f32_e32 v54, v51, v49
	v_min_f32_e32 v49, v51, v49
	v_max_f32_e32 v51, v52, v56
	v_min_f32_e32 v52, v52, v56
	v_max_f32_e32 v56, v23, v21
	v_min_f32_e32 v2, v2, v5
	v_max_f32_e32 v5, v36, v9
	v_min_f32_e32 v9, v36, v9
	v_max_f32_e32 v36, v19, v15
	v_min_f32_e32 v21, v23, v21
	v_max_f32_e32 v23, v56, v52
	v_min_f32_e32 v52, v56, v52
	v_and_b32_e32 v20, 0xffffff80, v72
	v_min_f32_e32 v15, v19, v15
	v_max_f32_e32 v19, v5, v7
	v_min_f32_e32 v5, v5, v7
	v_max_f32_e32 v7, v9, v6
	v_min_f32_e32 v6, v9, v6
	v_min_f32_e32 v9, v8, v34
	v_min_f32_e32 v42, v36, v13
	v_max_f32_e32 v56, v51, v54
	v_min_f32_e32 v51, v51, v54
	v_max_f32_e32 v54, v23, v49
	v_min_f32_e32 v23, v23, v49
	v_max_f32_e32 v49, v52, v48
	v_min_f32_e32 v48, v52, v48
	v_and_b32_e32 v39, 0xffffff80, v65
	v_min_f32_e32 v65, v48, v24
	v_max3_f32 v9, v9, v48, v24
	v_max3_f32 v24, v42, v49, v30
	v_add_f32_e32 v27, v27, v28
	v_add_f32_e32 v28, v20, v17
	v_add_f32_e32 v42, v20, v18
	v_add_f32_e32 v20, v20, v26
	v_and_b32_e32 v22, 0xffffff80, v73
	v_and_or_b32 v27, v27, s3, 51
	v_and_or_b32 v28, v28, s3, 64
	v_and_b32_e32 v42, 0xffffff00, v42
	v_and_b32_e32 v20, 0xffffff00, v20
	v_and_b32_e32 v29, 0xffffff80, v74
	v_and_b32_e32 v31, 0xffffff80, v75
	v_and_b32_e32 v33, 0xffffff80, v70
	v_and_b32_e32 v35, 0xffffff80, v71
	v_and_b32_e32 v37, 0xffffff80, v64
;     __device__ __forceinline__ void fused(f32x4 (&acc)[2][2][4][2], const Unit& u, int wr, int wc, int fr, int fq, PG8_LAS unsigned char* lds, int wid, int lane) const {
;     ...
;             { float cv[16]; cv[0] = __uint_as_float((__float_as_uint(v0[1] + v1[0]) & ~255u) | 16u); cv[1] = __uint_as_float((__float_as_uint(v0[1] + v1[1]) & ~255u) | 17u); cv[2] = __uint_as_float((__float_as_uint(v0[1] + v1[2]) & ~255u) | 18u); cv[3] = __uint_as_float((__float_as_uint(v0[1] + v1[3]) & ~255u) | 19u); cv[4] = __uint_as_float((__float_as_uint(v0[1] + v1[4]) & ~255u) | 20u); cv[5] = __uint_as_float((__float_as_uint(v0[1] + v1[5]) & ~255u) | 21u); cv[6] = __uint_as_float((__float_as_uint(v0[1] + v1[6]) & ~255u) | 22u); cv[7] = __uint_as_float((__float_as_uint(v0[1] + v1[7]) & ~255u) | 23u); cv[8] = __uint_as_float((__float_as_uint(v0[2] + v1[0]) & ~255u) | 32u); cv[9] = __uint_as_float((__float_as_uint(v0[2] + v1[1]) & ~255u) | 33u); cv[10] = __uint_as_float((__float_as_uint(v0[2] + v1[2]) & ~255u) | 34u); cv[11] = __uint_as_float((__float_as_uint(v0[2] + v1[3]) & ~255u) | 35u); cv[12] = __uint_as_float((__float_as_uint(v0[2] + v1[4]) & ~255u) | 36u); cv[13] = __uint_as_float((__float_as_uint(v0[3] + v1[0]) & ~255u) | 48u); cv[14] = __uint_as_float((__float_as_uint(v0[3] + v1[1]) & ~255u) | 49u); cv[15] = __uint_as_float((__float_as_uint(v0[3] + v1[2]) & ~255u) | 50u); sort16_desc(cv); merge_top16(best, cv); }
	v_min_f32_e32 v43, v15, v41
	v_min_f32_e32 v44, v19, v10
	v_min_f32_e32 v62, v54, v25
	v_or_b32_e32 v42, 0x41, v42
	v_or_b32_e32 v20, 0x42, v20
	v_add_f32_e32 v26, v22, v17
	v_add_f32_e32 v22, v22, v18
	v_min_f32_e32 v63, v23, v53
	v_max3_f32 v23, v43, v23, v53
	v_max3_f32 v10, v19, v10, v62
	v_max3_f32 v19, v44, v54, v25
	v_and_b32_e32 v26, 0xffffff00, v26
	v_and_b32_e32 v22, 0xffffff00, v22
	v_add_f32_e32 v43, v29, v17
	v_add_f32_e32 v29, v29, v18
	v_add_f32_e32 v44, v31, v17
	v_add_f32_e32 v18, v31, v18
	v_add_f32_e32 v31, v33, v17
	v_add_f32_e32 v33, v35, v17
	v_add_f32_e32 v35, v37, v17
	v_add_f32_e32 v37, v39, v17
	v_max_f32_e32 v39, v27, v28
	v_min_f32_e32 v27, v27, v28
	v_max_f32_e32 v28, v42, v42
	v_or_b32_e32 v26, 0x50, v26
	v_or_b32_e32 v22, 0x51, v22
	v_and_b32_e32 v43, 0xffffff00, v43
	v_and_b32_e32 v29, 0xffffff00, v29
	v_max_f32_e32 v42, v28, v20
	v_min_f32_e32 v20, v28, v20
	v_or_b32_e32 v43, 0x60, v43
	v_or_b32_e32 v29, 0x61, v29
	v_max_f32_e32 v28, v39, v42
	v_min_f32_e32 v39, v39, v42
	v_max_f32_e32 v42, v27, v20
	v_min_f32_e32 v20, v27, v20
	v_max_f32_e32 v27, v42, v39
	v_min_f32_e32 v39, v42, v39
	v_max_f32_e32 v42, v26, v22
	v_min_f32_e32 v22, v26, v22
	v_max_f32_e32 v26, v29, v29
	v_max_f32_e32 v29, v43, v43
	v_max_f32_e32 v43, v29, v26
	v_min_f32_e32 v26, v29, v26
	v_max_f32_e32 v29, v42, v43
	v_min_f32_e32 v42, v42, v43
	v_max_f32_e32 v43, v22, v26
	v_and_b32_e32 v12, 0xffffff80, v68
	v_and_b32_e32 v14, 0xffffff80, v69
	v_min_f32_e32 v22, v22, v26
	v_max_f32_e32 v26, v43, v42
	v_min_f32_e32 v42, v43, v42
	v_add_f32_e32 v12, v12, v17
	v_add_f32_e32 v14, v14, v17
	v_max_f32_e32 v43, v28, v29
	v_min_f32_e32 v28, v28, v29
	v_max_f32_e32 v29, v39, v42
	v_and_b32_e32 v44, 0xffffff00, v44
	v_and_b32_e32 v18, 0xffffff00, v18
	v_and_b32_e32 v12, 0xffffff00, v12
	v_and_b32_e32 v14, 0xffffff00, v14
	v_min_f32_e32 v39, v39, v42
	v_max_f32_e32 v42, v29, v28
	v_min_f32_e32 v28, v29, v28
	v_max_f32_e32 v29, v27, v26
	v_min_f32_e32 v26, v27, v26
	v_max_f32_e32 v27, v20, v22
	v_or_b32_e32 v44, 0x70, v44
	v_or_b32_e32 v18, 0x71, v18
	v_or_b32_e32 v12, 0x80, v12
	v_or_b32_e32 v14, 0x90, v14
	v_min_f32_e32 v20, v20, v22
	v_max_f32_e32 v22, v27, v26
	v_min_f32_e32 v26, v27, v26
	v_and_b32_e32 v31, 0xffffff00, v31
	v_and_b32_e32 v33, 0xffffff00, v33
	v_max_f32_e32 v27, v29, v42
	v_min_f32_e32 v29, v29, v42
	v_max_f32_e32 v42, v22, v28
	v_min_f32_e32 v22, v22, v28
	v_max_f32_e32 v28, v26, v39
	v_min_f32_e32 v26, v26, v39
	v_max_f32_e32 v39, v44, v44
	v_or_b32_e32 v31, 0xa0, v31
	v_or_b32_e32 v33, 0xb0, v33
	v_and_b32_e32 v35, 0xffffff00, v35
	v_and_b32_e32 v37, 0xffffff00, v37
	v_max_f32_e32 v44, v39, v18
	v_min_f32_e32 v18, v39, v18
	v_max_f32_e32 v39, v12, v14
	v_min_f32_e32 v12, v12, v14
	v_or_b32_e32 v35, 0xc0, v35
	v_or_b32_e32 v37, 0xd0, v37
	v_max_f32_e32 v14, v44, v39
	v_min_f32_e32 v39, v44, v39
	v_max_f32_e32 v44, v18, v12
	v_min_f32_e32 v12, v18, v12
	v_max_f32_e32 v18, v44, v39
	v_min_f32_e32 v39, v44, v39
	v_max_f32_e32 v44, v31, v33
	v_min_f32_e32 v31, v31, v33
	v_max_f32_e32 v33, v37, v37
	v_max_f32_e32 v37, v35, v33
	v_min_f32_e32 v33, v35, v33
	v_max_f32_e32 v35, v44, v37
	v_min_f32_e32 v37, v44, v37
	v_max_f32_e32 v44, v31, v33
	v_min_f32_e32 v31, v31, v33
	v_max_f32_e32 v33, v44, v37
	v_min_f32_e32 v37, v44, v37
	v_max_f32_e32 v44, v14, v35
	v_min_f32_e32 v14, v14, v35
	v_max_f32_e32 v35, v39, v37
	v_min_f32_e32 v37, v39, v37
	v_max_f32_e32 v39, v35, v14
	v_min_f32_e32 v14, v35, v14
	v_max_f32_e32 v35, v18, v33
	v_min_f32_e32 v18, v18, v33
	v_max_f32_e32 v33, v12, v31
	v_min_f32_e32 v12, v12, v31
	v_max_f32_e32 v31, v33, v18
	v_min_f32_e32 v45, v5, v11
	v_min_f32_e32 v61, v51, v59
	v_min_f32_e32 v18, v33, v18
	v_max_f32_e32 v33, v35, v39
	v_min_f32_e32 v35, v35, v39
	v_max_f32_e32 v39, v31, v14
	v_min_f32_e32 v14, v31, v14
	v_max3_f32 v5, v5, v11, v61
	v_max3_f32 v11, v45, v51, v59
	v_max_f32_e32 v31, v18, v37
	v_min_f32_e32 v18, v18, v37
	v_min_f32_e32 v37, v43, v44
	v_max_f32_e32 v45, v22, v14
	v_min_f32_e32 v14, v22, v14
	v_max_f32_e32 v22, v45, v37
	v_min_f32_e32 v37, v45, v37
	v_max_f32_e32 v45, v29, v35
	v_min_f32_e32 v29, v29, v35
	v_max_f32_e32 v35, v26, v18
	v_min_f32_e32 v46, v7, v4
	v_min_f32_e32 v47, v6, v3
	v_min_f32_e32 v52, v50, v55
	v_min_f32_e32 v60, v56, v32
	v_min_f32_e32 v64, v49, v30
	v_min_f32_e32 v18, v26, v18
	v_max_f32_e32 v26, v35, v29
	v_min_f32_e32 v29, v35, v29
	v_max3_f32 v21, v40, v38, v21
	v_max3_f32 v8, v8, v34, v65
	v_max3_f32 v13, v36, v13, v64
	v_max3_f32 v15, v15, v41, v63
	v_max3_f32 v4, v7, v4, v60
	v_max3_f32 v7, v46, v56, v32
	v_max3_f32 v3, v6, v3, v52
	v_max3_f32 v6, v47, v50, v55
	v_max3_f32 v2, v2, v58, v57
	v_max_f32_e32 v35, v45, v22
	v_min_f32_e32 v22, v45, v22
	v_max_f32_e32 v45, v26, v37
	v_min_f32_e32 v26, v26, v37
	v_max_f32_e32 v37, v29, v14
	v_min_f32_e32 v14, v29, v14
	v_max_f32_e32 v29, v27, v33
	v_min_f32_e32 v27, v27, v33
	v_max_f32_e32 v33, v28, v31
	v_max_f32_e32 v25, v21, v19
	v_min_f32_e32 v19, v21, v19
	v_max_f32_e32 v21, v8, v5
	v_min_f32_e32 v5, v8, v5
	v_max_f32_e32 v8, v9, v11
	v_min_f32_e32 v9, v9, v11
	v_max_f32_e32 v11, v13, v4
	v_min_f32_e32 v4, v13, v4
	v_max_f32_e32 v13, v24, v7
	v_min_f32_e32 v7, v24, v7
	v_max_f32_e32 v24, v15, v3
	v_min_f32_e32 v3, v15, v3
	v_max_f32_e32 v15, v23, v6
	v_min_f32_e32 v6, v23, v6
	v_max_f32_e32 v23, v10, v2
	v_min_f32_e32 v2, v10, v2
	v_min_f32_e32 v28, v28, v31
	v_max_f32_e32 v31, v33, v27
	v_min_f32_e32 v27, v33, v27
	v_max_f32_e32 v33, v42, v39
	v_min_f32_e32 v39, v42, v39
	v_max_f32_e32 v42, v20, v12
	v_max_f32_e32 v10, v25, v13
	v_min_f32_e32 v13, v25, v13
	v_max_f32_e32 v25, v21, v24
	v_min_f32_e32 v21, v21, v24
; __device__ __forceinline__ void merge_top16(float (&v)[16], const float (&nw)[16]) {
;     v[0] = fmaxf(v[0], nw[15]); v[1] = fmaxf(v[1], nw[14]); v[2] = fmaxf(v[2], nw[13]); v[3] = fmaxf(v[3], nw[12]); v[4] = fmaxf(v[4], nw[11]); v[5] = fmaxf(v[5], nw[10]); v[6] = fmaxf(v[6], nw[9]); v[7] = fmaxf(v[7], nw[8]); v[8] = fmaxf(v[8], nw[7]); v[9] = fmaxf(v[9], nw[6]); v[10] = fmaxf(v[10], nw[5]); v[11] = fmaxf(v[11], nw[4]); v[12] = fmaxf(v[12], nw[3]); v[13] = fmaxf(v[13], nw[2]); v[14] = fmaxf(v[14], nw[1]); v[15] = fmaxf(v[15], nw[0]);
;     CE(v[0], v[8]); CE(v[1], v[9]); CE(v[2], v[10]); CE(v[3], v[11]);
;     CE(v[4], v[12]); CE(v[5], v[13]); CE(v[6], v[14]); CE(v[7], v[15]);
;     CE(v[0], v[4]); CE(v[1], v[5]); CE(v[2], v[6]); CE(v[3], v[7]);
;     CE(v[8], v[12]); CE(v[9], v[13]); CE(v[10], v[14]); CE(v[11], v[15]);
;     CE(v[0], v[2]); CE(v[1], v[3]); CE(v[4], v[6]); CE(v[5], v[7]);
;     CE(v[8], v[10]); CE(v[9], v[11]); CE(v[12], v[14]); CE(v[13], v[15]);
;     __device__ __forceinline__ void fused(f32x4 (&acc)[2][2][4][2], const Unit& u, int wr, int wc, int fr, int fq, PG8_LAS unsigned char* lds, int wid, int lane) const {
;     ...
;             { float cv[16]; cv[0] = __uint_as_float((__float_as_uint(v0[14] + v1[0]) & ~255u) | 224u); cv[1] = __uint_as_float((__float_as_uint(v0[15] + v1[0]) & ~255u) | 240u); cv[2] = -INFINITY; cv[3] = -INFINITY; cv[4] = -INFINITY; cv[5] = -INFINITY; cv[6] = -INFINITY; cv[7] = -INFINITY; cv[8] = -INFINITY; cv[9] = -INFINITY; cv[10] = -INFINITY; cv[11] = -INFINITY; cv[12] = -INFINITY; cv[13] = -INFINITY; cv[14] = -INFINITY; cv[15] = -INFINITY; sort16_desc(cv); merge_top16(best, cv); }
;             float sc[16], sum = 0.f;
; #pragma unroll
;             for (int q = 0; q < 16; ++q) { sc[q] = __uint_as_float(__float_as_uint(best[q]) & ~255u); }
;             const float smax = sc[0];
; #pragma unroll
;             for (int q = 0; q < 16; ++q) { sc[q] = __builtin_amdgcn_exp2f((sc[q] - smax) * 1.4426950408889634f); }
; #pragma unroll
;             for (int q = 0; q < 16; ++q) sum += sc[q];
;             const float rs = 1.0f / sum;
;             asm volatile("s_waitcnt lgkmcnt(0)" ::: "memory");
;             int ex[16];
; #pragma unroll
;             for (int q = 0; q < 16; ++q) { const unsigned cid = __float_as_uint(best[q]) & 255u; ex[q] = idxl[cid >> 4] * 128 + idxl[16 + (cid & 15u)]; }
	v_max_f32_e32 v24, v8, v15
	v_min_f32_e32 v8, v8, v15
	v_max_f32_e32 v15, v11, v23
	v_min_f32_e32 v11, v11, v23
	v_max_f32_e32 v23, v19, v7
	v_min_f32_e32 v7, v19, v7
	v_max_f32_e32 v19, v5, v3
	v_min_f32_e32 v3, v5, v3
	v_max_f32_e32 v5, v9, v6
	v_min_f32_e32 v6, v9, v6
	v_max_f32_e32 v9, v4, v2
	v_min_f32_e32 v2, v4, v2
	v_min_f32_e32 v12, v20, v12
	v_max_f32_e32 v20, v42, v39
	v_min_f32_e32 v39, v42, v39
	v_and_b32_e32 v1, 0xffffff80, v66
	v_and_b32_e32 v0, 0xffffff80, v67
	v_max_f32_e32 v4, v10, v24
	v_min_f32_e32 v10, v10, v24
	v_max_f32_e32 v24, v25, v15
	v_min_f32_e32 v15, v25, v15
	v_max_f32_e32 v25, v13, v8
	v_min_f32_e32 v8, v13, v8
	v_max_f32_e32 v13, v21, v11
	v_min_f32_e32 v11, v21, v11
	v_max_f32_e32 v21, v23, v5
	v_min_f32_e32 v5, v23, v5
	v_max_f32_e32 v23, v19, v9
	v_min_f32_e32 v9, v19, v9
	v_max_f32_e32 v19, v7, v6
	v_min_f32_e32 v6, v7, v6
	v_max_f32_e32 v7, v3, v2
	v_min_f32_e32 v2, v3, v2
	v_max_f32_e32 v42, v33, v31
	v_min_f32_e32 v31, v33, v31
	v_max_f32_e32 v33, v20, v27
	v_min_f32_e32 v20, v20, v27
	v_max_f32_e32 v27, v39, v28
	v_min_f32_e32 v28, v39, v28
	v_min_f32_e32 v3, v4, v24
	v_min_f32_e32 v30, v10, v15
	v_min_f32_e32 v32, v25, v13
	v_min_f32_e32 v34, v8, v11
	v_min_f32_e32 v36, v21, v23
	v_min_f32_e32 v38, v5, v9
	v_min_f32_e32 v40, v19, v7
	v_min_f32_e32 v41, v6, v2
	v_max_f32_e32 v39, v29, v35
	v_min_f32_e32 v29, v29, v35
	v_max_f32_e32 v35, v42, v22
	v_min_f32_e32 v22, v42, v22
	v_max_f32_e32 v42, v31, v45
	v_min_f32_e32 v31, v31, v45
	v_max_f32_e32 v45, v33, v26
	v_min_f32_e32 v26, v33, v26
	v_max_f32_e32 v33, v20, v37
	v_min_f32_e32 v20, v20, v37
	v_max_f32_e32 v37, v27, v14
	v_min_f32_e32 v14, v27, v14
	v_max_f32_e32 v27, v28, v18
	v_min_f32_e32 v18, v28, v18
	v_add_f32_e32 v1, v1, v17
	v_add_f32_e32 v0, v0, v17
	v_max3_f32 v4, v4, v24, v12
	v_max_f32_e32 v3, v3, v18
	v_max3_f32 v10, v10, v15, v27
	v_max_f32_e32 v12, v30, v14
	v_max3_f32 v13, v25, v13, v37
	v_max_f32_e32 v14, v32, v20
	v_max3_f32 v8, v8, v11, v33
	v_max_f32_e32 v11, v34, v26
	v_max3_f32 v15, v21, v23, v45
	v_max_f32_e32 v18, v36, v31
	v_max3_f32 v5, v5, v9, v42
	v_max_f32_e32 v9, v38, v22
	v_max3_f32 v7, v19, v7, v35
	v_max_f32_e32 v19, v40, v29
	v_max3_f32 v2, v6, v2, v39
	v_max3_f32 v6, v41, v43, v44
	v_and_b32_e32 v1, 0xffffff00, v1
	v_and_b32_e32 v0, 0xffffff00, v0
	v_max_f32_e32 v20, v4, v15
	v_min_f32_e32 v4, v4, v15
	v_max_f32_e32 v15, v3, v18
	v_min_f32_e32 v3, v3, v18
	v_max_f32_e32 v18, v10, v5
	v_min_f32_e32 v5, v10, v5
	v_max_f32_e32 v10, v12, v9
	v_min_f32_e32 v9, v12, v9
	v_max_f32_e32 v12, v13, v7
	v_min_f32_e32 v7, v13, v7
	v_max_f32_e32 v13, v14, v19
	v_min_f32_e32 v14, v14, v19
	v_max_f32_e32 v19, v8, v2
	v_min_f32_e32 v2, v8, v2
	v_max_f32_e32 v8, v11, v6
	v_min_f32_e32 v6, v11, v6
	v_or_b32_e32 v1, 0xe0, v1
	v_or_b32_e32 v0, 0xf0, v0
	v_max_f32_e32 v11, v20, v12
	v_min_f32_e32 v12, v20, v12
	v_max_f32_e32 v20, v15, v13
	v_min_f32_e32 v13, v15, v13
	v_max_f32_e32 v15, v18, v19
	v_min_f32_e32 v18, v18, v19
	v_max_f32_e32 v19, v10, v8
	v_min_f32_e32 v8, v10, v8
	v_max_f32_e32 v10, v4, v7
	v_min_f32_e32 v4, v4, v7
	v_max_f32_e32 v7, v3, v14
	v_min_f32_e32 v3, v3, v14
	v_max_f32_e32 v14, v5, v2
	v_min_f32_e32 v2, v5, v2
	v_max_f32_e32 v5, v9, v6
	v_min_f32_e32 v6, v9, v6
	v_max_f32_e32 v9, v11, v15
	v_min_f32_e32 v11, v11, v15
	v_max_f32_e32 v15, v20, v19
	v_min_f32_e32 v19, v20, v19
	v_max_f32_e32 v20, v12, v18
	v_min_f32_e32 v12, v12, v18
	v_max_f32_e32 v18, v13, v8
	v_min_f32_e32 v8, v13, v8
	v_max_f32_e32 v13, v10, v14
	v_min_f32_e32 v10, v10, v14
	v_max_f32_e32 v14, v7, v5
	v_min_f32_e32 v5, v7, v5
	v_max_f32_e32 v7, v4, v2
	v_min_f32_e32 v2, v4, v2
	v_max_f32_e32 v4, v3, v6
	v_min_f32_e32 v3, v3, v6
	v_max_f32_e32 v17, v1, v0
	v_min_f32_e32 v0, v1, v0
	v_min_f32_e32 v6, v9, v15
	v_min_f32_e32 v21, v11, v19
	v_min_f32_e32 v22, v20, v18
	v_min_f32_e32 v23, v12, v8
	v_min_f32_e32 v24, v13, v14
	v_min_f32_e32 v25, v10, v5
	v_min_f32_e32 v26, v7, v4
	v_min_f32_e32 v27, v2, v3
	s_mov_b32 s3, 0xff800000
	v_max_f32_e32 v0, 0xff800000, v0
	v_max3_f32 v1, v9, v15, s3
	v_max_f32_e32 v6, 0xff800000, v6
	v_max3_f32 v9, v11, v19, s3
	v_max_f32_e32 v11, 0xff800000, v21
	v_max3_f32 v15, v20, v18, s3
	v_max_f32_e32 v18, 0xff800000, v22
	v_max3_f32 v8, v12, v8, s3
	v_max_f32_e32 v12, 0xff800000, v23
	v_max3_f32 v13, v13, v14, s3
	v_max_f32_e32 v14, 0xff800000, v24
	v_max3_f32 v5, v10, v5, s3
	v_max_f32_e32 v10, 0xff800000, v25
	v_max3_f32 v4, v7, v4, s3
	v_max_f32_e32 v7, 0xff800000, v26
	v_max3_f32 v0, v2, v3, v0
	v_max3_f32 v2, v27, v17, s3
	v_max_f32_e32 v3, v1, v13
	v_min_f32_e32 v1, v1, v13
	v_max_f32_e32 v13, v6, v14
	v_min_f32_e32 v6, v6, v14
	v_max_f32_e32 v14, v9, v5
	v_min_f32_e32 v5, v9, v5
	v_max_f32_e32 v9, v11, v10
	v_min_f32_e32 v10, v11, v10
	v_max_f32_e32 v11, v15, v4
	v_min_f32_e32 v4, v15, v4
	v_max_f32_e32 v15, v18, v7
	v_max_f32_e32 v17, v8, v0
	v_min_f32_e32 v0, v8, v0
	v_max_f32_e32 v8, v12, v2
	v_min_f32_e32 v2, v12, v2
	v_max_f32_e32 v12, v3, v11
	v_min_f32_e32 v3, v3, v11
	v_max_f32_e32 v11, v13, v15
	v_min_f32_e32 v13, v13, v15
	v_max_f32_e32 v15, v14, v17
	v_min_f32_e32 v14, v14, v17
	v_max_f32_e32 v17, v9, v8
	v_min_f32_e32 v8, v9, v8
	v_max_f32_e32 v9, v1, v4
	v_min_f32_e32 v24, v1, v4
	v_max_f32_e32 v27, v5, v0
	v_min_f32_e32 v28, v5, v0
	v_max_f32_e32 v29, v10, v2
	v_min_f32_e32 v30, v10, v2
	v_max_f32_e32 v0, v12, v15
	v_min_f32_e32 v1, v12, v15
	v_max_f32_e32 v2, v11, v17
	v_min_f32_e32 v4, v11, v17
	v_min_f32_e32 v7, v18, v7
	v_max_f32_e32 v33, v0, v2
	v_min_f32_e32 v34, v0, v2
	v_min_f32_e32 v36, v1, v4
	v_max_f32_e32 v25, v6, v7
	v_min_f32_e32 v26, v6, v7
	v_max_f32_e32 v35, v1, v4
	v_lshrrev_b32_e32 v0, 2, v33
	v_lshrrev_b32_e32 v2, 2, v34
	v_lshrrev_b32_e32 v6, 2, v36
	v_max_f32_e32 v17, v3, v14
	v_min_f32_e32 v31, v3, v14
	v_and_b32_e32 v0, 60, v0
	v_and_b32_e32 v1, 15, v33
	v_and_b32_e32 v2, 60, v2
	v_and_b32_e32 v3, 15, v34
	v_lshrrev_b32_e32 v4, 2, v35
	v_and_b32_e32 v5, 15, v35
	v_and_b32_e32 v6, 60, v6
	v_and_b32_e32 v7, 15, v36
	s_waitcnt lgkmcnt(0)
; #define RT_PK(q_) (ex[q_] | (int)((__float_as_uint(usc[ex[q_]]) >> 23) << 14))
;     __device__ __forceinline__ void fused(f32x4 (&acc)[2][2][4][2], const Unit& u, int wr, int wc, int fr, int fq, PG8_LAS unsigned char* lds, int wid, int lane) const {
;     ...
;             float sc[16], sum = 0.f;
; #pragma unroll
;             for (int q = 0; q < 16; ++q) { sc[q] = __uint_as_float(__float_as_uint(best[q]) & ~255u); }
;             const float smax = sc[0];
; #pragma unroll
;             for (int q = 0; q < 16; ++q) { sc[q] = __builtin_amdgcn_exp2f((sc[q] - smax) * 1.4426950408889634f); }
; #pragma unroll
;             for (int q = 0; q < 16; ++q) sum += sc[q];
;             const float rs = 1.0f / sum;
;             asm volatile("s_waitcnt lgkmcnt(0)" ::: "memory");
;             int ex[16];
; #pragma unroll
;             for (int q = 0; q < 16; ++q) { const unsigned cid = __float_as_uint(best[q]) & 255u; ex[q] = idxl[cid >> 4] * 128 + idxl[16 + (cid & 15u)]; }
;             const size_t o = ((size_t)u.pn * 16384 + (size_t)(u.pm * BM + row)) * 16;
;             typedef int i32x4 __attribute__((ext_vector_type(4)));
; #pragma unroll
;             for (int i = 0; i < 4; ++i) {
;     ...
;                 *(i32x4*)(eidx + o + 4 * i) = (i32x4){RT_PK(4 * i), RT_PK(4 * i + 1), RT_PK(4 * i + 2), RT_PK(4 * i + 3)};
;                 *(f32x4*)(egate + o + 4 * i) = (f32x4){sc[4 * i] * rs * vsc[ex[4 * i]], sc[4 * i + 1] * rs * vsc[ex[4 * i + 1]], sc[4 * i + 2] * rs * vsc[ex[4 * i + 2]], sc[4 * i + 3] * rs * vsc[ex[4 * i + 3]]};
	v_add_u32_e32 v0, v16, v0
	v_lshl_add_u32 v1, v1, 2, v16
	v_add_u32_e32 v2, v16, v2
	v_lshl_add_u32 v3, v3, 2, v16
	v_and_b32_e32 v4, 60, v4
	v_lshl_add_u32 v5, v5, 2, v16
	v_add_u32_e32 v6, v16, v6
	v_lshl_add_u32 v7, v7, 2, v16
	v_add_u32_e32 v4, v16, v4
	ds_read_b32 v0, v0
	ds_read_b32 v1, v1 offset:64
	ds_read_b32 v2, v2
	ds_read_b32 v3, v3 offset:64
	ds_read_b32 v10, v4
	ds_read_b32 v5, v5 offset:64
	ds_read_b32 v6, v6
	ds_read_b32 v7, v7 offset:64
	s_waitcnt lgkmcnt(0)
	v_lshl_add_u32 v0, v0, 7, v1
	v_ashrrev_i32_e32 v1, 31, v0
	v_lshl_add_u32 v4, v2, 7, v3
	v_lshlrev_b64 v[14:15], 3, v[0:1]
	v_lshl_add_u32 v10, v10, 7, v5
	v_lshl_add_u32 v12, v6, 7, v7
	v_lshl_add_u64 v[2:3], s[8:9], 0, v[14:15]
	v_ashrrev_i32_e32 v5, 31, v4
	v_max_f32_e32 v32, v13, v8
	v_min_f32_e32 v8, v13, v8
	global_load_dwordx2 v[170:171], v[2:3], off
	v_lshlrev_b64 v[18:19], 3, v[4:5]
	v_ashrrev_i32_e32 v11, 31, v10
	v_ashrrev_i32_e32 v13, 31, v12
	v_lshl_add_u64 v[2:3], s[8:9], 0, v[18:19]
	v_lshlrev_b64 v[20:21], 3, v[10:11]
	v_lshlrev_b64 v[22:23], 3, v[12:13]
	v_lshl_add_u64 v[6:7], s[8:9], 0, v[20:21]
	global_load_dwordx2 v[172:173], v[2:3], off
	global_load_dwordx2 v[174:175], v[6:7], off
	v_lshl_add_u64 v[2:3], s[8:9], 0, v[22:23]
	global_load_dwordx2 v[176:177], v[2:3], off
	v_min_f32_e32 v2, v9, v27
	v_min_f32_e32 v6, v25, v29
	v_max_f32_e32 v43, v2, v6
	v_min_f32_e32 v44, v2, v6
	v_and_b32_e32 v2, 0xffffff00, v34
	v_and_b32_e32 v51, 0xffffff00, v33
	v_max_f32_e32 v37, v9, v27
	v_max_f32_e32 v3, v25, v29
	v_sub_f32_e32 v2, v2, v51
	v_min_f32_e32 v9, v24, v28
	v_min_f32_e32 v25, v26, v30
	v_max_f32_e32 v41, v37, v3
	v_min_f32_e32 v42, v37, v3
	v_and_b32_e32 v3, 0xffffff00, v35
	v_mul_f32_e32 v2, 0x3fb8aa3b, v2
	v_max_f32_e32 v47, v9, v25
	v_min_f32_e32 v48, v9, v25
	v_exp_f32_e32 v25, v2
	v_sub_f32_e32 v2, v3, v51
	v_and_b32_e32 v6, 0xffffff00, v36
	v_mul_f32_e32 v2, 0x3fb8aa3b, v2
	v_max_f32_e32 v7, v24, v28
	v_max_f32_e32 v24, v26, v30
	v_max_f32_e32 v38, v17, v32
	v_exp_f32_e32 v26, v2
	v_sub_f32_e32 v2, v6, v51
	v_max_f32_e32 v45, v7, v24
	v_min_f32_e32 v46, v7, v24
	v_and_b32_e32 v7, 0xffffff00, v38
	v_mul_f32_e32 v2, 0x3fb8aa3b, v2
	v_min_f32_e32 v17, v17, v32
	v_exp_f32_e32 v27, v2
	v_sub_f32_e32 v2, v7, v51
	v_max_f32_e32 v39, v31, v8
	v_min_f32_e32 v40, v31, v8
	v_and_b32_e32 v8, 0xffffff00, v17
	v_mul_f32_e32 v2, 0x3fb8aa3b, v2
	v_exp_f32_e32 v28, v2
	v_sub_f32_e32 v2, v8, v51
	v_and_b32_e32 v9, 0xffffff00, v39
	v_mul_f32_e32 v2, 0x3fb8aa3b, v2
	v_exp_f32_e32 v29, v2
	v_sub_f32_e32 v2, v9, v51
	v_and_b32_e32 v31, 0xffffff00, v40
	v_mul_f32_e32 v2, 0x3fb8aa3b, v2
	v_exp_f32_e32 v30, v2
	v_sub_f32_e32 v2, v31, v51
	v_and_b32_e32 v32, 0xffffff00, v41
	v_mul_f32_e32 v2, 0x3fb8aa3b, v2
	v_exp_f32_e32 v31, v2
	v_sub_f32_e32 v2, v32, v51
	v_and_b32_e32 v34, 0xffffff00, v42
	v_mul_f32_e32 v2, 0x3fb8aa3b, v2
	v_exp_f32_e32 v6, v2
	v_sub_f32_e32 v2, v34, v51
	v_and_b32_e32 v35, 0xffffff00, v43
	v_mul_f32_e32 v2, 0x3fb8aa3b, v2
	v_exp_f32_e32 v7, v2
	v_sub_f32_e32 v2, v35, v51
	v_mul_f32_e32 v2, 0x3fb8aa3b, v2
	v_exp_f32_e32 v8, v2
	v_lshl_or_b32 v2, s18, 8, v128
	v_ashrrev_i32_e32 v3, 31, v2
	s_lshl_b64 s[4:5], s[16:17], 18
	s_mov_b32 s3, 0x7fc000
	v_lshl_add_u64 v[32:33], v[2:3], 4, s[4:5]
	v_sub_f32_e32 v24, v51, v51
	v_mul_f32_e32 v24, 0x3fb8aa3b, v24
	v_exp_f32_e32 v24, v24
	s_waitcnt vmcnt(0)
	v_lshrrev_b32_e32 v1, 9, v170
	v_and_or_b32 v2, v1, s3, v0
	v_and_b32_e32 v36, 0xffffff00, v44
	v_and_b32_e32 v37, 0xffffff00, v45
	v_and_b32_e32 v49, 0xffffff00, v46
	v_and_b32_e32 v50, 0xffffff00, v47
	v_and_b32_e32 v52, 0xffffff00, v48
	v_lshrrev_b32_e32 v0, 9, v172
	v_and_or_b32 v3, v0, s3, v4
	v_lshrrev_b32_e32 v0, 9, v174
	v_and_or_b32 v4, v0, s3, v10
	v_lshrrev_b32_e32 v0, 9, v176
	v_and_or_b32 v5, v0, s3, v12
	v_lshlrev_b64 v[12:13], 2, v[32:33]
	v_lshl_add_u64 v[0:1], s[12:13], 0, v[12:13]
	global_store_dwordx4 v[0:1], v[2:5], off
	v_lshrrev_b32_e32 v32, 2, v40
	v_add_f32_e32 v10, 0, v24
	v_add_f32_e32 v10, v25, v10
	v_add_f32_e32 v10, v26, v10
	v_add_f32_e32 v10, v27, v10
	v_sub_f32_e32 v2, v36, v51
	v_add_f32_e32 v10, v28, v10
	v_mul_f32_e32 v2, 0x3fb8aa3b, v2
	v_add_f32_e32 v10, v29, v10
	v_exp_f32_e32 v9, v2
	v_sub_f32_e32 v2, v37, v51
	v_add_f32_e32 v10, v30, v10
	v_mul_f32_e32 v2, 0x3fb8aa3b, v2
	v_sub_f32_e32 v3, v49, v51
	v_add_f32_e32 v10, v31, v10
	v_exp_f32_e32 v2, v2
	v_mul_f32_e32 v3, 0x3fb8aa3b, v3
	v_sub_f32_e32 v4, v50, v51
	v_add_f32_e32 v10, v6, v10
	v_exp_f32_e32 v3, v3
	v_mul_f32_e32 v4, 0x3fb8aa3b, v4
	v_sub_f32_e32 v5, v52, v51
	v_add_f32_e32 v10, v7, v10
	v_exp_f32_e32 v4, v4
	v_mul_f32_e32 v5, 0x3fb8aa3b, v5
	v_add_f32_e32 v10, v8, v10
	v_exp_f32_e32 v5, v5
	v_add_f32_e32 v10, v9, v10
	v_add_f32_e32 v10, v2, v10
	v_lshrrev_b32_e32 v11, 2, v38
	v_lshrrev_b32_e32 v15, 2, v17
	v_add_f32_e32 v10, v3, v10
	v_and_b32_e32 v11, 60, v11
	v_and_b32_e32 v14, 15, v38
	v_and_b32_e32 v15, 60, v15
	v_and_b32_e32 v17, 15, v17
	v_lshrrev_b32_e32 v22, 2, v39
	v_and_b32_e32 v23, 15, v39
	v_and_b32_e32 v33, 15, v40
	v_add_f32_e32 v10, v4, v10
	v_add_u32_e32 v11, v16, v11
	v_lshl_add_u32 v14, v14, 2, v16
	v_add_u32_e32 v15, v16, v15
	v_lshl_add_u32 v17, v17, 2, v16
	v_and_b32_e32 v22, 60, v22
	v_lshl_add_u32 v23, v23, 2, v16
	v_and_b32_e32 v32, 60, v32
	v_lshl_add_u32 v33, v33, 2, v16
	v_add_f32_e32 v10, v5, v10
	v_add_u32_e32 v22, v16, v22
	v_add_u32_e32 v32, v16, v32
	ds_read_b32 v11, v11
	ds_read_b32 v14, v14 offset:64
	ds_read_b32 v15, v15
	ds_read_b32 v17, v17 offset:64
	ds_read_b32 v34, v22
	ds_read_b32 v23, v23 offset:64
	ds_read_b32 v35, v32
	ds_read_b32 v33, v33 offset:64
	s_waitcnt lgkmcnt(6)
; #define RT_PK(q_) (ex[q_] | (int)((__float_as_uint(usc[ex[q_]]) >> 23) << 14))
;     __device__ __forceinline__ void fused(f32x4 (&acc)[2][2][4][2], const Unit& u, int wr, int wc, int fr, int fq, PG8_LAS unsigned char* lds, int wid, int lane) const {
;     ...
;             for (int q = 0; q < 16; ++q) { sc[q] = __builtin_amdgcn_exp2f((sc[q] - smax) * 1.4426950408889634f); }
; #pragma unroll
;             for (int q = 0; q < 16; ++q) sum += sc[q];
;             const float rs = 1.0f / sum;
;             asm volatile("s_waitcnt lgkmcnt(0)" ::: "memory");
;             int ex[16];
; #pragma unroll
;             for (int q = 0; q < 16; ++q) { const unsigned cid = __float_as_uint(best[q]) & 255u; ex[q] = idxl[cid >> 4] * 128 + idxl[16 + (cid & 15u)]; }
;             const size_t o = ((size_t)u.pn * 16384 + (size_t)(u.pm * BM + row)) * 16;
;             typedef int i32x4 __attribute__((ext_vector_type(4)));
; #pragma unroll
;             for (int i = 0; i < 4; ++i) {
;     ...
;                 *(i32x4*)(eidx + o + 4 * i) = (i32x4){RT_PK(4 * i), RT_PK(4 * i + 1), RT_PK(4 * i + 2), RT_PK(4 * i + 3)};
;                 *(f32x4*)(egate + o + 4 * i) = (f32x4){sc[4 * i] * rs * vsc[ex[4 * i]], sc[4 * i + 1] * rs * vsc[ex[4 * i + 1]], sc[4 * i + 2] * rs * vsc[ex[4 * i + 2]], sc[4 * i + 3] * rs * vsc[ex[4 * i + 3]]};
	v_lshl_add_u32 v14, v11, 7, v14
	v_div_scale_f32 v11, s[4:5], v10, v10, 1.0
	v_rcp_f32_e32 v36, v11
	s_waitcnt lgkmcnt(4)
	v_lshl_add_u32 v22, v15, 7, v17
	s_waitcnt lgkmcnt(2)
	v_lshl_add_u32 v32, v34, 7, v23
	s_waitcnt lgkmcnt(0)
	v_lshl_add_u32 v34, v35, 7, v33
	v_fma_f32 v15, -v11, v36, 1.0
	v_fmac_f32_e32 v36, v15, v36
	v_div_scale_f32 v15, vcc, 1.0, v10, 1.0
	v_mul_f32_e32 v17, v15, v36
	v_fma_f32 v23, -v11, v17, v15
	v_fmac_f32_e32 v17, v23, v36
	v_fma_f32 v11, -v11, v17, v15
	v_div_fmas_f32 v11, v11, v36, v17
	v_div_fixup_f32 v10, v11, v10, 1.0
	v_pk_mul_f32 v[24:25], v[24:25], v[10:11] op_sel_hi:[1,0]
	v_pk_mul_f32 v[26:27], v[26:27], v[10:11] op_sel_hi:[1,0]
	v_ashrrev_i32_e32 v15, 31, v14
	v_ashrrev_i32_e32 v33, 31, v32
	v_lshl_add_u64 v[12:13], s[10:11], 0, v[12:13]
	v_ashrrev_i32_e32 v23, 31, v22
	v_lshlrev_b64 v[36:37], 3, v[32:33]
	v_lshl_add_u64 v[38:39], s[8:9], 0, v[36:37]
	v_ashrrev_i32_e32 v35, 31, v34
	v_mul_f32_e32 v18, v24, v171
	v_mul_f32_e32 v19, v25, v173
	v_lshlrev_b64 v[24:25], 3, v[14:15]
	v_mul_f32_e32 v20, v26, v175
	v_mul_f32_e32 v21, v27, v177
	global_store_dwordx4 v[12:13], v[18:21], off
	v_lshlrev_b64 v[26:27], 3, v[22:23]
	s_nop 0
	v_lshl_add_u64 v[18:19], s[8:9], 0, v[24:25]
	v_lshl_add_u64 v[20:21], s[8:9], 0, v[26:27]
	global_load_dwordx2 v[178:179], v[18:19], off
	global_load_dwordx2 v[180:181], v[20:21], off
	global_load_dwordx2 v[182:183], v[38:39], off
	v_lshlrev_b64 v[38:39], 3, v[34:35]
	v_lshl_add_u64 v[18:19], s[8:9], 0, v[38:39]
	global_load_dwordx2 v[184:185], v[18:19], off
	s_waitcnt vmcnt(3)
	v_lshrrev_b32_e32 v11, 9, v178
	v_and_or_b32 v18, v11, s3, v14
	s_waitcnt vmcnt(2)
	v_lshrrev_b32_e32 v11, 9, v180
	v_and_or_b32 v19, v11, s3, v22
	s_waitcnt vmcnt(1)
	v_lshrrev_b32_e32 v11, 9, v182
	v_and_or_b32 v20, v11, s3, v32
	s_waitcnt vmcnt(0)
	v_lshrrev_b32_e32 v11, 9, v184
	v_and_or_b32 v21, v11, s3, v34
	global_store_dwordx4 v[0:1], v[18:21], off offset:16
	v_lshrrev_b32_e32 v11, 2, v41
	v_lshrrev_b32_e32 v15, 2, v42
	v_lshrrev_b32_e32 v18, 2, v43
	v_lshrrev_b32_e32 v20, 2, v44
	v_and_b32_e32 v11, 60, v11
	v_and_b32_e32 v14, 15, v41
	v_and_b32_e32 v15, 60, v15
	v_and_b32_e32 v17, 15, v42
	v_and_b32_e32 v18, 60, v18
	v_and_b32_e32 v19, 15, v43
	v_and_b32_e32 v20, 60, v20
	v_and_b32_e32 v21, 15, v44
	v_add_u32_e32 v11, v16, v11
	v_lshl_add_u32 v14, v14, 2, v16
	v_add_u32_e32 v15, v16, v15
	v_lshl_add_u32 v17, v17, 2, v16
	v_add_u32_e32 v18, v16, v18
	v_lshl_add_u32 v19, v19, 2, v16
	v_add_u32_e32 v20, v16, v20
	v_lshl_add_u32 v21, v21, 2, v16
	ds_read_b32 v11, v11
	ds_read_b32 v14, v14 offset:64
	ds_read_b32 v15, v15
	ds_read_b32 v17, v17 offset:64
	ds_read_b32 v18, v18
	ds_read_b32 v19, v19 offset:64
	ds_read_b32 v20, v20
	ds_read_b32 v21, v21 offset:64
	s_waitcnt lgkmcnt(6)
	v_lshl_add_u32 v14, v11, 7, v14
	s_waitcnt lgkmcnt(4)
	v_lshl_add_u32 v22, v15, 7, v17
	s_waitcnt lgkmcnt(2)
	v_lshl_add_u32 v32, v18, 7, v19
	v_pk_mul_f32 v[18:19], v[28:29], v[10:11] op_sel_hi:[1,0]
	s_waitcnt lgkmcnt(0)
	v_lshl_add_u32 v34, v20, 7, v21
	v_pk_mul_f32 v[20:21], v[30:31], v[10:11] op_sel_hi:[1,0]
	v_ashrrev_i32_e32 v15, 31, v14
	v_ashrrev_i32_e32 v33, 31, v32
	v_ashrrev_i32_e32 v23, 31, v22
	v_lshlrev_b64 v[28:29], 3, v[32:33]
	v_lshl_add_u64 v[30:31], s[8:9], 0, v[28:29]
	v_ashrrev_i32_e32 v35, 31, v34
	v_mul_f32_e32 v20, v20, v183
	v_mul_f32_e32 v21, v21, v185
	v_mul_f32_e32 v18, v18, v179
	v_mul_f32_e32 v19, v19, v181
	v_lshlrev_b64 v[24:25], 3, v[14:15]
	global_store_dwordx4 v[12:13], v[18:21], off offset:16
	v_lshlrev_b64 v[26:27], 3, v[22:23]
	s_nop 0
	v_lshl_add_u64 v[18:19], s[8:9], 0, v[24:25]
	v_lshl_add_u64 v[20:21], s[8:9], 0, v[26:27]
	global_load_dwordx2 v[186:187], v[18:19], off
	global_load_dwordx2 v[188:189], v[20:21], off
	global_load_dwordx2 v[190:191], v[30:31], off
	v_lshlrev_b64 v[30:31], 3, v[34:35]
	v_lshl_add_u64 v[18:19], s[8:9], 0, v[30:31]
	global_load_dwordx2 v[192:193], v[18:19], off
	s_waitcnt vmcnt(3)
	v_lshrrev_b32_e32 v11, 9, v186
	v_and_or_b32 v18, v11, s3, v14
	s_waitcnt vmcnt(2)
	v_lshrrev_b32_e32 v11, 9, v188
	v_and_or_b32 v19, v11, s3, v22
	s_waitcnt vmcnt(1)
	v_lshrrev_b32_e32 v11, 9, v190
	v_and_or_b32 v20, v11, s3, v32
	s_waitcnt vmcnt(0)
	v_lshrrev_b32_e32 v11, 9, v192
	v_and_or_b32 v21, v11, s3, v34
	global_store_dwordx4 v[0:1], v[18:21], off offset:32
	v_lshrrev_b32_e32 v11, 2, v45
	v_lshrrev_b32_e32 v15, 2, v46
	v_lshrrev_b32_e32 v18, 2, v47
	v_lshrrev_b32_e32 v20, 2, v48
	v_and_b32_e32 v11, 60, v11
	v_and_b32_e32 v14, 15, v45
	v_and_b32_e32 v15, 60, v15
	v_and_b32_e32 v17, 15, v46
	v_and_b32_e32 v18, 60, v18
	v_and_b32_e32 v19, 15, v47
	v_and_b32_e32 v20, 60, v20
	v_add_u32_e32 v11, v16, v11
	v_lshl_add_u32 v14, v14, 2, v16
	v_add_u32_e32 v15, v16, v15
	v_lshl_add_u32 v17, v17, 2, v16
	v_add_u32_e32 v18, v16, v18
	v_lshl_add_u32 v19, v19, 2, v16
	v_add_u32_e32 v20, v16, v20
	v_and_b32_e32 v21, 15, v48
	v_lshl_add_u32 v16, v21, 2, v16
	ds_read_b32 v11, v11
	ds_read_b32 v14, v14 offset:64
	ds_read_b32 v15, v15
	ds_read_b32 v17, v17 offset:64
	ds_read_b32 v18, v18
	ds_read_b32 v19, v19 offset:64
	ds_read_b32 v20, v20
	ds_read_b32 v21, v16 offset:64
	s_waitcnt lgkmcnt(6)
	v_lshl_add_u32 v14, v11, 7, v14
	s_waitcnt lgkmcnt(4)
	v_lshl_add_u32 v16, v15, 7, v17
	s_waitcnt lgkmcnt(2)
	v_lshl_add_u32 v18, v18, 7, v19
	v_pk_mul_f32 v[6:7], v[6:7], v[10:11] op_sel_hi:[1,0]
	v_pk_mul_f32 v[8:9], v[8:9], v[10:11] op_sel_hi:[1,0]
	v_ashrrev_i32_e32 v15, 31, v14
	v_ashrrev_i32_e32 v19, 31, v18
	s_waitcnt lgkmcnt(0)
	v_lshl_add_u32 v20, v20, 7, v21
	v_lshlrev_b64 v[22:23], 3, v[14:15]
	v_ashrrev_i32_e32 v17, 31, v16
	v_ashrrev_i32_e32 v21, 31, v20
	v_mul_f32_e32 v8, v8, v191
	v_mul_f32_e32 v9, v9, v193
	v_mul_f32_e32 v6, v6, v187
	v_mul_f32_e32 v7, v7, v189
	v_lshlrev_b64 v[26:27], 3, v[18:19]
	global_store_dwordx4 v[12:13], v[6:9], off offset:32
	v_lshlrev_b64 v[24:25], 3, v[16:17]
	v_lshl_add_u64 v[28:29], s[8:9], 0, v[26:27]
	v_lshl_add_u64 v[6:7], s[8:9], 0, v[22:23]
	v_lshl_add_u64 v[8:9], s[8:9], 0, v[24:25]
	global_load_dwordx2 v[194:195], v[6:7], off
	global_load_dwordx2 v[196:197], v[8:9], off
	global_load_dwordx2 v[198:199], v[28:29], off
	v_lshlrev_b64 v[28:29], 3, v[20:21]
	v_lshl_add_u64 v[6:7], s[8:9], 0, v[28:29]
	global_load_dwordx2 v[200:201], v[6:7], off
	s_waitcnt vmcnt(3)
	v_lshrrev_b32_e32 v6, 9, v194
	s_waitcnt vmcnt(2)
	v_lshrrev_b32_e32 v7, 9, v196
	s_waitcnt vmcnt(1)
	v_lshrrev_b32_e32 v8, 9, v198
	v_and_or_b32 v6, v6, s3, v14
	v_and_or_b32 v7, v7, s3, v16
	s_waitcnt vmcnt(0)
	v_lshrrev_b32_e32 v9, 9, v200
	v_and_or_b32 v8, v8, s3, v18
	v_and_or_b32 v9, v9, s3, v20
	global_store_dwordx4 v[0:1], v[6:9], off offset:48
	v_pk_mul_f32 v[0:1], v[2:3], v[10:11] op_sel_hi:[1,0]
	v_pk_mul_f32 v[2:3], v[4:5], v[10:11] op_sel_hi:[1,0]
	v_mul_f32_e32 v0, v0, v195
	v_mul_f32_e32 v1, v1, v197
	v_mul_f32_e32 v2, v2, v199
	v_mul_f32_e32 v3, v3, v201
	global_store_dwordx4 v[12:13], v[0:3], off offset:48

; #define GAS __attribute__((address_space(1)))
; __device__ __forceinline__ void row_to_fp8_2(int lane, const float* xrow0, const float* xrow1, unsigned (&ow0)[4], unsigned (&ow1)[4], float& isc0, float& isc1) {
;     const GAS f32x4* xr0 = (const GAS f32x4*)xrow0 + lane; const GAS f32x4* xr1 = (const GAS f32x4*)xrow1 + lane;
;     f32x4 v0[4], v1[4];
; #pragma unroll
;     for (int j = 0; j < 4; ++j) { v0[j] = __builtin_nontemporal_load(xr0 + 64 * j); v1[j] = __builtin_nontemporal_load(xr1 + 64 * j); }
;     float m0 = 0.f, m1 = 0.f;
; #pragma unroll
;     for (int j = 0; j < 4; ++j) { m0 = fmaxf(m0, fmaxf(fmaxf(fabsf(v0[j].x), fabsf(v0[j].y)), fmaxf(fabsf(v0[j].z), fabsf(v0[j].w)))); m1 = fmaxf(m1, fmaxf(fmaxf(fabsf(v1[j].x), fabsf(v1[j].y)), fmaxf(fabsf(v1[j].z), fabsf(v1[j].w)))); }
; #pragma unroll
;     for (int o = 1; o < 64; o <<= 1) { m0 = fmaxf(m0, __shfl_xor(m0, o)); m1 = fmaxf(m1, __shfl_xor(m1, o)); }
;     int b0 = (int)((__float_as_uint(m0) >> 23) & 255u); b0 = b0 < 16 ? 16 : (b0 > 240 ? 240 : b0);
;     int b1 = (int)((__float_as_uint(m1) >> 23) & 255u); b1 = b1 < 16 ? 16 : (b1 > 240 ? 240 : b1);
;     const float s0 = __uint_as_float((unsigned)(261 - b0) << 23), s1 = __uint_as_float((unsigned)(261 - b1) << 23);
;     isc0 = __uint_as_float((unsigned)(b0 - 7) << 23); isc1 = __uint_as_float((unsigned)(b1 - 7) << 23);
; #pragma unroll
;     for (int j = 0; j < 4; ++j) { int p = __builtin_amdgcn_cvt_pk_fp8_f32(v0[j].x * s0, v0[j].y * s0, 0, false); p = __builtin_amdgcn_cvt_pk_fp8_f32(v0[j].z * s0, v0[j].w * s0, p, true); ow0[j] = (unsigned)p;
; __device__ __forceinline__ void tables_part(LAS unsigned char* lds, int wave, int lane, const float* pu, const float* pv, unsigned char* ws, int gw, int ngw, int wg, int nwg, int r0, int r1, int i0, int i1) {
;     for (int m = r0 + gw; m < r1; m += 2 * ngw) {
;         const int m1 = (m + ngw < r1) ? m + ngw : m;
;         float isc0, isc1; unsigned ow0[4], ow1[4];
;         row_to_fp8_2(lane, pu + (size_t)m * D, pu + (size_t)m1 * D, ow0, ow1, isc0, isc1);
; #pragma unroll
;         for (int j = 0; j < 4; ++j) { *((GAS unsigned*)(ws + WS_UT + (size_t)m * D + j * 256) + lane) = ow0[j]; *((GAS unsigned*)(ws + WS_UT + (size_t)m1 * D + j * 256) + lane) = ow1[j]; }
;         if (lane == 0) { ((float*)(ws + WS_ESC))[m] = isc0; ((float*)(ws + WS_ESC))[m1] = isc1; } }
.LBB0_1172:
	s_cmpk_lt_i32 s3, 0x80
	s_cselect_b32 s99, 0x100, 0
	s_add_i32 s3, s3, s99
	v_xor_b32_e32 v0, 16, v172
	v_cmp_lt_i32_e32 vcc, v0, v177
	s_lshl_b32 s4, s3, 3
	s_add_i32 s4, s61, s4
	v_cndmask_b32_e32 v0, v172, v0, vcc
	v_lshlrev_b32_e32 v10, 2, v0
	v_xor_b32_e32 v0, 32, v172
	v_cmp_lt_i32_e32 vcc, v0, v177
	s_addk_i32 s4, 0xfc00
	s_cmpk_gt_i32 s4, 0x3fff
	s_waitcnt lgkmcnt(0)
	v_cndmask_b32_e32 v1, v172, v0, vcc
	v_mov_b32_e32 v0, v172
	s_load_dwordx2 s[14:15], s[12:13], 0x60
	v_lshlrev_b32_e32 v11, 2, v1
	s_cbranch_scc1 .LBB0_1177
	s_cmp_lg_u32 s99, 0
	s_cbranch_scc1 .LBB0_1177
	s_add_u32 s20, s10, 0x19000000
	v_ashrrev_i32_e32 v1, 31, v0
	s_addc_u32 s21, s11, 0
	s_add_i32 s6, s4, 0x4000
	v_lshlrev_b64 v[6:7], 2, v[0:1]
	s_load_dwordx2 s[8:9], s[12:13], 0x58
	v_lshl_add_u64 v[4:5], s[10:11], 0, v[6:7]
	s_mov_b64 s[12:13], 0x15000000
	s_ashr_i32 s7, s6, 31
	v_lshl_add_u64 v[4:5], v[4:5], 0, s[12:13]
	s_lshl_b64 s[12:13], s[6:7], 3
	s_add_u32 s22, s12, 0x19000000
	s_addc_u32 s23, s13, 0
	s_lshl_b64 s[12:13], s[6:7], 10
	v_lshlrev_b64 v[8:9], 4, v[0:1]
	v_lshl_add_u64 v[6:7], s[12:13], 0, v[6:7]
	s_lshl_b64 s[12:13], s[6:7], 12
	s_waitcnt lgkmcnt(0)
	v_lshl_add_u64 v[2:3], s[8:9], 0, v[8:9]
	s_add_u32 s8, s8, s12
	s_addc_u32 s9, s9, s13
	v_lshl_add_u64 v[8:9], s[8:9], 0, v[8:9]
	s_mov_b64 s[8:9], 0x800
	v_cmp_eq_u32_e64 s[4:5], 0, v0
	v_lshl_add_u64 v[8:9], v[8:9], 0, s[8:9]
	v_mov_b32_e32 v1, 0xf0
	v_mov_b32_e32 v12, 0
	s_mov_b64 s[8:9], 0x200000
	s_mov_b64 s[12:13], 0x800000
	s_branch .LBB0_1175
.LBB0_1174:
	s_or_b64 exec, exec, s[18:19]
	s_add_u32 s22, s22, 0x4000
	s_addc_u32 s23, s23, 0
	s_add_i32 s7, s6, 0x800
	v_lshl_add_u64 v[6:7], v[6:7], 0, s[8:9]
	v_lshl_add_u64 v[8:9], v[8:9], 0, s[12:13]
	s_cmpk_gt_i32 s6, 0x77ff
	s_mov_b32 s6, s7
	s_cbranch_scc1 .LBB0_1177
.LBB0_1175:
	global_load_dwordx4 v[14:17], v[8:9], off offset:-2048 nt
	global_load_dwordx4 v[18:21], v[8:9], off offset:-1024 nt
	global_load_dwordx4 v[22:25], v[8:9], off nt
	global_load_dwordx4 v[26:29], v[8:9], off offset:1024 nt
	s_add_i32 s7, s6, 0x400
	s_cmpk_lt_i32 s6, 0x7c00
	s_cselect_b32 s16, s7, s6
	s_ashr_i32 s17, s16, 31
	s_lshl_b64 s[18:19], s[16:17], 12
	v_lshl_add_u64 v[46:47], v[2:3], 0, s[18:19]
	global_load_dwordx4 v[30:33], v[46:47], off nt
	global_load_dwordx4 v[34:37], v[46:47], off offset:1024 nt
	global_load_dwordx4 v[38:41], v[46:47], off offset:2048 nt
	global_load_dwordx4 v[42:45], v[46:47], off offset:3072 nt
	v_mov_b32_e32 v55, 0
	s_lshl_b64 s[18:19], s[16:17], 10
	s_waitcnt vmcnt(0)
	v_max_f32_e64 v13, |v17|, |v17|
	v_max_f32_e64 v46, |v16|, |v16|
	v_max_f32_e64 v47, |v21|, |v21|
	v_max_f32_e64 v48, |v20|, |v20|
	v_max_f32_e64 v49, |v25|, |v25|
	v_max_f32_e64 v50, |v24|, |v24|
	v_max_f32_e64 v51, |v29|, |v29|
	v_max_f32_e64 v52, |v28|, |v28|
	v_max_f32_e32 v13, v46, v13
	v_max_f32_e32 v46, v48, v47
	v_max_f32_e32 v47, v50, v49
	v_max_f32_e32 v48, v52, v51
	v_max3_f32 v13, |v14|, |v15|, v13
	v_max3_f32 v46, |v18|, |v19|, v46
	v_max3_f32 v47, |v22|, |v23|, v47
	v_max3_f32 v48, |v26|, |v27|, v48
	v_max3_f32 v13, v13, 0, v46
	v_max3_f32 v13, v13, v47, v48
	ds_bpermute_b32 v46, v173, v13
	v_max_f32_e64 v47, |v33|, |v33|
	v_max_f32_e64 v48, |v32|, |v32|
	v_max_f32_e64 v49, |v37|, |v37|
	v_max_f32_e64 v50, |v36|, |v36|
	v_max_f32_e64 v51, |v41|, |v41|
	v_max_f32_e64 v52, |v40|, |v40|
	v_max_f32_e64 v53, |v45|, |v45|
	v_max_f32_e64 v54, |v44|, |v44|
	v_max_f32_e32 v47, v48, v47
	v_max_f32_e32 v48, v50, v49
	v_max_f32_e32 v49, v52, v51
	v_max_f32_e32 v50, v54, v53
	v_max3_f32 v47, |v30|, |v31|, v47
	v_max3_f32 v48, |v34|, |v35|, v48
	v_max3_f32 v49, |v38|, |v39|, v49
	v_max3_f32 v50, |v42|, |v43|, v50
	v_max3_f32 v47, v47, 0, v48
	v_max3_f32 v47, v47, v49, v50
	s_waitcnt lgkmcnt(0)
	v_max_f32_e32 v46, v46, v46
	ds_bpermute_b32 v48, v173, v47
	v_max_f32_e32 v13, v13, v46
	ds_bpermute_b32 v46, v174, v13
	v_mov_b32_e32 v49, 0
	v_mov_b32_e32 v53, 0
	s_waitcnt lgkmcnt(1)
	v_max_f32_e32 v48, v48, v48
	v_max_f32_e32 v47, v47, v48
	s_waitcnt lgkmcnt(0)
	v_max_f32_e32 v46, v46, v46
	ds_bpermute_b32 v48, v174, v47
	v_max_f32_e32 v13, v13, v46
	ds_bpermute_b32 v46, v175, v13
	v_mov_b32_e32 v51, 0
	v_mov_b32_e32 v54, 0
	s_waitcnt lgkmcnt(1)
	v_max_f32_e32 v48, v48, v48
	v_max_f32_e32 v47, v47, v48
	s_waitcnt lgkmcnt(0)
	v_max_f32_e32 v46, v46, v46
	ds_bpermute_b32 v48, v175, v47
	v_max_f32_e32 v13, v13, v46
	ds_bpermute_b32 v46, v176, v13
	v_mov_b32_e32 v50, 0
	v_mov_b32_e32 v52, 0
	s_waitcnt lgkmcnt(1)
; __device__ __forceinline__ void row_to_fp8_2(int lane, const float* xrow0, const float* xrow1, unsigned (&ow0)[4], unsigned (&ow1)[4], float& isc0, float& isc1) {
;     ...
;     for (int o = 1; o < 64; o <<= 1) { m0 = fmaxf(m0, __shfl_xor(m0, o)); m1 = fmaxf(m1, __shfl_xor(m1, o)); }
;     int b0 = (int)((__float_as_uint(m0) >> 23) & 255u); b0 = b0 < 16 ? 16 : (b0 > 240 ? 240 : b0);
;     int b1 = (int)((__float_as_uint(m1) >> 23) & 255u); b1 = b1 < 16 ? 16 : (b1 > 240 ? 240 : b1);
;     const float s0 = __uint_as_float((unsigned)(261 - b0) << 23), s1 = __uint_as_float((unsigned)(261 - b1) << 23);
;     isc0 = __uint_as_float((unsigned)(b0 - 7) << 23); isc1 = __uint_as_float((unsigned)(b1 - 7) << 23);
; #pragma unroll
;     for (int j = 0; j < 4; ++j) { int p = __builtin_amdgcn_cvt_pk_fp8_f32(v0[j].x * s0, v0[j].y * s0, 0, false); p = __builtin_amdgcn_cvt_pk_fp8_f32(v0[j].z * s0, v0[j].w * s0, p, true); ow0[j] = (unsigned)p;
;         int q = __builtin_amdgcn_cvt_pk_fp8_f32(v1[j].x * s1, v1[j].y * s1, 0, false); q = __builtin_amdgcn_cvt_pk_fp8_f32(v1[j].z * s1, v1[j].w * s1, q, true); ow1[j] = (unsigned)q; }
; }
; __device__ __forceinline__ void p0_vslice_item(LAS unsigned char* lds, int wave, int tid, const float* vt_l, unsigned char* VS_l, float* vsc_l, int item) {
;     const int lane = tid & 63, e0 = item * 64;
;     __syncthreads();
; #pragma unroll 1
;     for (int i = 0; i < 8; i += 2) { const int er = wave * 8 + i; float isc0, isc1; unsigned ow0[4], ow1[4];
;         row_to_fp8_2(lane, vt_l + (size_t)(e0 + er) * 1024, vt_l + (size_t)(e0 + er + 1) * 1024, ow0, ow1, isc0, isc1);
; #pragma unroll
;         for (int j = 0; j < 4; ++j) { *(LAS unsigned*)(lds + er * 1032 + j * 256 + lane * 4) = ow0[j]; *(LAS unsigned*)(lds + (er + 1) * 1032 + j * 256 + lane * 4) = ow1[j]; }
;         if (lane == 0) { vsc_l[e0 + er] = isc0; vsc_l[e0 + er + 1] = isc1; } }
; __device__ __forceinline__ void tables_part(LAS unsigned char* lds, int wave, int lane, const float* pu, const float* pv, unsigned char* ws, int gw, int ngw, int wg, int nwg, int r0, int r1, int i0, int i1) {
;     for (int m = r0 + gw; m < r1; m += 2 * ngw) {
;         const int m1 = (m + ngw < r1) ? m + ngw : m;
;         float isc0, isc1; unsigned ow0[4], ow1[4];
;         row_to_fp8_2(lane, pu + (size_t)m * D, pu + (size_t)m1 * D, ow0, ow1, isc0, isc1);
; #pragma unroll
	v_max_f32_e32 v48, v48, v48
	v_max_f32_e32 v47, v47, v48
	s_waitcnt lgkmcnt(0)
	v_max_f32_e32 v46, v46, v46
	ds_bpermute_b32 v48, v176, v47
	v_max_f32_e32 v13, v13, v46
	ds_bpermute_b32 v46, v10, v13
	s_waitcnt lgkmcnt(1)
	v_max_f32_e32 v48, v48, v48
	v_max_f32_e32 v47, v47, v48
	s_waitcnt lgkmcnt(0)
	v_max_f32_e32 v46, v46, v46
	ds_bpermute_b32 v48, v10, v47
	v_max_f32_e32 v13, v13, v46
	ds_bpermute_b32 v46, v11, v13
	s_waitcnt lgkmcnt(1)
	v_max_f32_e32 v48, v48, v48
	v_max_f32_e32 v47, v47, v48
	s_waitcnt lgkmcnt(0)
	v_max_f32_e32 v46, v46, v46
	v_max_f32_e32 v13, v13, v46
	ds_bpermute_b32 v46, v11, v47
	v_bfe_u32 v13, v13, 23, 8
	v_med3_u32 v13, v13, 16, v1
	v_lshlrev_b32_e32 v13, 23, v13
	v_sub_u32_e32 v48, 0x82800000, v13
	s_waitcnt lgkmcnt(0)
	v_max_f32_e32 v46, v46, v46
	v_mul_f32_e32 v14, v14, v48
	v_mul_f32_e32 v15, v15, v48
	v_mul_f32_e32 v22, v22, v48
	v_mul_f32_e32 v23, v23, v48
	v_max_f32_e32 v46, v47, v46
	v_cvt_pk_fp8_f32 v49, v14, v15
	v_cvt_pk_fp8_f32 v53, v22, v23
	v_bfe_u32 v14, v46, 23, 8
	v_med3_u32 v14, v14, 16, v1
	v_lshlrev_b32_e32 v14, 23, v14
	v_mul_f32_e32 v18, v18, v48
	v_mul_f32_e32 v19, v19, v48
	v_mul_f32_e32 v24, v24, v48
	v_mul_f32_e32 v25, v25, v48
	v_sub_u32_e32 v15, 0x82800000, v14
	v_cvt_pk_fp8_f32 v51, v18, v19
	v_cvt_pk_fp8_f32 v53, v24, v25 op_sel:[0,0,1]
	v_mul_f32_e32 v24, v38, v15
	v_mul_f32_e32 v25, v39, v15
	v_cvt_pk_fp8_f32 v54, v24, v25
	v_mul_f32_e32 v16, v16, v48
	v_mul_f32_e32 v17, v17, v48
	v_mul_f32_e32 v20, v20, v48
	v_mul_f32_e32 v21, v21, v48
	v_mul_f32_e32 v26, v26, v48
	v_mul_f32_e32 v27, v27, v48
	v_cvt_pk_fp8_f32 v49, v16, v17 op_sel:[0,0,1]
	v_mul_f32_e32 v16, v30, v15
	v_mul_f32_e32 v17, v31, v15
	v_cvt_pk_fp8_f32 v55, v26, v27
	v_cvt_pk_fp8_f32 v51, v20, v21 op_sel:[0,0,1]
	v_mul_f32_e32 v20, v34, v15
	v_mul_f32_e32 v21, v35, v15
	v_mul_f32_e32 v26, v40, v15
	v_cvt_pk_fp8_f32 v50, v16, v17
	v_mul_f32_e32 v16, v41, v15
	v_cvt_pk_fp8_f32 v52, v20, v21
	v_cvt_pk_fp8_f32 v54, v26, v16 op_sel:[0,0,1]
	v_mul_f32_e32 v16, v42, v15
	v_mul_f32_e32 v17, v43, v15
	v_mov_b32_e32 v20, 0
	v_cvt_pk_fp8_f32 v20, v16, v17
	v_mul_f32_e32 v18, v32, v15
	v_mul_f32_e32 v19, v33, v15
	v_mul_f32_e32 v22, v36, v15
	v_mul_f32_e32 v23, v37, v15
	v_cvt_pk_fp8_f32 v50, v18, v19 op_sel:[0,0,1]
	v_mul_f32_e32 v16, v44, v15
	v_mul_f32_e32 v15, v45, v15
	v_cvt_pk_fp8_f32 v20, v16, v15 op_sel:[0,0,1]
	v_lshl_add_u64 v[16:17], s[10:11], 0, v[6:7]
	v_cvt_pk_fp8_f32 v52, v22, v23 op_sel:[0,0,1]
	v_add_co_u32_e32 v16, vcc, 0x15000000, v16
	v_mul_f32_e32 v28, v28, v48
	v_mul_f32_e32 v29, v29, v48
	v_addc_co_u32_e32 v17, vcc, 0, v17, vcc
	v_lshl_add_u64 v[18:19], v[4:5], 0, s[18:19]
	v_cvt_pk_fp8_f32 v55, v28, v29 op_sel:[0,0,1]
	global_store_dword v[16:17], v49, off
	global_store_dword v[18:19], v50, off
	global_store_dword v[16:17], v51, off offset:256
	global_store_dword v[18:19], v52, off offset:256
	global_store_dword v[16:17], v53, off offset:512
	global_store_dword v[18:19], v54, off offset:512
	global_store_dword v[16:17], v55, off offset:768
	global_store_dword v[18:19], v20, off offset:768
	s_and_saveexec_b64 s[18:19], s[4:5]
	s_cbranch_execz .LBB0_1174
	s_lshl_b64 s[16:17], s[16:17], 3
	s_add_u32 s16, s20, s16
	s_addc_u32 s17, s21, s17
	s_add_u32 s24, s10, s22
	v_add_u32_e32 v13, 0xfc800000, v13
	s_addc_u32 s25, s11, s23
	v_add_u32_e32 v14, 0xfc800000, v14
	global_store_dword v12, v13, s[24:25]
	global_store_dword v12, v14, s[16:17]
	s_branch .LBB0_1174
.LBB0_1177:
	s_cmpk_gt_u32 s3, 0x17f
	s_cbranch_scc1 .LBB0_1187
	s_add_u32 s20, s10, 0x17000000
	s_addc_u32 s21, s11, 0
	s_lshl_b32 s16, s61, 3
	s_mul_i32 s8, s61, 0x2040
	s_ashr_i32 s17, s16, 31
	s_add_i32 s8, s8, 0
	s_lshl_b64 s[12:13], s[16:17], 12
	v_or_b32_e32 v6, s56, v0
	v_and_b32_e32 v0, 63, v0
	s_waitcnt lgkmcnt(0)
	s_add_u32 s12, s14, s12
	v_cmp_eq_u32_e64 s[4:5], 0, v0
	v_lshl_add_u32 v7, v0, 2, s8
	v_lshlrev_b32_e32 v0, 4, v0
	v_mov_b32_e32 v1, 0
	s_addc_u32 s13, s15, s13
	v_lshl_add_u64 v[2:3], s[12:13], 0, v[0:1]
	s_mov_b64 s[12:13], 0x1c00
	v_lshl_add_u64 v[2:3], v[2:3], 0, s[12:13]
	s_add_u32 s12, s3, 0x80
	s_addc_u32 s13, 0, 0
	s_lshl_b32 s8, s3, 6
	s_addk_i32 s8, 0x2000
	s_lshr_b32 s22, s8, 6
	s_lshl_b64 s[14:15], s[16:17], 3
	s_add_u32 s8, s10, s14
	s_addc_u32 s10, s11, s15
	s_movk_i32 s6, 0x1000
	s_add_u32 s23, s8, 0x19000008
	s_mov_b32 s9, 0
	v_cmp_gt_i32_e64 s[6:7], s6, v6
	s_addc_u32 s24, s10, 0
	s_add_i32 s25, s3, 0x80
	v_lshlrev_b32_e32 v0, 1, v6
	v_mov_b32_e32 v8, 0xf0
	s_mov_b64 s[10:11], 0x2000
	s_movk_i32 s26, 0xdff
	s_mov_b32 s27, s3
	s_branch .LBB0_1180

; #define GAS __attribute__((address_space(1)))
; #define LAS __attribute__((address_space(3)))
; __device__ __forceinline__ void row_to_fp8_2(int lane, const float* xrow0, const float* xrow1, unsigned (&ow0)[4], unsigned (&ow1)[4], float& isc0, float& isc1) {
;     const GAS f32x4* xr0 = (const GAS f32x4*)xrow0 + lane; const GAS f32x4* xr1 = (const GAS f32x4*)xrow1 + lane;
;     f32x4 v0[4], v1[4];
; #pragma unroll
;     for (int j = 0; j < 4; ++j) { v0[j] = __builtin_nontemporal_load(xr0 + 64 * j); v1[j] = __builtin_nontemporal_load(xr1 + 64 * j); }
;     float m0 = 0.f, m1 = 0.f;
; #pragma unroll
;     for (int j = 0; j < 4; ++j) { m0 = fmaxf(m0, fmaxf(fmaxf(fabsf(v0[j].x), fabsf(v0[j].y)), fmaxf(fabsf(v0[j].z), fabsf(v0[j].w)))); m1 = fmaxf(m1, fmaxf(fmaxf(fabsf(v1[j].x), fabsf(v1[j].y)), fmaxf(fabsf(v1[j].z), fabsf(v1[j].w)))); }
; #pragma unroll
;     for (int o = 1; o < 64; o <<= 1) { m0 = fmaxf(m0, __shfl_xor(m0, o)); m1 = fmaxf(m1, __shfl_xor(m1, o)); }
;     int b0 = (int)((__float_as_uint(m0) >> 23) & 255u); b0 = b0 < 16 ? 16 : (b0 > 240 ? 240 : b0);
;     int b1 = (int)((__float_as_uint(m1) >> 23) & 255u); b1 = b1 < 16 ? 16 : (b1 > 240 ? 240 : b1);
;     const float s0 = __uint_as_float((unsigned)(261 - b0) << 23), s1 = __uint_as_float((unsigned)(261 - b1) << 23);
;     isc0 = __uint_as_float((unsigned)(b0 - 7) << 23); isc1 = __uint_as_float((unsigned)(b1 - 7) << 23);
; #pragma unroll
;     for (int j = 0; j < 4; ++j) { int p = __builtin_amdgcn_cvt_pk_fp8_f32(v0[j].x * s0, v0[j].y * s0, 0, false); p = __builtin_amdgcn_cvt_pk_fp8_f32(v0[j].z * s0, v0[j].w * s0, p, true); ow0[j] = (unsigned)p;
; __device__ __forceinline__ void p0_vslice_item(LAS unsigned char* lds, int wave, int tid, const float* vt_l, unsigned char* VS_l, float* vsc_l, int item) {
;     const int lane = tid & 63, e0 = item * 64;
;     __syncthreads();
; #pragma unroll 1
;     for (int i = 0; i < 8; i += 2) { const int er = wave * 8 + i; float isc0, isc1; unsigned ow0[4], ow1[4];
;         row_to_fp8_2(lane, vt_l + (size_t)(e0 + er) * 1024, vt_l + (size_t)(e0 + er + 1) * 1024, ow0, ow1, isc0, isc1);
; #pragma unroll
;         for (int j = 0; j < 4; ++j) { *(LAS unsigned*)(lds + er * 1032 + j * 256 + lane * 4) = ow0[j]; *(LAS unsigned*)(lds + (er + 1) * 1032 + j * 256 + lane * 4) = ow1[j]; }
;         if (lane == 0) { vsc_l[e0 + er] = isc0; vsc_l[e0 + er + 1] = isc1; } }
.LBB0_1180:
	s_lshl_b64 s[14:15], s[12:13], 18
	s_and_b32 s16, s22, 0xff
	s_and_b32 s8, s14, 0xfc000000
	s_lshl_b32 s14, s16, 18
	s_or_b32 s14, s8, s14
	s_lshl_b32 s8, s25, 6
	s_and_b32 s8, s8, 0xffffc000
	v_lshl_add_u64 v[4:5], v[2:3], 0, s[14:15]
	s_lshl_b32 s16, s16, 9
	s_lshl_b64 s[14:15], s[8:9], 3
	s_or_b32 s8, s14, s16
	s_add_u32 s14, s23, s8
	s_addc_u32 s15, s24, s15
	s_mov_b32 s8, -2
	v_mov_b32_e32 v9, v7
	s_waitcnt vmcnt(0)
	s_barrier
	s_branch .LBB0_1182
.LBB0_1181:
	s_or_b64 exec, exec, s[16:17]
	s_add_i32 s8, s8, 2
	s_add_u32 s14, s14, 16
	s_addc_u32 s15, s15, 0
	v_add_u32_e32 v9, 0x810, v9
	s_cmp_gt_u32 s8, 5
	v_lshl_add_u64 v[4:5], v[4:5], 0, s[10:11]
	s_cbranch_scc1 .LBB0_1184
.LBB0_1182:
	global_load_dwordx4 v[14:17], v[4:5], off offset:-3072 nt
	global_load_dwordx4 v[18:21], v[4:5], off offset:-2048 nt
	global_load_dwordx4 v[22:25], v[4:5], off offset:-1024 nt
	global_load_dwordx4 v[26:29], v[4:5], off nt
	v_add_co_u32_e32 v12, vcc, 0xfffff000, v4
	s_waitcnt vmcnt(2)
	v_max_f32_e64 v46, |v21|, |v21|
	v_addc_co_u32_e32 v13, vcc, -1, v5, vcc
	global_load_dwordx4 v[30:33], v[12:13], off offset:-3072 nt
	global_load_dwordx4 v[34:37], v[12:13], off offset:-2048 nt
	global_load_dwordx4 v[38:41], v[12:13], off offset:-1024 nt
	global_load_dwordx4 v[42:45], v[4:5], off offset:-4096 nt
	v_max_f32_e64 v12, |v17|, |v17|
	v_max_f32_e64 v13, |v16|, |v16|
	v_max_f32_e64 v47, |v20|, |v20|
	s_waitcnt vmcnt(5)
	v_max_f32_e64 v48, |v25|, |v25|
	v_max_f32_e64 v49, |v24|, |v24|
	s_waitcnt vmcnt(4)
	v_max_f32_e64 v50, |v29|, |v29|
	v_max_f32_e64 v51, |v28|, |v28|
	v_max_f32_e32 v12, v13, v12
	v_max_f32_e32 v13, v47, v46
	v_max_f32_e32 v46, v49, v48
	v_max_f32_e32 v47, v51, v50
	v_max3_f32 v12, |v14|, |v15|, v12
	v_max3_f32 v13, |v18|, |v19|, v13
	v_max3_f32 v46, |v22|, |v23|, v46
	v_max3_f32 v47, |v26|, |v27|, v47
	v_max3_f32 v12, v12, 0, v13
	v_max3_f32 v12, v12, v46, v47
	ds_bpermute_b32 v47, v173, v12
	s_waitcnt lgkmcnt(0)
	v_max_f32_e32 v47, v47, v47
	v_max_f32_e32 v12, v12, v47
	ds_bpermute_b32 v47, v174, v12
	s_waitcnt lgkmcnt(0)
	v_max_f32_e32 v47, v47, v47
	v_max_f32_e32 v12, v12, v47
	ds_bpermute_b32 v47, v175, v12
	s_waitcnt lgkmcnt(0)
	v_max_f32_e32 v47, v47, v47
	v_max_f32_e32 v12, v12, v47
	ds_bpermute_b32 v47, v176, v12
	s_waitcnt lgkmcnt(0)
	v_max_f32_e32 v47, v47, v47
	v_max_f32_e32 v12, v12, v47
	ds_bpermute_b32 v47, v10, v12
	s_waitcnt lgkmcnt(0)
	v_max_f32_e32 v47, v47, v47
	v_max_f32_e32 v12, v12, v47
	ds_bpermute_b32 v47, v11, v12
	s_waitcnt lgkmcnt(0)
	v_max_f32_e32 v47, v47, v47
	v_max_f32_e32 v12, v12, v47
	v_bfe_u32 v12, v12, 23, 8
	v_med3_u32 v12, v12, 16, v8
	v_lshlrev_b32_e32 v12, 23, v12
	s_waitcnt vmcnt(3)
	v_max_f32_e64 v48, |v33|, |v33|
	v_max_f32_e64 v49, |v32|, |v32|
	s_waitcnt vmcnt(2)
	v_max_f32_e64 v50, |v37|, |v37|
	v_max_f32_e64 v51, |v36|, |v36|
	s_waitcnt vmcnt(1)
	v_max_f32_e64 v52, |v41|, |v41|
	v_max_f32_e64 v53, |v40|, |v40|
	s_waitcnt vmcnt(0)
	v_max_f32_e64 v54, |v45|, |v45|
	v_max_f32_e64 v55, |v44|, |v44|
	v_max_f32_e32 v48, v49, v48
	v_max_f32_e32 v49, v51, v50
	v_max_f32_e32 v13, v53, v52
	v_max_f32_e32 v50, v55, v54
	v_max3_f32 v48, |v30|, |v31|, v48
	v_max3_f32 v49, |v34|, |v35|, v49
	v_max3_f32 v13, |v38|, |v39|, v13
	v_max3_f32 v50, |v42|, |v43|, v50
	v_max3_f32 v46, v48, 0, v49
	v_max3_f32 v13, v46, v13, v50
	ds_bpermute_b32 v46, v173, v13
	v_mov_b32_e32 v49, 0
	v_mov_b32_e32 v48, 0
	v_mov_b32_e32 v53, 0
	v_mov_b32_e32 v50, 0
	s_waitcnt lgkmcnt(0)
	v_max_f32_e32 v46, v46, v46
	v_max_f32_e32 v13, v13, v46
	ds_bpermute_b32 v46, v174, v13
	v_mov_b32_e32 v51, 0
	v_mov_b32_e32 v52, 0
	v_mov_b32_e32 v54, 0
	s_waitcnt lgkmcnt(0)
	v_max_f32_e32 v46, v46, v46
	v_max_f32_e32 v13, v13, v46
	ds_bpermute_b32 v46, v175, v13
	s_waitcnt lgkmcnt(0)
	v_max_f32_e32 v46, v46, v46
	v_max_f32_e32 v13, v13, v46
	ds_bpermute_b32 v46, v176, v13
	s_waitcnt lgkmcnt(0)
	v_max_f32_e32 v46, v46, v46
	v_max_f32_e32 v13, v13, v46
	ds_bpermute_b32 v46, v10, v13
	s_waitcnt lgkmcnt(0)
	v_max_f32_e32 v46, v46, v46
	v_max_f32_e32 v13, v13, v46
	ds_bpermute_b32 v46, v11, v13
	s_waitcnt lgkmcnt(0)
	v_max_f32_e32 v46, v46, v46
	v_max_f32_e32 v13, v13, v46
	v_bfe_u32 v13, v13, 23, 8
	v_med3_u32 v13, v13, 16, v8
	v_sub_u32_e32 v46, 0x82800000, v12
	v_lshlrev_b32_e32 v13, 23, v13
	v_mul_f32_e32 v14, v14, v46
	v_mul_f32_e32 v15, v15, v46
	v_sub_u32_e32 v47, 0x82800000, v13
	v_cvt_pk_fp8_f32 v49, v14, v15
	v_mul_f32_e32 v14, v30, v47
	v_mul_f32_e32 v15, v31, v47
	v_cvt_pk_fp8_f32 v48, v14, v15
	v_mul_f32_e32 v22, v22, v46
	v_mul_f32_e32 v23, v23, v46
	v_mul_f32_e32 v18, v18, v46
	v_mul_f32_e32 v19, v19, v46
	v_cvt_pk_fp8_f32 v53, v22, v23
	v_mul_f32_e32 v22, v34, v47
	v_mul_f32_e32 v23, v35, v47
	v_mul_f32_e32 v16, v16, v46
	v_mul_f32_e32 v17, v17, v46
	v_cvt_pk_fp8_f32 v51, v18, v19
	v_mul_f32_e32 v18, v32, v47
	v_mul_f32_e32 v19, v33, v47
	v_mul_f32_e32 v30, v36, v47
	v_mul_f32_e32 v31, v37, v47
	v_mul_f32_e32 v32, v38, v47
	v_mul_f32_e32 v33, v39, v47
	v_mul_f32_e32 v36, v42, v47
	v_mul_f32_e32 v37, v43, v47
	v_cvt_pk_fp8_f32 v50, v22, v23
	v_cvt_pk_fp8_f32 v52, v32, v33
	v_cvt_pk_fp8_f32 v54, v36, v37
	v_cvt_pk_fp8_f32 v49, v16, v17 op_sel:[0,0,1]
	v_cvt_pk_fp8_f32 v48, v18, v19 op_sel:[0,0,1]
	v_mul_f32_e32 v16, v26, v46
	v_mul_f32_e32 v17, v27, v46
	v_mov_b32_e32 v18, 0
	v_cvt_pk_fp8_f32 v18, v16, v17
	v_mul_f32_e32 v20, v20, v46
	v_mul_f32_e32 v21, v21, v46
	v_mul_f32_e32 v34, v40, v47
	v_mul_f32_e32 v35, v41, v47
	v_cvt_pk_fp8_f32 v51, v20, v21 op_sel:[0,0,1]
	v_cvt_pk_fp8_f32 v50, v30, v31 op_sel:[0,0,1]
	v_mul_f32_e32 v14, v44, v47
	v_mul_f32_e32 v15, v45, v47
	v_mul_f32_e32 v24, v24, v46
	v_mul_f32_e32 v25, v25, v46
	v_cvt_pk_fp8_f32 v52, v34, v35 op_sel:[0,0,1]
	v_cvt_pk_fp8_f32 v54, v14, v15 op_sel:[0,0,1]
	v_mul_f32_e32 v14, v28, v46
	v_mul_f32_e32 v15, v29, v46
	v_cvt_pk_fp8_f32 v53, v24, v25 op_sel:[0,0,1]
	v_cvt_pk_fp8_f32 v18, v14, v15 op_sel:[0,0,1]
	v_add_u32_e32 v14, 8, v9
	ds_write2st64_b32 v9, v48, v50 offset1:1
	ds_write2st64_b32 v14, v49, v51 offset0:4 offset1:5
	ds_write2st64_b32 v9, v52, v54 offset0:2 offset1:3
	ds_write2st64_b32 v14, v53, v18 offset0:6 offset1:7
	s_and_saveexec_b64 s[16:17], s[4:5]
	s_cbranch_execz .LBB0_1181
	v_add_u32_e32 v14, 0xfc800000, v13
	v_add_u32_e32 v15, 0xfc800000, v12
	global_store_dword v1, v14, s[14:15] offset:-4
	global_store_dword v1, v15, s[14:15] offset:4
	s_branch .LBB0_1181

; #define PG8_WAIT_V(n) asm volatile("s_waitcnt vmcnt(" #n ")" ::: "memory")
; template <class Epi, class Sched, bool ALIGN_EPI = false, bool SP2 = false>
; __device__ __forceinline__ void gemm_phase(int wave_id  , PG8_LAS unsigned char* lds, const Gemm g, const Sched& S, const Epi& E) {
;     ...
;     for (int i = 0; i < 2; ++i) { int R, C; stage_rc(tid * 16 + i * 8192, R, C); const int Rb = Epi::PERM ? ((R & ~31) + perm32(R & 31)) : R;
;         voffA[i] = (unsigned)(R * K + C) * 2u; voffB[i] = (unsigned)(Rb * K + C) * 2u; }
;     const size_t kstep = (size_t)(BK * 2);
;     const size_t hstep = (size_t)HALF * K * 2;
;     const size_t tstep = 2 * hstep;
;     const unsigned ldsw = (unsigned)wid * 1024u;
;     const int aoff = lds_byte(wr * 64 + fr, fq * 8), boff = lds_byte(wc * 32 + fr, fq * 8);
;     ...
;     Unit cur, nxt; int ui = 0;
;     if (!S.next(0, cur)) return;
;     f32x4 acc[2][2][4][2];
; #pragma unroll
;     for (int a = 0; a < 2; ++a)
; #pragma unroll
;         for (int b = 0; b < 2; ++b)
; #pragma unroll
;             for (int m = 0; m < 4; ++m)
; #pragma unroll
;                 for (int n = 0; n < 2; ++n) acc[a][b][m][n] = (f32x4){0.f, 0.f, 0.f, 0.f};
;     bf16x8 At[4][2], B0[2][2], B1[2][2];
;     const char* cA = (const char*)g.A + (size_t)cur.pm * tstep; const char* cB = (const char*)g.Bt + (size_t)cur.pn * tstep;
;     S.a_ready(cur);
;     if constexpr (SP2) {
;         PG8_STAGE(PG8_SB(0, 0), cB, voffB); PG8_STAGE(PG8_SB(0, 1), cB + hstep, voffB); PG8_STAGE(PG8_SA(0, 0), cA, voffA); PG8_STAGE(PG8_SA(0, 1), cA + hstep, voffA);
;         if (wr == 1) PG8_BAR;
;         PG8_WAIT_V(2); PG8_BAR;
; template <int K> __device__ __forceinline__ void run_phase(Frame& F, const XcdBarrier& bar, int lo, int hi, unsigned char* lds) {
;     ...
;             pg8::Gemm g{X1B, (bf16*)(ws + WS_WQ) + (size_t)l * NPQ * D, M, NPQ, D}; pg8::StaticOrder S; S.init(M, NPQ, G, bx, MK_WGM3);
;     ...
;             pg8::EpiRoute E{(int*)(ws + WS_EIDX), (float*)(ws + WS_EGATE), (float*)(ws + WS_EUS), (const float*)(ws + WS_ESC) + l * 16384, (const float*)(ws + WS_ESC) + 32768 + l * 16384};
;             pg8::OneUnit S0{S, 0}, S1{S, 1};
;             pg8::gemm_phase<pg8::EpiRoute, pg8::OneUnit, false, true>(F.wave, F.lds + RING_OFF, g, S0, E);
;             pg8::gemm_phase<pg8::EpiRoute, pg8::OneUnit, false, true>(F.wave, F.lds + RING_OFF, g, S1, E);
.LBB0_1568:
	s_cmp_gt_i32 s40, 11
	s_cselect_b64 s[4:5], -1, 0
	s_cmp_lt_i32 s41, 12
	s_cselect_b64 s[6:7], -1, 0
	s_or_b64 s[4:5], s[4:5], s[6:7]
	s_and_b64 vcc, exec, s[4:5]
	s_cbranch_vccnz .LBB0_1661
	s_mov_b64 s[4:5], s[0:1]
	s_waitcnt lgkmcnt(0)
	s_load_dwordx2 s[14:15], s[4:5], 0x80
	s_waitcnt vmcnt(0)
	v_mbcnt_lo_u32_b32 v0, -1, 0
	v_mbcnt_hi_u32_b32 v136, -1, v0
	v_lshl_or_b32 v137, s61, 6, v136
	s_mov_b32 s49, s2
	s_waitcnt lgkmcnt(0)
	s_add_u32 s3, s14, 0x6000000
	s_addc_u32 s46, s15, 0
	s_add_u32 s47, s14, 0x1400000
	s_addc_u32 s48, s15, 0
	s_add_u32 s12, s14, 0x14000000
	s_addc_u32 s13, s15, 0
	s_add_u32 s10, s14, 0x14800000
	s_addc_u32 s11, s15, 0
	s_add_u32 s8, s14, 0x19020000
	s_addc_u32 s9, s15, 0
	s_add_u32 s6, s14, 0x19020004
	s_mov_b32 s50, s60
	s_addc_u32 s7, s15, 0
	v_mov_b32_e32 v139, v137
	s_cmpk_gt_i32 s49, 0x1ff
	s_nop 0
	v_readfirstlane_b32 s53, v139
	s_cbranch_scc1 .LBB0_1587
	v_lshlrev_b32_e32 v0, 4, v139
	v_add_u32_e32 v1, 0x2000, v0
	v_ashrrev_i32_e32 v2, 31, v1
	v_lshrrev_b32_e32 v2, 22, v2
	v_add_u32_e32 v2, v1, v2
	v_ashrrev_i32_e32 v8, 10, v2
	v_mul_i32_i24_e32 v3, 0x400, v8
	v_sub_u32_e32 v1, v1, v3
	v_lshrrev_b32_e32 v3, 4, v1
	v_bitop3_b32 v1, v3, v1, 32 bitop3:0x6c
	v_ashrrev_i32_e32 v3, 31, v1
	v_lshrrev_b32_e32 v3, 26, v3
	v_add_u32_e32 v3, v1, v3
	v_ashrrev_i32_e32 v10, 6, v3
	v_and_b32_e32 v3, 0xc0, v3
	v_sub_u32_e32 v1, v1, v3
	v_mov_b32_e32 v3, 1
	v_lshlrev_b32_e32 v2, 5, v8
	v_ashrrev_i16_sdwa v1, v3, sext(v1) dst_sel:DWORD dst_unused:UNUSED_PAD src0_sel:DWORD src1_sel:BYTE_0
	v_and_b32_e32 v2, 32, v2
	v_bfe_i32 v11, v1, 0, 16
	s_ashr_i32 s4, s49, 31
	v_add_u32_e32 v1, v2, v11
	v_lshlrev_b32_e32 v2, 3, v8
	s_lshr_b32 s4, s4, 29
	v_and_b32_e32 v2, 0x1ffff0, v2
	s_add_i32 s4, s49, s4
	v_add_lshl_u32 v2, v10, v2, 11
	s_ashr_i32 s5, s4, 3
	s_and_b32 s4, s4, -8
	s_ashr_i32 s51, s53, 6
	v_lshl_add_u32 v128, v1, 1, v2
	v_bfe_i32 v2, v139, 27, 1
	s_sub_i32 s4, s49, s4
	s_ashr_i32 s52, s53, 8
	s_lshl_b32 s42, s51, 10
	v_lshrrev_b32_e32 v2, 22, v2
	s_lshl_b32 s17, s4, 6
	v_add_u32_e32 v2, v0, v2
	s_mul_i32 s16, s4, 0x41
	s_cmp_lt_i32 s4, 0
	v_and_b32_e32 v2, 0xfffffc00, v2
	s_cselect_b32 s28, s16, s17
	v_sub_u32_e32 v0, v0, v2
	s_add_i32 s28, s28, s5
	v_lshrrev_b32_e32 v2, 4, v0
	s_ashr_i32 s4, s28, 31
	v_bitop3_b32 v0, v2, v0, 32 bitop3:0x6c
	s_lshr_b32 s4, s4, 27
	v_ashrrev_i32_e32 v2, 31, v0
	s_add_i32 s4, s28, s4
	v_ashrrev_i32_e32 v1, 31, v139
	v_lshrrev_b32_e32 v2, 26, v2
	s_ashr_i32 s43, s4, 5
	v_lshrrev_b32_e32 v1, 26, v1
	v_add_u32_e32 v2, v0, v2
	s_lshl_b32 s29, s43, 2
	v_add_u32_e32 v1, v139, v1
	v_ashrrev_i32_e32 v12, 6, v2
	v_and_b32_e32 v2, 0xc0, v2
	s_sub_i32 s5, 64, s29
	v_ashrrev_i32_e32 v9, 6, v1
	v_sub_u32_e32 v0, v0, v2
	s_min_u32 s16, s5, 4
	s_andn2_b32 s4, s4, 31
	v_lshlrev_b32_e32 v1, 5, v9
	v_ashrrev_i16_sdwa v0, v3, sext(v0) dst_sel:DWORD dst_unused:UNUSED_PAD src0_sel:DWORD src1_sel:BYTE_0
	s_sub_i32 s17, s28, s4
	v_cvt_f32_ubyte0_e32 v3, s16
	v_and_b32_e32 v1, 32, v1
	v_bfe_i32 v13, v0, 0, 16
	v_cvt_f32_i32_e32 v2, s17
	v_rcp_iflag_f32_e32 v4, v3
	v_add_u32_e32 v0, v1, v13
	v_lshlrev_b32_e32 v1, 3, v9
	v_and_b32_e32 v1, 0x1ffff0, v1
	v_add_lshl_u32 v1, v12, v1, 11
	v_lshl_add_u32 v130, v0, 1, v1
	v_mul_f32_e32 v0, v2, v4
	v_trunc_f32_e32 v0, v0
	v_fma_f32 v1, -v0, v3, v2
	v_cvt_i32_f32_e32 v0, v0
	s_ashr_i32 s4, s17, 30
	s_or_b32 s18, s4, 1
	v_cmp_ge_f32_e64 s[4:5], |v1|, v3
	s_and_b64 s[4:5], s[4:5], exec
	s_cselect_b32 s4, s18, 0
	v_readfirstlane_b32 s5, v0
	s_add_i32 s4, s5, s4
	s_mul_i32 s44, s4, s16
	s_sub_i32 s5, s17, s44
	s_sext_i32_i8 s5, s5
	s_add_i32 s18, s29, s5
	s_bfe_i64 s[16:17], s[4:5], 0x80000
	s_ashr_i32 s19, s18, 31
	s_lshl_b64 s[20:21], s[18:19], 19
	s_lshl_b64 s[26:27], s[16:17], 19
	s_add_u32 s4, s47, s26
	s_addc_u32 s5, s48, s27
	s_add_i32 s19, s42, 0
	s_add_i32 m0, s19, 0x10000
	v_mov_b32_e32 v131, 0
	global_load_lds_dwordx4 v130, s[4:5]
	s_add_i32 m0, s19, 0x12000
	s_add_u32 s22, s4, 0x40000
	global_load_lds_dwordx4 v128, s[4:5]
	s_addc_u32 s23, s5, 0
	s_add_i32 m0, s19, 0x14000
	v_mov_b32_e32 v129, v131
	global_load_lds_dwordx4 v130, s[22:23]
	s_add_i32 m0, s19, 0x16000
	v_lshl_add_u64 v[6:7], s[4:5], 0, v[130:131]
	global_load_lds_dwordx4 v128, s[22:23]
	s_add_u32 s22, s3, s20
	s_addc_u32 s23, s46, s21
	s_add_i32 s54, s19, 0x2000
	s_mov_b32 m0, s19
	s_add_u32 s20, s22, 0x40000
	global_load_lds_dwordx4 v130, s[22:23]
	s_mov_b32 m0, s54
	s_addc_u32 s21, s23, 0
	s_add_i32 s55, s19, 0x4000
	global_load_lds_dwordx4 v128, s[22:23]
	s_mov_b32 m0, s55
	s_add_i32 s56, s19, 0x6000
	global_load_lds_dwordx4 v130, s[20:21]
	s_mov_b32 m0, s56
	s_cmp_eq_u32 s52, 1
	global_load_lds_dwordx4 v128, s[20:21]
	v_lshl_add_u64 v[4:5], s[4:5], 0, v[128:129]
	v_lshl_add_u64 v[0:1], s[22:23], 0, v[130:131]
	s_cselect_b64 s[20:21], -1, 0
	s_cmp_lg_u32 s52, 1
	v_lshl_add_u64 v[2:3], s[22:23], 0, v[128:129]
	s_cbranch_scc1 .LBB0_1572
	s_barrier
